# k_f2 + loop-edge edits: loop-tail SALU moved above the loop-back barrier in all 12 GEMM K-loops and the MLA loop
# speedup vs baseline: 1.0057x; 1.0057x over previous
; #define PG8_STAGE(bufoff, gbase, voff) do { _Pragma("unroll") for (int _i = 0; _i < 2; ++_i) \
;         __builtin_amdgcn_global_load_lds((const unsigned*)((const char*)(gbase) + (voff)[_i]), (PG8_LAS unsigned*)(lds + (bufoff) + ldsw + _i * 8192), 16, 0, 0); } while (0)
; #define PG8_WAIT_V(n) asm volatile("s_waitcnt vmcnt(" #n ")" ::: "memory")
; #define PG8_WAIT_L(n) asm volatile("s_waitcnt lgkmcnt(" #n ")" ::: "memory")
; #define PG8_BAR __builtin_amdgcn_s_barrier()
; #define PG8_SCHED __builtin_amdgcn_sched_barrier(0)
; template <class Epi, class Sched, bool ALIGN_EPI = false, bool SP2 = false, bool F8 = false>
; __device__ __forceinline__ void gemm_phase(PG8_LAS unsigned char* lds, const Gemm g, const Sched& S, const Epi& E, const int tidb  ) {
;     ...
;             if constexpr (SP2) {
;             PG8_LDB(B0, 0, 0); PG8_LDB(B1, 0, 1); PG8_SCHED; PG8_LDA(At, 0, 0); PG8_STAGE(PG8_SA(1, 1), a1 + hstep, voffA);
;             PG8_WAIT_V(8); PG8_WAIT_L(0); PG8_BAR; PG8_MMA(0, 0, At, B0); PG8_MMA(0, 1, At, B1); PG8_BAR; PG8_SCHED;
;             PG8_LDA(At, 0, 1); PG8_STAGE(PG8_SB(0, 0), b2, voffB); PG8_STAGE(PG8_SB(0, 1), b2 + hstep, voffB); PG8_STAGE(PG8_SA(0, 0), a2, voffA);
;             PG8_WAIT_V(8); PG8_WAIT_L(0); PG8_BAR; PG8_MMA(1, 0, At, B0); PG8_MMA(1, 1, At, B1); PG8_BAR; PG8_SCHED;
.LBB0_51:
	s_add_i32 s14, s6, 2
	s_add_u32 s8, s4, 0x80
	s_addc_u32 s7, s5, 0
	s_add_i32 s15, 0, 0x10000
	s_cmp_eq_u32 s97, s6
	s_cselect_b32 s7, s73, s7
	s_cselect_b32 s6, s72, s8
	v_add_u32_e32 v0, s15, v190
	s_cselect_b32 s9, s53, s13
	s_cselect_b32 s8, s52, s12
	s_add_i32 s54, 0, 0x14000
	ds_read_b128 v[18:21], v0
	ds_read_b128 v[22:25], v0 offset:1024
	ds_read_b128 v[26:29], v0 offset:2048
	ds_read_b128 v[30:33], v0 offset:3072
	v_add_u32_e32 v0, s54, v190
	ds_read_b128 v[2:5], v0
	ds_read_b128 v[6:9], v0 offset:1024
	ds_read_b128 v[10:13], v0 offset:2048
	ds_read_b128 v[14:17], v0 offset:3072
	v_lshl_add_u64 v[184:185], s[4:5], 0, v[172:173]
	s_add_i32 m0, s43, 0xc000
	ds_read_b128 v[176:179], v191
	ds_read_b128 v[180:183], v191 offset:1024
	ds_read_b128 v[204:207], v191 offset:2048
	ds_read_b128 v[208:211], v191 offset:3072
	ds_read_b128 v[212:215], v191 offset:4096
	ds_read_b128 v[216:219], v191 offset:5120
	ds_read_b128 v[220:223], v191 offset:6144
	ds_read_b128 v[224:227], v191 offset:7168
	global_load_lds_dwordx4 v[184:185], off
	v_lshl_add_u64 v[184:185], s[4:5], 0, v[174:175]
	s_add_i32 m0, s43, 0xe000
	s_nop 0
	global_load_lds_dwordx4 v[184:185], off
	s_waitcnt vmcnt(8)
	s_waitcnt lgkmcnt(0)
	s_barrier
	s_setprio 1
	s_waitcnt lgkmcnt(0)
	v_mfma_scale_f32_16x16x128_f8f6f4 v[158:161], v[18:25], v[176:183], v[158:161], v246, v247 op_sel_hi:[0,0,0]
	v_mfma_scale_f32_16x16x128_f8f6f4 v[154:157], v[26:33], v[176:183], v[154:157], v246, v247 op_sel_hi:[0,0,0]
	v_mfma_scale_f32_16x16x128_f8f6f4 v[150:153], v[18:25], v[204:211], v[150:153], v246, v247 op_sel_hi:[0,0,0]
	v_mfma_scale_f32_16x16x128_f8f6f4 v[146:149], v[26:33], v[204:211], v[146:149], v246, v247 op_sel_hi:[0,0,0]
	v_mfma_scale_f32_16x16x128_f8f6f4 v[142:145], v[18:25], v[212:219], v[142:145], v246, v247 op_sel_hi:[0,0,0]
	v_mfma_scale_f32_16x16x128_f8f6f4 v[138:141], v[26:33], v[212:219], v[138:141], v246, v247 op_sel_hi:[0,0,0]
	v_mfma_scale_f32_16x16x128_f8f6f4 v[134:137], v[18:25], v[220:227], v[134:137], v246, v247 op_sel_hi:[0,0,0]
	v_mfma_scale_f32_16x16x128_f8f6f4 v[130:133], v[26:33], v[220:227], v[130:133], v246, v247 op_sel_hi:[0,0,0]
	s_setprio 0
	s_setprio 1
	v_mfma_scale_f32_16x16x128_f8f6f4 v[94:97], v[2:9], v[176:183], v[94:97], v246, v247 op_sel_hi:[0,0,0]
	v_mfma_scale_f32_16x16x128_f8f6f4 v[90:93], v[10:17], v[176:183], v[90:93], v246, v247 op_sel_hi:[0,0,0]
	v_mfma_scale_f32_16x16x128_f8f6f4 v[86:89], v[2:9], v[204:211], v[86:89], v246, v247 op_sel_hi:[0,0,0]
	v_mfma_scale_f32_16x16x128_f8f6f4 v[82:85], v[10:17], v[204:211], v[82:85], v246, v247 op_sel_hi:[0,0,0]
	v_mfma_scale_f32_16x16x128_f8f6f4 v[78:81], v[2:9], v[212:219], v[78:81], v246, v247 op_sel_hi:[0,0,0]
	v_mfma_scale_f32_16x16x128_f8f6f4 v[74:77], v[10:17], v[212:219], v[74:77], v246, v247 op_sel_hi:[0,0,0]
	v_mfma_scale_f32_16x16x128_f8f6f4 v[70:73], v[2:9], v[220:227], v[70:73], v246, v247 op_sel_hi:[0,0,0]
	v_mfma_scale_f32_16x16x128_f8f6f4 v[66:69], v[10:17], v[220:227], v[66:69], v246, v247 op_sel_hi:[0,0,0]
	s_setprio 0
	s_barrier
	s_add_i32 s15, s15, s41
	v_lshl_add_u64 v[176:177], s[8:9], 0, v[166:167]
	s_mov_b32 m0, s15
	ds_read_b128 v[204:207], v191 offset:16384
	ds_read_b128 v[208:211], v191 offset:17408
	ds_read_b128 v[212:215], v191 offset:18432
	ds_read_b128 v[216:219], v191 offset:19456
	ds_read_b128 v[220:223], v191 offset:20480
	ds_read_b128 v[224:227], v191 offset:21504
	ds_read_b128 v[228:231], v191 offset:22528
	ds_read_b128 v[232:235], v191 offset:23552
	global_load_lds_dwordx4 v[176:177], off
	s_add_i32 m0, s15, 0x2000
	v_lshl_add_u64 v[178:179], s[8:9], 0, v[170:171]
	s_add_u32 s8, s8, s20
	s_addc_u32 s9, s9, s21
	s_add_i32 s15, s54, s41
	global_load_lds_dwordx4 v[178:179], off
	v_lshl_add_u64 v[180:181], s[8:9], 0, v[166:167]
	s_mov_b32 m0, s15
	v_lshl_add_u64 v[182:183], s[8:9], 0, v[170:171]
	global_load_lds_dwordx4 v[180:181], off
	s_add_i32 m0, s15, 0x2000
	v_lshl_add_u64 v[184:185], s[6:7], 0, v[164:165]
	global_load_lds_dwordx4 v[182:183], off
	s_mov_b32 m0, s43
	v_lshl_add_u64 v[186:187], s[6:7], 0, v[168:169]
	global_load_lds_dwordx4 v[184:185], off
	s_mov_b32 m0, s66
	s_nop 0
	global_load_lds_dwordx4 v[186:187], off
	s_waitcnt vmcnt(8)
	s_waitcnt lgkmcnt(0)
	s_barrier
	s_setprio 1
	s_waitcnt lgkmcnt(0)
	v_mfma_scale_f32_16x16x128_f8f6f4 v[126:129], v[18:25], v[204:211], v[126:129], v246, v247 op_sel_hi:[0,0,0]
	v_mfma_scale_f32_16x16x128_f8f6f4 v[122:125], v[26:33], v[204:211], v[122:125], v246, v247 op_sel_hi:[0,0,0]
	v_mfma_scale_f32_16x16x128_f8f6f4 v[118:121], v[18:25], v[212:219], v[118:121], v246, v247 op_sel_hi:[0,0,0]
	v_mfma_scale_f32_16x16x128_f8f6f4 v[114:117], v[26:33], v[212:219], v[114:117], v246, v247 op_sel_hi:[0,0,0]
	v_mfma_scale_f32_16x16x128_f8f6f4 v[110:113], v[18:25], v[220:227], v[110:113], v246, v247 op_sel_hi:[0,0,0]
	v_mfma_scale_f32_16x16x128_f8f6f4 v[106:109], v[26:33], v[220:227], v[106:109], v246, v247 op_sel_hi:[0,0,0]
	v_mfma_scale_f32_16x16x128_f8f6f4 v[102:105], v[18:25], v[228:235], v[102:105], v246, v247 op_sel_hi:[0,0,0]
	v_mfma_scale_f32_16x16x128_f8f6f4 v[98:101], v[26:33], v[228:235], v[98:101], v246, v247 op_sel_hi:[0,0,0]
	s_setprio 0
	s_setprio 1
	v_mfma_scale_f32_16x16x128_f8f6f4 v[62:65], v[2:9], v[204:211], v[62:65], v246, v247 op_sel_hi:[0,0,0]
	v_mfma_scale_f32_16x16x128_f8f6f4 v[58:61], v[10:17], v[204:211], v[58:61], v246, v247 op_sel_hi:[0,0,0]
	v_mfma_scale_f32_16x16x128_f8f6f4 v[54:57], v[2:9], v[212:219], v[54:57], v246, v247 op_sel_hi:[0,0,0]
	v_mfma_scale_f32_16x16x128_f8f6f4 v[50:53], v[10:17], v[212:219], v[50:53], v246, v247 op_sel_hi:[0,0,0]
	v_mfma_scale_f32_16x16x128_f8f6f4 v[46:49], v[2:9], v[220:227], v[46:49], v246, v247 op_sel_hi:[0,0,0]
	v_mfma_scale_f32_16x16x128_f8f6f4 v[42:45], v[10:17], v[220:227], v[42:45], v246, v247 op_sel_hi:[0,0,0]
	v_mfma_scale_f32_16x16x128_f8f6f4 v[38:41], v[2:9], v[228:235], v[38:41], v246, v247 op_sel_hi:[0,0,0]
	v_mfma_scale_f32_16x16x128_f8f6f4 v[34:37], v[10:17], v[228:235], v[34:37], v246, v247 op_sel_hi:[0,0,0]
	s_setprio 0
	s_barrier
; #define PG8_STAGE(bufoff, gbase, voff) do { _Pragma("unroll") for (int _i = 0; _i < 2; ++_i) \
;         __builtin_amdgcn_global_load_lds((const unsigned*)((const char*)(gbase) + (voff)[_i]), (PG8_LAS unsigned*)(lds + (bufoff) + ldsw + _i * 8192), 16, 0, 0); } while (0)
; #define PG8_WAIT_V(n) asm volatile("s_waitcnt vmcnt(" #n ")" ::: "memory")
; #define PG8_WAIT_L(n) asm volatile("s_waitcnt lgkmcnt(" #n ")" ::: "memory")
; #define PG8_BAR __builtin_amdgcn_s_barrier()
; #define PG8_SCHED __builtin_amdgcn_sched_barrier(0)
; template <class Epi, class Sched, bool ALIGN_EPI = false, bool SP2 = false, bool F8 = false>
; __device__ __forceinline__ void gemm_phase(PG8_LAS unsigned char* lds, const Gemm g, const Sched& S, const Epi& E, const int tidb  ) {
;     ...
;         for (int t = 0; t < nt; t += 2) {
;             const bool last = (t == nt - 2);
;             if constexpr (Epi::PREFETCH) { if (t == 0) E.prefetch(cur, wid, lane); }
;             const char* a1 = cA + (size_t)(t + 1) * kstep;
;             const char* a2 = last ? nA : cA + (size_t)(t + 2) * kstep; const char* b2 = last ? nB : cB + (size_t)(t + 2) * kstep;
;             const char* a3 = a2 + kstep; const char* b3 = b2 + kstep;
;     ...
;             PG8_LDB(B0, 1, 0); PG8_LDB(B1, 1, 1); PG8_SCHED; PG8_LDA(At, 1, 0); PG8_STAGE(PG8_SA(0, 1), a2 + hstep, voffA);
;             PG8_WAIT_V(8); PG8_WAIT_L(0); PG8_BAR; PG8_MMA(0, 0, At, B0); PG8_MMA(0, 1, At, B1); PG8_BAR; PG8_SCHED;
;             PG8_LDA(At, 1, 1); PG8_STAGE(PG8_SB(1, 0), b3, voffB); PG8_STAGE(PG8_SB(1, 1), b3 + hstep, voffB); PG8_STAGE(PG8_SA(1, 0), a3, voffA);
;             PG8_WAIT_V(8); PG8_WAIT_L(0); PG8_BAR; PG8_MMA(1, 0, At, B0); PG8_MMA(1, 1, At, B1); PG8_BAR; PG8_SCHED;
	s_add_i32 s8, 0, 0x18000
	v_add_u32_e32 v0, s8, v190
	s_add_i32 s9, 0, 0x1c000
	ds_read_b128 v[2:5], v0
	ds_read_b128 v[6:9], v0 offset:1024
	ds_read_b128 v[10:13], v0 offset:2048
	ds_read_b128 v[14:17], v0 offset:3072
	v_add_u32_e32 v0, s9, v190
	ds_read_b128 v[18:21], v0
	ds_read_b128 v[22:25], v0 offset:1024
	ds_read_b128 v[26:29], v0 offset:2048
	ds_read_b128 v[30:33], v0 offset:3072
	s_add_u32 s6, s6, s20
	s_addc_u32 s7, s7, s21
	s_mov_b32 m0, s48
	v_lshl_add_u64 v[192:193], s[6:7], 0, v[164:165]
	ds_read_b128 v[204:207], v191 offset:32768
	ds_read_b128 v[208:211], v191 offset:33792
	ds_read_b128 v[212:215], v191 offset:34816
	ds_read_b128 v[216:219], v191 offset:35840
	ds_read_b128 v[220:223], v191 offset:36864
	ds_read_b128 v[224:227], v191 offset:37888
	ds_read_b128 v[228:231], v191 offset:38912
	ds_read_b128 v[232:235], v191 offset:39936
	global_load_lds_dwordx4 v[192:193], off
	v_lshl_add_u64 v[192:193], s[6:7], 0, v[168:169]
	s_mov_b32 m0, s90
	s_nop 0
	global_load_lds_dwordx4 v[192:193], off
	s_waitcnt vmcnt(8)
	s_waitcnt lgkmcnt(0)
	s_barrier
	s_setprio 1
	s_waitcnt lgkmcnt(0)
	v_mfma_scale_f32_16x16x128_f8f6f4 v[158:161], v[2:9], v[204:211], v[158:161], v246, v247 op_sel_hi:[0,0,0]
	v_mfma_scale_f32_16x16x128_f8f6f4 v[154:157], v[10:17], v[204:211], v[154:157], v246, v247 op_sel_hi:[0,0,0]
	v_mfma_scale_f32_16x16x128_f8f6f4 v[150:153], v[2:9], v[212:219], v[150:153], v246, v247 op_sel_hi:[0,0,0]
	v_mfma_scale_f32_16x16x128_f8f6f4 v[146:149], v[10:17], v[212:219], v[146:149], v246, v247 op_sel_hi:[0,0,0]
	v_mfma_scale_f32_16x16x128_f8f6f4 v[142:145], v[2:9], v[220:227], v[142:145], v246, v247 op_sel_hi:[0,0,0]
	v_mfma_scale_f32_16x16x128_f8f6f4 v[138:141], v[10:17], v[220:227], v[138:141], v246, v247 op_sel_hi:[0,0,0]
	v_mfma_scale_f32_16x16x128_f8f6f4 v[134:137], v[2:9], v[228:235], v[134:137], v246, v247 op_sel_hi:[0,0,0]
	v_mfma_scale_f32_16x16x128_f8f6f4 v[130:133], v[10:17], v[228:235], v[130:133], v246, v247 op_sel_hi:[0,0,0]
	s_setprio 0
	s_setprio 1
	v_mfma_scale_f32_16x16x128_f8f6f4 v[94:97], v[18:25], v[204:211], v[94:97], v246, v247 op_sel_hi:[0,0,0]
	v_mfma_scale_f32_16x16x128_f8f6f4 v[90:93], v[26:33], v[204:211], v[90:93], v246, v247 op_sel_hi:[0,0,0]
	v_mfma_scale_f32_16x16x128_f8f6f4 v[86:89], v[18:25], v[212:219], v[86:89], v246, v247 op_sel_hi:[0,0,0]
	v_mfma_scale_f32_16x16x128_f8f6f4 v[82:85], v[26:33], v[212:219], v[82:85], v246, v247 op_sel_hi:[0,0,0]
	v_mfma_scale_f32_16x16x128_f8f6f4 v[78:81], v[18:25], v[220:227], v[78:81], v246, v247 op_sel_hi:[0,0,0]
	v_mfma_scale_f32_16x16x128_f8f6f4 v[74:77], v[26:33], v[220:227], v[74:77], v246, v247 op_sel_hi:[0,0,0]
	v_mfma_scale_f32_16x16x128_f8f6f4 v[70:73], v[18:25], v[228:235], v[70:73], v246, v247 op_sel_hi:[0,0,0]
	v_mfma_scale_f32_16x16x128_f8f6f4 v[66:69], v[26:33], v[228:235], v[66:69], v246, v247 op_sel_hi:[0,0,0]
	s_setprio 0
	s_barrier
	s_add_i32 s6, s8, s41
	v_lshl_add_u64 v[176:177], v[176:177], 0, s[92:93]
	s_mov_b32 m0, s6
	ds_read_b128 v[204:207], v191 offset:49152
	ds_read_b128 v[208:211], v191 offset:50176
	ds_read_b128 v[212:215], v191 offset:51200
	ds_read_b128 v[216:219], v191 offset:52224
	ds_read_b128 v[220:223], v191 offset:53248
	ds_read_b128 v[224:227], v191 offset:54272
	ds_read_b128 v[228:231], v191 offset:55296
	ds_read_b128 v[232:235], v191 offset:56320
	global_load_lds_dwordx4 v[176:177], off
	v_lshl_add_u64 v[176:177], v[178:179], 0, s[92:93]
	s_add_i32 m0, s6, 0x2000
	s_add_i32 s6, s9, s41
	global_load_lds_dwordx4 v[176:177], off
	v_lshl_add_u64 v[176:177], v[180:181], 0, s[92:93]
	s_mov_b32 m0, s6
	s_nop 0
	global_load_lds_dwordx4 v[176:177], off
	v_lshl_add_u64 v[176:177], v[182:183], 0, s[92:93]
	s_add_i32 m0, s6, 0x2000
	s_nop 0
	global_load_lds_dwordx4 v[176:177], off
	v_lshl_add_u64 v[176:177], v[184:185], 0, s[92:93]
	s_mov_b32 m0, s91
	s_nop 0
	global_load_lds_dwordx4 v[176:177], off
	v_lshl_add_u64 v[176:177], v[186:187], 0, s[92:93]
	s_mov_b32 m0, s51
	s_nop 0
	global_load_lds_dwordx4 v[176:177], off
	s_waitcnt vmcnt(8)
	s_waitcnt lgkmcnt(0)
	s_barrier
	s_setprio 1
	s_waitcnt lgkmcnt(0)
	v_mfma_scale_f32_16x16x128_f8f6f4 v[126:129], v[2:9], v[204:211], v[126:129], v246, v247 op_sel_hi:[0,0,0]
	v_mfma_scale_f32_16x16x128_f8f6f4 v[122:125], v[10:17], v[204:211], v[122:125], v246, v247 op_sel_hi:[0,0,0]
	v_mfma_scale_f32_16x16x128_f8f6f4 v[118:121], v[2:9], v[212:219], v[118:121], v246, v247 op_sel_hi:[0,0,0]
	v_mfma_scale_f32_16x16x128_f8f6f4 v[114:117], v[10:17], v[212:219], v[114:117], v246, v247 op_sel_hi:[0,0,0]
	v_mfma_scale_f32_16x16x128_f8f6f4 v[110:113], v[2:9], v[220:227], v[110:113], v246, v247 op_sel_hi:[0,0,0]
	v_mfma_scale_f32_16x16x128_f8f6f4 v[106:109], v[10:17], v[220:227], v[106:109], v246, v247 op_sel_hi:[0,0,0]
	v_mfma_scale_f32_16x16x128_f8f6f4 v[102:105], v[2:9], v[228:235], v[102:105], v246, v247 op_sel_hi:[0,0,0]
	v_mfma_scale_f32_16x16x128_f8f6f4 v[98:101], v[10:17], v[228:235], v[98:101], v246, v247 op_sel_hi:[0,0,0]
	s_setprio 0
	s_setprio 1
	v_mfma_scale_f32_16x16x128_f8f6f4 v[62:65], v[18:25], v[204:211], v[62:65], v246, v247 op_sel_hi:[0,0,0]
	v_mfma_scale_f32_16x16x128_f8f6f4 v[58:61], v[26:33], v[204:211], v[58:61], v246, v247 op_sel_hi:[0,0,0]
	v_mfma_scale_f32_16x16x128_f8f6f4 v[54:57], v[18:25], v[212:219], v[54:57], v246, v247 op_sel_hi:[0,0,0]
	v_mfma_scale_f32_16x16x128_f8f6f4 v[50:53], v[26:33], v[212:219], v[50:53], v246, v247 op_sel_hi:[0,0,0]
	v_mfma_scale_f32_16x16x128_f8f6f4 v[46:49], v[18:25], v[220:227], v[46:49], v246, v247 op_sel_hi:[0,0,0]
	v_mfma_scale_f32_16x16x128_f8f6f4 v[42:45], v[26:33], v[220:227], v[42:45], v246, v247 op_sel_hi:[0,0,0]
	v_mfma_scale_f32_16x16x128_f8f6f4 v[38:41], v[18:25], v[228:235], v[38:41], v246, v247 op_sel_hi:[0,0,0]
	v_mfma_scale_f32_16x16x128_f8f6f4 v[34:37], v[26:33], v[228:235], v[34:37], v246, v247 op_sel_hi:[0,0,0]
	s_setprio 0
	s_add_u32 s4, s4, 0x100
	s_addc_u32 s5, s5, 0
	s_add_u32 s12, s12, 0x100
	s_addc_u32 s13, s13, 0
	s_cmp_ge_i32 s14, s84
	s_mov_b32 s6, s14
	s_barrier
	s_cbranch_scc0 .LBB0_51

; #define PG8_STAGE(bufoff, gbase, voff) do { _Pragma("unroll") for (int _i = 0; _i < 2; ++_i) \
;         __builtin_amdgcn_global_load_lds((const unsigned*)((const char*)(gbase) + (voff)[_i]), (PG8_LAS unsigned*)(lds + (bufoff) + ldsw + _i * 8192), 16, 0, 0); } while (0)
; #define PG8_WAIT_V(n) asm volatile("s_waitcnt vmcnt(" #n ")" ::: "memory")
; #define PG8_WAIT_L(n) asm volatile("s_waitcnt lgkmcnt(" #n ")" ::: "memory")
; #define PG8_BAR __builtin_amdgcn_s_barrier()
; #define PG8_SCHED __builtin_amdgcn_sched_barrier(0)
; template <class Epi, class Sched, bool ALIGN_EPI = false, bool SP2 = false, bool F8 = false>
; __device__ __forceinline__ void gemm_phase(PG8_LAS unsigned char* lds, const Gemm g, const Sched& S, const Epi& E, const int tidb  ) {
;     ...
;             if constexpr (SP2) {
;             PG8_LDB(B0, 0, 0); PG8_LDB(B1, 0, 1); PG8_SCHED; PG8_LDA(At, 0, 0); PG8_STAGE(PG8_SA(1, 1), a1 + hstep, voffA);
;             PG8_WAIT_V(8); PG8_WAIT_L(0); PG8_BAR; PG8_MMA(0, 0, At, B0); PG8_MMA(0, 1, At, B1); PG8_BAR; PG8_SCHED;
;             PG8_LDA(At, 0, 1); PG8_STAGE(PG8_SB(0, 0), b2, voffB); PG8_STAGE(PG8_SB(0, 1), b2 + hstep, voffB); PG8_STAGE(PG8_SA(0, 0), a2, voffA);
;             PG8_WAIT_V(8); PG8_WAIT_L(0); PG8_BAR; PG8_MMA(1, 0, At, B0); PG8_MMA(1, 1, At, B1); PG8_BAR; PG8_SCHED;
.LBB0_393:
	s_add_i32 s63, s28, 2
	s_add_u32 s65, s4, 0x80
	s_addc_u32 s29, s5, 0
	s_add_i32 s68, 0, 0x10000
	s_cmp_eq_u32 s55, s28
	s_cselect_b32 s29, s25, s29
	s_cselect_b32 s28, s24, s65
	v_add_u32_e32 v0, s68, v152
	s_cselect_b32 s67, s27, s31
	s_cselect_b32 s66, s26, s30
	s_add_i32 s65, 0, 0x14000
	ds_read_b128 v[158:161], v0
	s_waitcnt vmcnt(0)
	ds_read_b128 v[164:167], v0 offset:1024
	ds_read_b128 v[168:171], v0 offset:2048
	ds_read_b128 v[172:175], v0 offset:3072
	v_add_u32_e32 v0, s65, v152
	ds_read_b128 v[176:179], v0
	ds_read_b128 v[180:183], v0 offset:1024
	ds_read_b128 v[184:187], v0 offset:2048
	ds_read_b128 v[188:191], v0 offset:3072
	v_lshl_add_u64 v[148:149], s[4:5], 0, v[144:145]
	s_add_i32 m0, s46, 0xc000
	ds_read_b128 v[192:195], v156
	ds_read_b128 v[204:207], v156 offset:1024
	ds_read_b128 v[208:211], v156 offset:2048
	ds_read_b128 v[212:215], v156 offset:3072
	ds_read_b128 v[216:219], v156 offset:4096
	ds_read_b128 v[220:223], v156 offset:5120
	ds_read_b128 v[224:227], v156 offset:6144
	ds_read_b128 v[228:231], v156 offset:7168
	global_load_lds_dwordx4 v[148:149], off
	v_lshl_add_u64 v[148:149], s[4:5], 0, v[146:147]
	s_add_i32 m0, s46, 0xe000
	s_nop 0
	global_load_lds_dwordx4 v[148:149], off
	s_waitcnt vmcnt(8)
	s_waitcnt lgkmcnt(0)
	s_barrier
	s_setprio 1
	s_waitcnt lgkmcnt(0)
	v_mfma_f32_16x16x32_bf16 v[122:125], v[158:161], v[192:195], v[122:125]
	v_mfma_f32_16x16x32_bf16 v[126:129], v[168:171], v[192:195], v[126:129]
	v_mfma_f32_16x16x32_bf16 v[118:121], v[158:161], v[208:211], v[118:121]
	v_mfma_f32_16x16x32_bf16 v[114:117], v[168:171], v[208:211], v[114:117]
	v_mfma_f32_16x16x32_bf16 v[110:113], v[158:161], v[216:219], v[110:113]
	v_mfma_f32_16x16x32_bf16 v[106:109], v[168:171], v[216:219], v[106:109]
	v_mfma_f32_16x16x32_bf16 v[102:105], v[158:161], v[224:227], v[102:105]
	v_mfma_f32_16x16x32_bf16 v[98:101], v[168:171], v[224:227], v[98:101]
	v_mfma_f32_16x16x32_bf16 v[122:125], v[164:167], v[204:207], v[122:125]
	v_mfma_f32_16x16x32_bf16 v[126:129], v[172:175], v[204:207], v[126:129]
	v_mfma_f32_16x16x32_bf16 v[118:121], v[164:167], v[212:215], v[118:121]
	v_mfma_f32_16x16x32_bf16 v[114:117], v[172:175], v[212:215], v[114:117]
	v_mfma_f32_16x16x32_bf16 v[110:113], v[164:167], v[220:223], v[110:113]
	v_mfma_f32_16x16x32_bf16 v[106:109], v[172:175], v[220:223], v[106:109]
	v_mfma_f32_16x16x32_bf16 v[102:105], v[164:167], v[228:231], v[102:105]
	v_mfma_f32_16x16x32_bf16 v[98:101], v[172:175], v[228:231], v[98:101]
	s_setprio 0
	s_setprio 1
	v_mfma_f32_16x16x32_bf16 v[62:65], v[176:179], v[192:195], v[62:65]
	v_mfma_f32_16x16x32_bf16 v[58:61], v[184:187], v[192:195], v[58:61]
	v_mfma_f32_16x16x32_bf16 v[54:57], v[176:179], v[208:211], v[54:57]
	v_mfma_f32_16x16x32_bf16 v[50:53], v[184:187], v[208:211], v[50:53]
	v_mfma_f32_16x16x32_bf16 v[46:49], v[176:179], v[216:219], v[46:49]
	v_mfma_f32_16x16x32_bf16 v[42:45], v[184:187], v[216:219], v[42:45]
	v_mfma_f32_16x16x32_bf16 v[38:41], v[176:179], v[224:227], v[38:41]
	v_mfma_f32_16x16x32_bf16 v[34:37], v[184:187], v[224:227], v[34:37]
	v_mfma_f32_16x16x32_bf16 v[62:65], v[180:183], v[204:207], v[62:65]
	v_mfma_f32_16x16x32_bf16 v[58:61], v[188:191], v[204:207], v[58:61]
	v_mfma_f32_16x16x32_bf16 v[54:57], v[180:183], v[212:215], v[54:57]
	v_mfma_f32_16x16x32_bf16 v[50:53], v[188:191], v[212:215], v[50:53]
	v_mfma_f32_16x16x32_bf16 v[46:49], v[180:183], v[220:223], v[46:49]
	v_mfma_f32_16x16x32_bf16 v[42:45], v[188:191], v[220:223], v[42:45]
	v_mfma_f32_16x16x32_bf16 v[38:41], v[180:183], v[228:231], v[38:41]
	v_mfma_f32_16x16x32_bf16 v[34:37], v[188:191], v[228:231], v[34:37]
	s_setprio 0
	s_barrier
	s_add_i32 s68, s68, s45
	v_lshl_add_u64 v[148:149], s[66:67], 0, v[132:133]
	s_mov_b32 m0, s68
	ds_read_b128 v[192:195], v156 offset:16384
	ds_read_b128 v[204:207], v156 offset:17408
	ds_read_b128 v[208:211], v156 offset:18432
	ds_read_b128 v[212:215], v156 offset:19456
	ds_read_b128 v[216:219], v156 offset:20480
	ds_read_b128 v[220:223], v156 offset:21504
	ds_read_b128 v[224:227], v156 offset:22528
	ds_read_b128 v[228:231], v156 offset:23552
	global_load_lds_dwordx4 v[148:149], off
	s_add_i32 m0, s68, 0x2000
	v_lshl_add_u64 v[196:197], s[66:67], 0, v[136:137]
	s_add_u32 s66, s66, s10
	s_addc_u32 s67, s67, s11
	s_add_i32 s65, s65, s45
	global_load_lds_dwordx4 v[196:197], off
	v_lshl_add_u64 v[200:201], s[66:67], 0, v[132:133]
	s_mov_b32 m0, s65
	v_lshl_add_u64 v[232:233], s[66:67], 0, v[136:137]
	global_load_lds_dwordx4 v[200:201], off
	s_add_i32 m0, s65, 0x2000
	v_lshl_add_u64 v[234:235], s[28:29], 0, v[130:131]
	global_load_lds_dwordx4 v[232:233], off
	s_mov_b32 m0, s46
	v_lshl_add_u64 v[236:237], s[28:29], 0, v[134:135]
	global_load_lds_dwordx4 v[234:235], off
	s_mov_b32 m0, s47
	s_nop 0
	global_load_lds_dwordx4 v[236:237], off
	s_waitcnt vmcnt(8)
	s_waitcnt lgkmcnt(0)
	s_barrier
; #define PG8_STAGE(bufoff, gbase, voff) do { _Pragma("unroll") for (int _i = 0; _i < 2; ++_i) \
;         __builtin_amdgcn_global_load_lds((const unsigned*)((const char*)(gbase) + (voff)[_i]), (PG8_LAS unsigned*)(lds + (bufoff) + ldsw + _i * 8192), 16, 0, 0); } while (0)
; #define PG8_WAIT_V(n) asm volatile("s_waitcnt vmcnt(" #n ")" ::: "memory")
; #define PG8_WAIT_L(n) asm volatile("s_waitcnt lgkmcnt(" #n ")" ::: "memory")
; #define PG8_BAR __builtin_amdgcn_s_barrier()
; #define PG8_SCHED __builtin_amdgcn_sched_barrier(0)
; template <class Epi, class Sched, bool ALIGN_EPI = false, bool SP2 = false, bool F8 = false>
; __device__ __forceinline__ void gemm_phase(PG8_LAS unsigned char* lds, const Gemm g, const Sched& S, const Epi& E, const int tidb  ) {
;     ...
;             PG8_WAIT_V(8); PG8_WAIT_L(0); PG8_BAR; PG8_MMA(1, 0, At, B0); PG8_MMA(1, 1, At, B1); PG8_BAR; PG8_SCHED;
;             PG8_LDB(B0, 1, 0); PG8_LDB(B1, 1, 1); PG8_SCHED; PG8_LDA(At, 1, 0); PG8_STAGE(PG8_SA(0, 1), a2 + hstep, voffA);
;             PG8_WAIT_V(8); PG8_WAIT_L(0); PG8_BAR; PG8_MMA(0, 0, At, B0); PG8_MMA(0, 1, At, B1); PG8_BAR; PG8_SCHED;
	s_setprio 1
	s_waitcnt lgkmcnt(0)
	v_mfma_f32_16x16x32_bf16 v[94:97], v[158:161], v[192:195], v[94:97]
	v_mfma_f32_16x16x32_bf16 v[90:93], v[168:171], v[192:195], v[90:93]
	v_mfma_f32_16x16x32_bf16 v[86:89], v[158:161], v[208:211], v[86:89]
	v_mfma_f32_16x16x32_bf16 v[82:85], v[168:171], v[208:211], v[82:85]
	v_mfma_f32_16x16x32_bf16 v[78:81], v[158:161], v[216:219], v[78:81]
	v_mfma_f32_16x16x32_bf16 v[74:77], v[168:171], v[216:219], v[74:77]
	v_mfma_f32_16x16x32_bf16 v[70:73], v[158:161], v[224:227], v[70:73]
	v_mfma_f32_16x16x32_bf16 v[66:69], v[168:171], v[224:227], v[66:69]
	v_mfma_f32_16x16x32_bf16 v[94:97], v[164:167], v[204:207], v[94:97]
	v_mfma_f32_16x16x32_bf16 v[90:93], v[172:175], v[204:207], v[90:93]
	v_mfma_f32_16x16x32_bf16 v[86:89], v[164:167], v[212:215], v[86:89]
	v_mfma_f32_16x16x32_bf16 v[82:85], v[172:175], v[212:215], v[82:85]
	v_mfma_f32_16x16x32_bf16 v[78:81], v[164:167], v[220:223], v[78:81]
	v_mfma_f32_16x16x32_bf16 v[74:77], v[172:175], v[220:223], v[74:77]
	v_mfma_f32_16x16x32_bf16 v[70:73], v[164:167], v[228:231], v[70:73]
	v_mfma_f32_16x16x32_bf16 v[66:69], v[172:175], v[228:231], v[66:69]
	s_setprio 0
	s_setprio 1
	v_mfma_f32_16x16x32_bf16 v[30:33], v[176:179], v[192:195], v[30:33]
	v_mfma_f32_16x16x32_bf16 v[26:29], v[184:187], v[192:195], v[26:29]
	v_mfma_f32_16x16x32_bf16 v[22:25], v[176:179], v[208:211], v[22:25]
	v_mfma_f32_16x16x32_bf16 v[18:21], v[184:187], v[208:211], v[18:21]
	v_mfma_f32_16x16x32_bf16 v[14:17], v[176:179], v[216:219], v[14:17]
	v_mfma_f32_16x16x32_bf16 v[10:13], v[184:187], v[216:219], v[10:13]
	v_mfma_f32_16x16x32_bf16 v[6:9], v[176:179], v[224:227], v[6:9]
	v_mfma_f32_16x16x32_bf16 v[2:5], v[184:187], v[224:227], v[2:5]
	v_mfma_f32_16x16x32_bf16 v[30:33], v[180:183], v[204:207], v[30:33]
	v_mfma_f32_16x16x32_bf16 v[26:29], v[188:191], v[204:207], v[26:29]
	v_mfma_f32_16x16x32_bf16 v[22:25], v[180:183], v[212:215], v[22:25]
	v_mfma_f32_16x16x32_bf16 v[18:21], v[188:191], v[212:215], v[18:21]
	v_mfma_f32_16x16x32_bf16 v[14:17], v[180:183], v[220:223], v[14:17]
	v_mfma_f32_16x16x32_bf16 v[10:13], v[188:191], v[220:223], v[10:13]
	v_mfma_f32_16x16x32_bf16 v[6:9], v[180:183], v[228:231], v[6:9]
	v_mfma_f32_16x16x32_bf16 v[2:5], v[188:191], v[228:231], v[2:5]
	s_setprio 0
	s_barrier
	s_add_i32 s65, 0, 0x18000
	v_add_u32_e32 v0, s65, v152
	s_add_i32 s66, 0, 0x1c000
	ds_read_b128 v[158:161], v0
	ds_read_b128 v[164:167], v0 offset:1024
	ds_read_b128 v[168:171], v0 offset:2048
	ds_read_b128 v[172:175], v0 offset:3072
	v_add_u32_e32 v0, s66, v152
	ds_read_b128 v[176:179], v0
	ds_read_b128 v[180:183], v0 offset:1024
	ds_read_b128 v[184:187], v0 offset:2048
	ds_read_b128 v[188:191], v0 offset:3072
	s_add_u32 s28, s28, s10
	s_addc_u32 s29, s29, s11
	s_mov_b32 m0, s48
	v_lshl_add_u64 v[238:239], s[28:29], 0, v[130:131]
	ds_read_b128 v[192:195], v156 offset:32768
	ds_read_b128 v[204:207], v156 offset:33792
	ds_read_b128 v[208:211], v156 offset:34816
	ds_read_b128 v[212:215], v156 offset:35840
	ds_read_b128 v[216:219], v156 offset:36864
	ds_read_b128 v[220:223], v156 offset:37888
	ds_read_b128 v[224:227], v156 offset:38912
	ds_read_b128 v[228:231], v156 offset:39936
	global_load_lds_dwordx4 v[238:239], off
	v_lshl_add_u64 v[238:239], s[28:29], 0, v[134:135]
	s_mov_b32 m0, s49
	s_nop 0
	global_load_lds_dwordx4 v[238:239], off
	s_waitcnt vmcnt(8)
	s_waitcnt lgkmcnt(0)
	s_barrier
	s_setprio 1
	s_waitcnt lgkmcnt(0)
	v_mfma_f32_16x16x32_bf16 v[122:125], v[158:161], v[192:195], v[122:125]
	v_mfma_f32_16x16x32_bf16 v[126:129], v[168:171], v[192:195], v[126:129]
	v_mfma_f32_16x16x32_bf16 v[118:121], v[158:161], v[208:211], v[118:121]
	v_mfma_f32_16x16x32_bf16 v[114:117], v[168:171], v[208:211], v[114:117]
	v_mfma_f32_16x16x32_bf16 v[110:113], v[158:161], v[216:219], v[110:113]
	v_mfma_f32_16x16x32_bf16 v[106:109], v[168:171], v[216:219], v[106:109]
	v_mfma_f32_16x16x32_bf16 v[102:105], v[158:161], v[224:227], v[102:105]
	v_mfma_f32_16x16x32_bf16 v[98:101], v[168:171], v[224:227], v[98:101]
	v_mfma_f32_16x16x32_bf16 v[122:125], v[164:167], v[204:207], v[122:125]
	v_mfma_f32_16x16x32_bf16 v[126:129], v[172:175], v[204:207], v[126:129]
	v_mfma_f32_16x16x32_bf16 v[118:121], v[164:167], v[212:215], v[118:121]
	v_mfma_f32_16x16x32_bf16 v[114:117], v[172:175], v[212:215], v[114:117]
	v_mfma_f32_16x16x32_bf16 v[110:113], v[164:167], v[220:223], v[110:113]
	v_mfma_f32_16x16x32_bf16 v[106:109], v[172:175], v[220:223], v[106:109]
	v_mfma_f32_16x16x32_bf16 v[102:105], v[164:167], v[228:231], v[102:105]
	v_mfma_f32_16x16x32_bf16 v[98:101], v[172:175], v[228:231], v[98:101]
	s_setprio 0
	s_setprio 1
	v_mfma_f32_16x16x32_bf16 v[62:65], v[176:179], v[192:195], v[62:65]
	v_mfma_f32_16x16x32_bf16 v[58:61], v[184:187], v[192:195], v[58:61]
	v_mfma_f32_16x16x32_bf16 v[54:57], v[176:179], v[208:211], v[54:57]
	v_mfma_f32_16x16x32_bf16 v[50:53], v[184:187], v[208:211], v[50:53]
	v_mfma_f32_16x16x32_bf16 v[46:49], v[176:179], v[216:219], v[46:49]
	v_mfma_f32_16x16x32_bf16 v[42:45], v[184:187], v[216:219], v[42:45]
	v_mfma_f32_16x16x32_bf16 v[38:41], v[176:179], v[224:227], v[38:41]
	v_mfma_f32_16x16x32_bf16 v[34:37], v[184:187], v[224:227], v[34:37]
	v_mfma_f32_16x16x32_bf16 v[62:65], v[180:183], v[204:207], v[62:65]
	v_mfma_f32_16x16x32_bf16 v[58:61], v[188:191], v[204:207], v[58:61]
	v_mfma_f32_16x16x32_bf16 v[54:57], v[180:183], v[212:215], v[54:57]
	v_mfma_f32_16x16x32_bf16 v[50:53], v[188:191], v[212:215], v[50:53]
	v_mfma_f32_16x16x32_bf16 v[46:49], v[180:183], v[220:223], v[46:49]
	v_mfma_f32_16x16x32_bf16 v[42:45], v[188:191], v[220:223], v[42:45]
	v_mfma_f32_16x16x32_bf16 v[38:41], v[180:183], v[228:231], v[38:41]
	v_mfma_f32_16x16x32_bf16 v[34:37], v[188:191], v[228:231], v[34:37]
	s_setprio 0
	s_barrier
; #define PG8_STAGE(bufoff, gbase, voff) do { _Pragma("unroll") for (int _i = 0; _i < 2; ++_i) \
;         __builtin_amdgcn_global_load_lds((const unsigned*)((const char*)(gbase) + (voff)[_i]), (PG8_LAS unsigned*)(lds + (bufoff) + ldsw + _i * 8192), 16, 0, 0); } while (0)
; #define PG8_WAIT_V(n) asm volatile("s_waitcnt vmcnt(" #n ")" ::: "memory")
; #define PG8_WAIT_L(n) asm volatile("s_waitcnt lgkmcnt(" #n ")" ::: "memory")
; #define PG8_BAR __builtin_amdgcn_s_barrier()
; #define PG8_SCHED __builtin_amdgcn_sched_barrier(0)
; template <class Epi, class Sched, bool ALIGN_EPI = false, bool SP2 = false, bool F8 = false>
; __device__ __forceinline__ void gemm_phase(PG8_LAS unsigned char* lds, const Gemm g, const Sched& S, const Epi& E, const int tidb  ) {
;     ...
;         for (int t = 0; t < nt; t += 2) {
;             const bool last = (t == nt - 2);
;             if constexpr (Epi::PREFETCH) { if (t == 0) E.prefetch(cur, wid, lane); }
;             const char* a1 = cA + (size_t)(t + 1) * kstep;
;             const char* a2 = last ? nA : cA + (size_t)(t + 2) * kstep; const char* b2 = last ? nB : cB + (size_t)(t + 2) * kstep;
;             const char* a3 = a2 + kstep; const char* b3 = b2 + kstep;
;     ...
;             PG8_LDA(At, 1, 1); PG8_STAGE(PG8_SB(1, 0), b3, voffB); PG8_STAGE(PG8_SB(1, 1), b3 + hstep, voffB); PG8_STAGE(PG8_SA(1, 0), a3, voffA);
;             PG8_WAIT_V(8); PG8_WAIT_L(0); PG8_BAR; PG8_MMA(1, 0, At, B0); PG8_MMA(1, 1, At, B1); PG8_BAR; PG8_SCHED;
	s_add_i32 s28, s65, s45
	v_lshl_add_u64 v[148:149], v[148:149], 0, s[92:93]
	s_mov_b32 m0, s28
	ds_read_b128 v[192:195], v156 offset:49152
	ds_read_b128 v[204:207], v156 offset:50176
	ds_read_b128 v[208:211], v156 offset:51200
	ds_read_b128 v[212:215], v156 offset:52224
	ds_read_b128 v[216:219], v156 offset:53248
	ds_read_b128 v[220:223], v156 offset:54272
	ds_read_b128 v[224:227], v156 offset:55296
	ds_read_b128 v[228:231], v156 offset:56320
	global_load_lds_dwordx4 v[148:149], off
	v_lshl_add_u64 v[148:149], v[196:197], 0, s[92:93]
	s_add_i32 m0, s28, 0x2000
	s_add_i32 s28, s66, s45
	global_load_lds_dwordx4 v[148:149], off
	v_lshl_add_u64 v[148:149], v[200:201], 0, s[92:93]
	s_mov_b32 m0, s28
	s_nop 0
	global_load_lds_dwordx4 v[148:149], off
	v_lshl_add_u64 v[148:149], v[232:233], 0, s[92:93]
	s_add_i32 m0, s28, 0x2000
	s_nop 0
	global_load_lds_dwordx4 v[148:149], off
	v_lshl_add_u64 v[148:149], v[234:235], 0, s[92:93]
	s_mov_b32 m0, s50
	s_nop 0
	global_load_lds_dwordx4 v[148:149], off
	v_lshl_add_u64 v[148:149], v[236:237], 0, s[92:93]
	s_mov_b32 m0, s51
	s_nop 0
	global_load_lds_dwordx4 v[148:149], off
	s_waitcnt vmcnt(8)
	s_waitcnt lgkmcnt(0)
	s_barrier
	s_setprio 1
	s_waitcnt lgkmcnt(0)
	v_mfma_f32_16x16x32_bf16 v[94:97], v[158:161], v[192:195], v[94:97]
	v_mfma_f32_16x16x32_bf16 v[90:93], v[168:171], v[192:195], v[90:93]
	v_mfma_f32_16x16x32_bf16 v[86:89], v[158:161], v[208:211], v[86:89]
	v_mfma_f32_16x16x32_bf16 v[82:85], v[168:171], v[208:211], v[82:85]
	v_mfma_f32_16x16x32_bf16 v[78:81], v[158:161], v[216:219], v[78:81]
	v_mfma_f32_16x16x32_bf16 v[74:77], v[168:171], v[216:219], v[74:77]
	v_mfma_f32_16x16x32_bf16 v[70:73], v[158:161], v[224:227], v[70:73]
	v_mfma_f32_16x16x32_bf16 v[66:69], v[168:171], v[224:227], v[66:69]
	v_mfma_f32_16x16x32_bf16 v[94:97], v[164:167], v[204:207], v[94:97]
	v_mfma_f32_16x16x32_bf16 v[90:93], v[172:175], v[204:207], v[90:93]
	v_mfma_f32_16x16x32_bf16 v[86:89], v[164:167], v[212:215], v[86:89]
	v_mfma_f32_16x16x32_bf16 v[82:85], v[172:175], v[212:215], v[82:85]
	v_mfma_f32_16x16x32_bf16 v[78:81], v[164:167], v[220:223], v[78:81]
	v_mfma_f32_16x16x32_bf16 v[74:77], v[172:175], v[220:223], v[74:77]
	v_mfma_f32_16x16x32_bf16 v[70:73], v[164:167], v[228:231], v[70:73]
	v_mfma_f32_16x16x32_bf16 v[66:69], v[172:175], v[228:231], v[66:69]
	s_setprio 0
	s_setprio 1
	v_mfma_f32_16x16x32_bf16 v[30:33], v[176:179], v[192:195], v[30:33]
	v_mfma_f32_16x16x32_bf16 v[26:29], v[184:187], v[192:195], v[26:29]
	v_mfma_f32_16x16x32_bf16 v[22:25], v[176:179], v[208:211], v[22:25]
	v_mfma_f32_16x16x32_bf16 v[18:21], v[184:187], v[208:211], v[18:21]
	v_mfma_f32_16x16x32_bf16 v[14:17], v[176:179], v[216:219], v[14:17]
	v_mfma_f32_16x16x32_bf16 v[10:13], v[184:187], v[216:219], v[10:13]
	v_mfma_f32_16x16x32_bf16 v[6:9], v[176:179], v[224:227], v[6:9]
	v_mfma_f32_16x16x32_bf16 v[2:5], v[184:187], v[224:227], v[2:5]
	v_mfma_f32_16x16x32_bf16 v[30:33], v[180:183], v[204:207], v[30:33]
	v_mfma_f32_16x16x32_bf16 v[26:29], v[188:191], v[204:207], v[26:29]
	v_mfma_f32_16x16x32_bf16 v[22:25], v[180:183], v[212:215], v[22:25]
	v_mfma_f32_16x16x32_bf16 v[18:21], v[188:191], v[212:215], v[18:21]
	v_mfma_f32_16x16x32_bf16 v[14:17], v[180:183], v[220:223], v[14:17]
	v_mfma_f32_16x16x32_bf16 v[10:13], v[188:191], v[220:223], v[10:13]
	v_mfma_f32_16x16x32_bf16 v[6:9], v[180:183], v[228:231], v[6:9]
	v_mfma_f32_16x16x32_bf16 v[2:5], v[188:191], v[228:231], v[2:5]
	s_setprio 0
	s_add_u32 s4, s4, 0x100
	s_addc_u32 s5, s5, 0
	s_add_u32 s30, s30, 0x100
	s_addc_u32 s31, s31, 0
	s_cmp_ge_i32 s63, s52
	s_mov_b32 s28, s63
	s_barrier
	s_cbranch_scc0 .LBB0_393
	s_movk_i32 s67, 0x300

; #define PG8_STAGE(bufoff, gbase, voff) do { _Pragma("unroll") for (int _i = 0; _i < 2; ++_i) \
;         __builtin_amdgcn_global_load_lds((const unsigned*)((const char*)(gbase) + (voff)[_i]), (PG8_LAS unsigned*)(lds + (bufoff) + ldsw + _i * 8192), 16, 0, 0); } while (0)
; #define PG8_WAIT_V(n) asm volatile("s_waitcnt vmcnt(" #n ")" ::: "memory")
; #define PG8_WAIT_L(n) asm volatile("s_waitcnt lgkmcnt(" #n ")" ::: "memory")
; #define PG8_BAR __builtin_amdgcn_s_barrier()
; #define PG8_SCHED __builtin_amdgcn_sched_barrier(0)
; template <class Epi, class Sched, bool ALIGN_EPI = false, bool SP2 = false, bool F8 = false>
; __device__ __forceinline__ void gemm_phase(PG8_LAS unsigned char* lds, const Gemm g, const Sched& S, const Epi& E, const int tidb  ) {
;     ...
;             if constexpr (SP2) {
;             PG8_LDB(B0, 0, 0); PG8_LDB(B1, 0, 1); PG8_SCHED; PG8_LDA(At, 0, 0); PG8_STAGE(PG8_SA(1, 1), a1 + hstep, voffA);
;             PG8_WAIT_V(8); PG8_WAIT_L(0); PG8_BAR; PG8_MMA(0, 0, At, B0); PG8_MMA(0, 1, At, B1); PG8_BAR; PG8_SCHED;
;             PG8_LDA(At, 0, 1); PG8_STAGE(PG8_SB(0, 0), b2, voffB); PG8_STAGE(PG8_SB(0, 1), b2 + hstep, voffB); PG8_STAGE(PG8_SA(0, 0), a2, voffA);
;             PG8_WAIT_V(8); PG8_WAIT_L(0); PG8_BAR; PG8_MMA(1, 0, At, B0); PG8_MMA(1, 1, At, B1); PG8_BAR; PG8_SCHED;
.LBB0_465:
	s_add_i32 s61, s6, 2
	s_add_u32 s62, s4, 0x80
	s_addc_u32 s7, s5, 0
	s_add_i32 s65, 0, 0x10000
	s_cmp_eq_u32 s54, s6
	s_cselect_b32 s7, s25, s7
	s_cselect_b32 s6, s24, s62
	v_add_u32_e32 v0, s65, v159
	s_cselect_b32 s63, s27, s29
	s_cselect_b32 s62, s26, s28
	s_add_i32 s66, 0, 0x14000
	ds_read_b128 v[142:145], v0
	ds_read_b128 v[146:149], v0 offset:1024
	ds_read_b128 v[154:157], v0 offset:2048
	s_waitcnt vmcnt(0)
	ds_read_b128 v[164:167], v0 offset:3072
	v_add_u32_e32 v0, s66, v159
	ds_read_b128 v[168:171], v0
	ds_read_b128 v[172:175], v0 offset:1024
	ds_read_b128 v[176:179], v0 offset:2048
	ds_read_b128 v[180:183], v0 offset:3072
	v_lshl_add_u64 v[150:151], s[4:5], 0, v[138:139]
	s_add_i32 m0, s45, 0xc000
	ds_read_b128 v[184:187], v160
	ds_read_b128 v[188:191], v160 offset:1024
	ds_read_b128 v[192:195], v160 offset:2048
	ds_read_b128 v[204:207], v160 offset:3072
	ds_read_b128 v[208:211], v160 offset:4096
	ds_read_b128 v[212:215], v160 offset:5120
	ds_read_b128 v[216:219], v160 offset:6144
	ds_read_b128 v[220:223], v160 offset:7168
	global_load_lds_dwordx4 v[150:151], off
	v_lshl_add_u64 v[150:151], s[4:5], 0, v[140:141]
	s_add_i32 m0, s45, 0xe000
	s_nop 0
	global_load_lds_dwordx4 v[150:151], off
	s_waitcnt vmcnt(8)
	s_waitcnt lgkmcnt(0)
	s_barrier
	s_setprio 1
	s_waitcnt lgkmcnt(0)
	v_mfma_f32_16x16x32_bf16 v[126:129], v[142:145], v[184:187], v[126:129]
	v_mfma_f32_16x16x32_bf16 v[122:125], v[154:157], v[184:187], v[122:125]
	v_mfma_f32_16x16x32_bf16 v[118:121], v[142:145], v[192:195], v[118:121]
	v_mfma_f32_16x16x32_bf16 v[114:117], v[154:157], v[192:195], v[114:117]
	v_mfma_f32_16x16x32_bf16 v[110:113], v[142:145], v[208:211], v[110:113]
	v_mfma_f32_16x16x32_bf16 v[106:109], v[154:157], v[208:211], v[106:109]
	v_mfma_f32_16x16x32_bf16 v[102:105], v[142:145], v[216:219], v[102:105]
	v_mfma_f32_16x16x32_bf16 v[98:101], v[154:157], v[216:219], v[98:101]
	v_mfma_f32_16x16x32_bf16 v[126:129], v[146:149], v[188:191], v[126:129]
	v_mfma_f32_16x16x32_bf16 v[122:125], v[164:167], v[188:191], v[122:125]
	v_mfma_f32_16x16x32_bf16 v[118:121], v[146:149], v[204:207], v[118:121]
	v_mfma_f32_16x16x32_bf16 v[114:117], v[164:167], v[204:207], v[114:117]
	v_mfma_f32_16x16x32_bf16 v[110:113], v[146:149], v[212:215], v[110:113]
	v_mfma_f32_16x16x32_bf16 v[106:109], v[164:167], v[212:215], v[106:109]
	v_mfma_f32_16x16x32_bf16 v[102:105], v[146:149], v[220:223], v[102:105]
	v_mfma_f32_16x16x32_bf16 v[98:101], v[164:167], v[220:223], v[98:101]
	s_setprio 0
	s_setprio 1
	v_mfma_f32_16x16x32_bf16 v[62:65], v[168:171], v[184:187], v[62:65]
	v_mfma_f32_16x16x32_bf16 v[58:61], v[176:179], v[184:187], v[58:61]
	v_mfma_f32_16x16x32_bf16 v[54:57], v[168:171], v[192:195], v[54:57]
	v_mfma_f32_16x16x32_bf16 v[50:53], v[176:179], v[192:195], v[50:53]
	v_mfma_f32_16x16x32_bf16 v[46:49], v[168:171], v[208:211], v[46:49]
	v_mfma_f32_16x16x32_bf16 v[42:45], v[176:179], v[208:211], v[42:45]
	v_mfma_f32_16x16x32_bf16 v[38:41], v[168:171], v[216:219], v[38:41]
	v_mfma_f32_16x16x32_bf16 v[34:37], v[176:179], v[216:219], v[34:37]
	v_mfma_f32_16x16x32_bf16 v[62:65], v[172:175], v[188:191], v[62:65]
	v_mfma_f32_16x16x32_bf16 v[58:61], v[180:183], v[188:191], v[58:61]
	v_mfma_f32_16x16x32_bf16 v[54:57], v[172:175], v[204:207], v[54:57]
	v_mfma_f32_16x16x32_bf16 v[50:53], v[180:183], v[204:207], v[50:53]
	v_mfma_f32_16x16x32_bf16 v[46:49], v[172:175], v[212:215], v[46:49]
	v_mfma_f32_16x16x32_bf16 v[42:45], v[180:183], v[212:215], v[42:45]
	v_mfma_f32_16x16x32_bf16 v[38:41], v[172:175], v[220:223], v[38:41]
	v_mfma_f32_16x16x32_bf16 v[34:37], v[180:183], v[220:223], v[34:37]
	s_setprio 0
	s_barrier
	s_add_i32 s65, s65, s43
	v_lshl_add_u64 v[150:151], s[62:63], 0, v[132:133]
	s_mov_b32 m0, s65
	ds_read_b128 v[184:187], v160 offset:16384
	ds_read_b128 v[188:191], v160 offset:17408
	ds_read_b128 v[192:195], v160 offset:18432
	ds_read_b128 v[204:207], v160 offset:19456
	ds_read_b128 v[208:211], v160 offset:20480
	ds_read_b128 v[212:215], v160 offset:21504
	ds_read_b128 v[216:219], v160 offset:22528
	ds_read_b128 v[220:223], v160 offset:23552
	global_load_lds_dwordx4 v[150:151], off
	s_add_i32 m0, s65, 0x2000
	v_lshl_add_u64 v[196:197], s[62:63], 0, v[136:137]
	s_add_u32 s62, s62, s8
	s_addc_u32 s63, s63, s9
	s_add_i32 s65, s66, s43
	global_load_lds_dwordx4 v[196:197], off
	v_lshl_add_u64 v[200:201], s[62:63], 0, v[132:133]
	s_mov_b32 m0, s65
	v_lshl_add_u64 v[224:225], s[62:63], 0, v[136:137]
	global_load_lds_dwordx4 v[200:201], off
	s_add_i32 m0, s65, 0x2000
	v_lshl_add_u64 v[226:227], s[6:7], 0, v[130:131]
	global_load_lds_dwordx4 v[224:225], off
	s_mov_b32 m0, s45
	v_lshl_add_u64 v[228:229], s[6:7], 0, v[134:135]
	global_load_lds_dwordx4 v[226:227], off
	s_mov_b32 m0, s46
	s_nop 0
	global_load_lds_dwordx4 v[228:229], off
	s_waitcnt vmcnt(8)
	s_waitcnt lgkmcnt(0)
	s_barrier
; #define PG8_STAGE(bufoff, gbase, voff) do { _Pragma("unroll") for (int _i = 0; _i < 2; ++_i) \
;         __builtin_amdgcn_global_load_lds((const unsigned*)((const char*)(gbase) + (voff)[_i]), (PG8_LAS unsigned*)(lds + (bufoff) + ldsw + _i * 8192), 16, 0, 0); } while (0)
; #define PG8_WAIT_V(n) asm volatile("s_waitcnt vmcnt(" #n ")" ::: "memory")
; #define PG8_WAIT_L(n) asm volatile("s_waitcnt lgkmcnt(" #n ")" ::: "memory")
; #define PG8_BAR __builtin_amdgcn_s_barrier()
; #define PG8_SCHED __builtin_amdgcn_sched_barrier(0)
; template <class Epi, class Sched, bool ALIGN_EPI = false, bool SP2 = false, bool F8 = false>
; __device__ __forceinline__ void gemm_phase(PG8_LAS unsigned char* lds, const Gemm g, const Sched& S, const Epi& E, const int tidb  ) {
;     ...
;             PG8_WAIT_V(8); PG8_WAIT_L(0); PG8_BAR; PG8_MMA(1, 0, At, B0); PG8_MMA(1, 1, At, B1); PG8_BAR; PG8_SCHED;
;             PG8_LDB(B0, 1, 0); PG8_LDB(B1, 1, 1); PG8_SCHED; PG8_LDA(At, 1, 0); PG8_STAGE(PG8_SA(0, 1), a2 + hstep, voffA);
;             PG8_WAIT_V(8); PG8_WAIT_L(0); PG8_BAR; PG8_MMA(0, 0, At, B0); PG8_MMA(0, 1, At, B1); PG8_BAR; PG8_SCHED;
	s_setprio 1
	s_waitcnt lgkmcnt(0)
	v_mfma_f32_16x16x32_bf16 v[94:97], v[142:145], v[184:187], v[94:97]
	v_mfma_f32_16x16x32_bf16 v[90:93], v[154:157], v[184:187], v[90:93]
	v_mfma_f32_16x16x32_bf16 v[86:89], v[142:145], v[192:195], v[86:89]
	v_mfma_f32_16x16x32_bf16 v[82:85], v[154:157], v[192:195], v[82:85]
	v_mfma_f32_16x16x32_bf16 v[78:81], v[142:145], v[208:211], v[78:81]
	v_mfma_f32_16x16x32_bf16 v[74:77], v[154:157], v[208:211], v[74:77]
	v_mfma_f32_16x16x32_bf16 v[70:73], v[142:145], v[216:219], v[70:73]
	v_mfma_f32_16x16x32_bf16 v[66:69], v[154:157], v[216:219], v[66:69]
	v_mfma_f32_16x16x32_bf16 v[94:97], v[146:149], v[188:191], v[94:97]
	v_mfma_f32_16x16x32_bf16 v[90:93], v[164:167], v[188:191], v[90:93]
	v_mfma_f32_16x16x32_bf16 v[86:89], v[146:149], v[204:207], v[86:89]
	v_mfma_f32_16x16x32_bf16 v[82:85], v[164:167], v[204:207], v[82:85]
	v_mfma_f32_16x16x32_bf16 v[78:81], v[146:149], v[212:215], v[78:81]
	v_mfma_f32_16x16x32_bf16 v[74:77], v[164:167], v[212:215], v[74:77]
	v_mfma_f32_16x16x32_bf16 v[70:73], v[146:149], v[220:223], v[70:73]
	v_mfma_f32_16x16x32_bf16 v[66:69], v[164:167], v[220:223], v[66:69]
	s_setprio 0
	s_setprio 1
	v_mfma_f32_16x16x32_bf16 v[30:33], v[168:171], v[184:187], v[30:33]
	v_mfma_f32_16x16x32_bf16 v[26:29], v[176:179], v[184:187], v[26:29]
	v_mfma_f32_16x16x32_bf16 v[22:25], v[168:171], v[192:195], v[22:25]
	v_mfma_f32_16x16x32_bf16 v[18:21], v[176:179], v[192:195], v[18:21]
	v_mfma_f32_16x16x32_bf16 v[14:17], v[168:171], v[208:211], v[14:17]
	v_mfma_f32_16x16x32_bf16 v[10:13], v[176:179], v[208:211], v[10:13]
	v_mfma_f32_16x16x32_bf16 v[6:9], v[168:171], v[216:219], v[6:9]
	v_mfma_f32_16x16x32_bf16 v[2:5], v[176:179], v[216:219], v[2:5]
	v_mfma_f32_16x16x32_bf16 v[30:33], v[172:175], v[188:191], v[30:33]
	v_mfma_f32_16x16x32_bf16 v[26:29], v[180:183], v[188:191], v[26:29]
	v_mfma_f32_16x16x32_bf16 v[22:25], v[172:175], v[204:207], v[22:25]
	v_mfma_f32_16x16x32_bf16 v[18:21], v[180:183], v[204:207], v[18:21]
	v_mfma_f32_16x16x32_bf16 v[14:17], v[172:175], v[212:215], v[14:17]
	v_mfma_f32_16x16x32_bf16 v[10:13], v[180:183], v[212:215], v[10:13]
	v_mfma_f32_16x16x32_bf16 v[6:9], v[172:175], v[220:223], v[6:9]
	v_mfma_f32_16x16x32_bf16 v[2:5], v[180:183], v[220:223], v[2:5]
	s_setprio 0
	s_barrier
	s_add_i32 s62, 0, 0x18000
	v_add_u32_e32 v0, s62, v159
	s_add_i32 s63, 0, 0x1c000
	ds_read_b128 v[142:145], v0
	ds_read_b128 v[146:149], v0 offset:1024
	ds_read_b128 v[154:157], v0 offset:2048
	ds_read_b128 v[164:167], v0 offset:3072
	v_add_u32_e32 v0, s63, v159
	ds_read_b128 v[168:171], v0
	ds_read_b128 v[172:175], v0 offset:1024
	ds_read_b128 v[176:179], v0 offset:2048
	ds_read_b128 v[180:183], v0 offset:3072
	s_add_u32 s6, s6, s8
	s_addc_u32 s7, s7, s9
	s_mov_b32 m0, s47
	v_lshl_add_u64 v[230:231], s[6:7], 0, v[130:131]
	ds_read_b128 v[184:187], v160 offset:32768
	ds_read_b128 v[188:191], v160 offset:33792
	ds_read_b128 v[192:195], v160 offset:34816
	ds_read_b128 v[204:207], v160 offset:35840
	ds_read_b128 v[208:211], v160 offset:36864
	ds_read_b128 v[212:215], v160 offset:37888
	ds_read_b128 v[216:219], v160 offset:38912
	ds_read_b128 v[220:223], v160 offset:39936
	global_load_lds_dwordx4 v[230:231], off
	v_lshl_add_u64 v[230:231], s[6:7], 0, v[134:135]
	s_mov_b32 m0, s48
	s_nop 0
	global_load_lds_dwordx4 v[230:231], off
	s_waitcnt vmcnt(8)
	s_waitcnt lgkmcnt(0)
	s_barrier
	s_setprio 1
	s_waitcnt lgkmcnt(0)
	v_mfma_f32_16x16x32_bf16 v[126:129], v[142:145], v[184:187], v[126:129]
	v_mfma_f32_16x16x32_bf16 v[122:125], v[154:157], v[184:187], v[122:125]
	v_mfma_f32_16x16x32_bf16 v[118:121], v[142:145], v[192:195], v[118:121]
	v_mfma_f32_16x16x32_bf16 v[114:117], v[154:157], v[192:195], v[114:117]
	v_mfma_f32_16x16x32_bf16 v[110:113], v[142:145], v[208:211], v[110:113]
	v_mfma_f32_16x16x32_bf16 v[106:109], v[154:157], v[208:211], v[106:109]
	v_mfma_f32_16x16x32_bf16 v[102:105], v[142:145], v[216:219], v[102:105]
	v_mfma_f32_16x16x32_bf16 v[98:101], v[154:157], v[216:219], v[98:101]
	v_mfma_f32_16x16x32_bf16 v[126:129], v[146:149], v[188:191], v[126:129]
	v_mfma_f32_16x16x32_bf16 v[122:125], v[164:167], v[188:191], v[122:125]
	v_mfma_f32_16x16x32_bf16 v[118:121], v[146:149], v[204:207], v[118:121]
	v_mfma_f32_16x16x32_bf16 v[114:117], v[164:167], v[204:207], v[114:117]
	v_mfma_f32_16x16x32_bf16 v[110:113], v[146:149], v[212:215], v[110:113]
	v_mfma_f32_16x16x32_bf16 v[106:109], v[164:167], v[212:215], v[106:109]
	v_mfma_f32_16x16x32_bf16 v[102:105], v[146:149], v[220:223], v[102:105]
	v_mfma_f32_16x16x32_bf16 v[98:101], v[164:167], v[220:223], v[98:101]
	s_setprio 0
	s_setprio 1
	v_mfma_f32_16x16x32_bf16 v[62:65], v[168:171], v[184:187], v[62:65]
	v_mfma_f32_16x16x32_bf16 v[58:61], v[176:179], v[184:187], v[58:61]
	v_mfma_f32_16x16x32_bf16 v[54:57], v[168:171], v[192:195], v[54:57]
	v_mfma_f32_16x16x32_bf16 v[50:53], v[176:179], v[192:195], v[50:53]
	v_mfma_f32_16x16x32_bf16 v[46:49], v[168:171], v[208:211], v[46:49]
	v_mfma_f32_16x16x32_bf16 v[42:45], v[176:179], v[208:211], v[42:45]
	v_mfma_f32_16x16x32_bf16 v[38:41], v[168:171], v[216:219], v[38:41]
	v_mfma_f32_16x16x32_bf16 v[34:37], v[176:179], v[216:219], v[34:37]
	v_mfma_f32_16x16x32_bf16 v[62:65], v[172:175], v[188:191], v[62:65]
	v_mfma_f32_16x16x32_bf16 v[58:61], v[180:183], v[188:191], v[58:61]
	v_mfma_f32_16x16x32_bf16 v[54:57], v[172:175], v[204:207], v[54:57]
	v_mfma_f32_16x16x32_bf16 v[50:53], v[180:183], v[204:207], v[50:53]
	v_mfma_f32_16x16x32_bf16 v[46:49], v[172:175], v[212:215], v[46:49]
	v_mfma_f32_16x16x32_bf16 v[42:45], v[180:183], v[212:215], v[42:45]
	v_mfma_f32_16x16x32_bf16 v[38:41], v[172:175], v[220:223], v[38:41]
	v_mfma_f32_16x16x32_bf16 v[34:37], v[180:183], v[220:223], v[34:37]
	s_setprio 0
	s_barrier
; #define PG8_STAGE(bufoff, gbase, voff) do { _Pragma("unroll") for (int _i = 0; _i < 2; ++_i) \
;         __builtin_amdgcn_global_load_lds((const unsigned*)((const char*)(gbase) + (voff)[_i]), (PG8_LAS unsigned*)(lds + (bufoff) + ldsw + _i * 8192), 16, 0, 0); } while (0)
; #define PG8_WAIT_V(n) asm volatile("s_waitcnt vmcnt(" #n ")" ::: "memory")
; #define PG8_WAIT_L(n) asm volatile("s_waitcnt lgkmcnt(" #n ")" ::: "memory")
; #define PG8_BAR __builtin_amdgcn_s_barrier()
; #define PG8_SCHED __builtin_amdgcn_sched_barrier(0)
; template <class Epi, class Sched, bool ALIGN_EPI = false, bool SP2 = false, bool F8 = false>
; __device__ __forceinline__ void gemm_phase(PG8_LAS unsigned char* lds, const Gemm g, const Sched& S, const Epi& E, const int tidb  ) {
;     ...
;         for (int t = 0; t < nt; t += 2) {
;             const bool last = (t == nt - 2);
;             if constexpr (Epi::PREFETCH) { if (t == 0) E.prefetch(cur, wid, lane); }
;             const char* a1 = cA + (size_t)(t + 1) * kstep;
;             const char* a2 = last ? nA : cA + (size_t)(t + 2) * kstep; const char* b2 = last ? nB : cB + (size_t)(t + 2) * kstep;
;             const char* a3 = a2 + kstep; const char* b3 = b2 + kstep;
;     ...
;             PG8_LDA(At, 1, 1); PG8_STAGE(PG8_SB(1, 0), b3, voffB); PG8_STAGE(PG8_SB(1, 1), b3 + hstep, voffB); PG8_STAGE(PG8_SA(1, 0), a3, voffA);
;             PG8_WAIT_V(8); PG8_WAIT_L(0); PG8_BAR; PG8_MMA(1, 0, At, B0); PG8_MMA(1, 1, At, B1); PG8_BAR; PG8_SCHED;
	s_add_i32 s6, s62, s43
	v_lshl_add_u64 v[150:151], v[150:151], 0, s[92:93]
	s_mov_b32 m0, s6
	ds_read_b128 v[184:187], v160 offset:49152
	ds_read_b128 v[188:191], v160 offset:50176
	ds_read_b128 v[192:195], v160 offset:51200
	ds_read_b128 v[204:207], v160 offset:52224
	ds_read_b128 v[208:211], v160 offset:53248
	ds_read_b128 v[212:215], v160 offset:54272
	ds_read_b128 v[216:219], v160 offset:55296
	ds_read_b128 v[220:223], v160 offset:56320
	global_load_lds_dwordx4 v[150:151], off
	v_lshl_add_u64 v[150:151], v[196:197], 0, s[92:93]
	s_add_i32 m0, s6, 0x2000
	s_add_i32 s6, s63, s43
	global_load_lds_dwordx4 v[150:151], off
	v_lshl_add_u64 v[150:151], v[200:201], 0, s[92:93]
	s_mov_b32 m0, s6
	s_nop 0
	global_load_lds_dwordx4 v[150:151], off
	v_lshl_add_u64 v[150:151], v[224:225], 0, s[92:93]
	s_add_i32 m0, s6, 0x2000
	s_nop 0
	global_load_lds_dwordx4 v[150:151], off
	v_lshl_add_u64 v[150:151], v[226:227], 0, s[92:93]
	s_mov_b32 m0, s49
	s_nop 0
	global_load_lds_dwordx4 v[150:151], off
	v_lshl_add_u64 v[150:151], v[228:229], 0, s[92:93]
	s_mov_b32 m0, s50
	s_nop 0
	global_load_lds_dwordx4 v[150:151], off
	s_waitcnt vmcnt(8)
	s_waitcnt lgkmcnt(0)
	s_barrier
	s_setprio 1
	s_waitcnt lgkmcnt(0)
	v_mfma_f32_16x16x32_bf16 v[94:97], v[142:145], v[184:187], v[94:97]
	v_mfma_f32_16x16x32_bf16 v[90:93], v[154:157], v[184:187], v[90:93]
	v_mfma_f32_16x16x32_bf16 v[86:89], v[142:145], v[192:195], v[86:89]
	v_mfma_f32_16x16x32_bf16 v[82:85], v[154:157], v[192:195], v[82:85]
	v_mfma_f32_16x16x32_bf16 v[78:81], v[142:145], v[208:211], v[78:81]
	v_mfma_f32_16x16x32_bf16 v[74:77], v[154:157], v[208:211], v[74:77]
	v_mfma_f32_16x16x32_bf16 v[70:73], v[142:145], v[216:219], v[70:73]
	v_mfma_f32_16x16x32_bf16 v[66:69], v[154:157], v[216:219], v[66:69]
	v_mfma_f32_16x16x32_bf16 v[94:97], v[146:149], v[188:191], v[94:97]
	v_mfma_f32_16x16x32_bf16 v[90:93], v[164:167], v[188:191], v[90:93]
	v_mfma_f32_16x16x32_bf16 v[86:89], v[146:149], v[204:207], v[86:89]
	v_mfma_f32_16x16x32_bf16 v[82:85], v[164:167], v[204:207], v[82:85]
	v_mfma_f32_16x16x32_bf16 v[78:81], v[146:149], v[212:215], v[78:81]
	v_mfma_f32_16x16x32_bf16 v[74:77], v[164:167], v[212:215], v[74:77]
	v_mfma_f32_16x16x32_bf16 v[70:73], v[146:149], v[220:223], v[70:73]
	v_mfma_f32_16x16x32_bf16 v[66:69], v[164:167], v[220:223], v[66:69]
	s_setprio 0
	s_setprio 1
	v_mfma_f32_16x16x32_bf16 v[30:33], v[168:171], v[184:187], v[30:33]
	v_mfma_f32_16x16x32_bf16 v[26:29], v[176:179], v[184:187], v[26:29]
	v_mfma_f32_16x16x32_bf16 v[22:25], v[168:171], v[192:195], v[22:25]
	v_mfma_f32_16x16x32_bf16 v[18:21], v[176:179], v[192:195], v[18:21]
	v_mfma_f32_16x16x32_bf16 v[14:17], v[168:171], v[208:211], v[14:17]
	v_mfma_f32_16x16x32_bf16 v[10:13], v[176:179], v[208:211], v[10:13]
	v_mfma_f32_16x16x32_bf16 v[6:9], v[168:171], v[216:219], v[6:9]
	v_mfma_f32_16x16x32_bf16 v[2:5], v[176:179], v[216:219], v[2:5]
	v_mfma_f32_16x16x32_bf16 v[30:33], v[172:175], v[188:191], v[30:33]
	v_mfma_f32_16x16x32_bf16 v[26:29], v[180:183], v[188:191], v[26:29]
	v_mfma_f32_16x16x32_bf16 v[22:25], v[172:175], v[204:207], v[22:25]
	v_mfma_f32_16x16x32_bf16 v[18:21], v[180:183], v[204:207], v[18:21]
	v_mfma_f32_16x16x32_bf16 v[14:17], v[172:175], v[212:215], v[14:17]
	v_mfma_f32_16x16x32_bf16 v[10:13], v[180:183], v[212:215], v[10:13]
	v_mfma_f32_16x16x32_bf16 v[6:9], v[172:175], v[220:223], v[6:9]
	v_mfma_f32_16x16x32_bf16 v[2:5], v[180:183], v[220:223], v[2:5]
	s_setprio 0
	s_add_u32 s4, s4, 0x100
	s_addc_u32 s5, s5, 0
	s_add_u32 s28, s28, 0x100
	s_addc_u32 s29, s29, 0
	s_cmp_ge_i32 s61, s51
	s_mov_b32 s6, s61
	s_barrier
	s_cbranch_scc0 .LBB0_465

; #define ALAS __attribute__((address_space(3)))
; #define ATT_WAIT_BAR() asm volatile("s_waitcnt vmcnt(0) lgkmcnt(0)\n\ts_barrier" ::: "memory")
; #define MF_ISSUE_K(t, s) do { glds16(ksrc + (long)(t) * 64 * 512, (unsigned)__builtin_amdgcn_readfirstlane(kdst + (s) * KSLOT)); \
;         if (wid < 4) glds16(krsrc + (long)(t) * 64 * 32, (unsigned)__builtin_amdgcn_readfirstlane(krdst + (s) * KSLOT)); } while (0)
; #define MF_ISSUE_V(t, s) glds16(vsrc + (long)(t) * 64 * 512, (unsigned)__builtin_amdgcn_readfirstlane(vdst + (s) * VSLOT))
; #define MF_ISSUE_K(t, s) glds16(ks8 + (long)(t) * kst8, (unsigned)__builtin_amdgcn_readfirstlane(kdst + (s) * KSLOT))
; #define MF_ISSUE_V(t, s) glds16(vsrc + (long)(t) * 64 * 512, (unsigned)__builtin_amdgcn_readfirstlane(vdst + (s) * VSLOT))
; #define MF_ISSUE_K(t, s) glds16(ks8 + (long)(t) * kst8, (unsigned)__builtin_amdgcn_readfirstlane(kdst + (s) * KSLOT))
; __device__ __forceinline__ bool mla_unit_fast88(const Args& A, int b, int h, int qb, ALAS char* shm, const int tidb) {
;     ...
;     for (int t2 = 0; t2 < t_end; t2 += 2) {
; #pragma unroll
;         for (int p = 0; p < 2; ++p) {
;             const int t = t2 + p; f32x16 &C0 = cs[p][0], &C1 = cs[p][1], &N0 = cs[p ^ 1][0], &N1 = cs[p ^ 1][1];
;             const bool vis = !bailed && t <= cw;
;             const int ks1 = ks == 2 ? 0 : ks + 1, ks2 = ks1 == 2 ? 0 : ks1 + 1;
;             if (t + 2 < t_end) MF_ISSUE_K(t + 2, ks2);
;             if (t + 1 < t_end) MF_ISSUE_V(t + 1, vs ^ 1);
;             if (vis) {
;                 {
;                     ALAS const char* Ks_ = Kfr + ks1 * KSLOT;
;                     v8i kfa, kfb; M8_KFRAG(kfa, Ks_, 0, 0);
;                     M8_KFRAG(kfb, Ks_, 0, 1);
;                     mfma8_new(N0, kfa, qf0, negm, sa8, sb8);
; #pragma unroll
;                     for (int e = 0; e < 8; ++e) C0[e] = __builtin_amdgcn_exp2f(C0[e]);
;                     __builtin_amdgcn_sched_barrier(0);
;                     M8_KFRAG(kfa, Ks_, 1, 0);
;     ...
;                 mfma8p_acc(o0, pf, vf0, 0x7f7f7f7f, 0x7c7c7c7c);
;                 mfma8p_acc(o1, pf, vf1, 0x7f7f7f7f, 0x7c7c7c7c);
;                 mfma8p_acc(ls, pf, ones8, 0x7f7f7f7f, 0x7f7f7f7f);
;                 __builtin_amdgcn_sched_barrier(0);
;             }
;             ks = ks1; vs ^= 1;
;             ATT_WAIT_BAR();
.LBB0_655:
	s_add_i32 s8, s4, 1
	s_waitcnt vmcnt(0) lgkmcnt(0)
	s_cmp_lg_u32 s4, 2
	s_cselect_b32 s4, s8, 0
	v_lshl_add_u32 v171, s4, 13, v157
	s_barrier
	ds_read_b128 v[82:85], v171
	ds_read_b128 v[86:89], v171 offset:1024
	ds_read_b128 v[164:167], v171 offset:2048
	ds_read_b128 v[168:171], v171 offset:3072
	v_mfma_scale_f32_32x32x64_f8f6f4 v[18:33], v[180:187], v[172:179], v[18:33], v251, v247 op_sel_hi:[0,0,0] cbsz:1
	s_cmp_ge_u32 s5, s0
	s_cbranch_scc1 .LBB0_661
	s_lshl_b32 s8, s4, 13
	s_addk_i32 s8, 0x2000
	s_cmp_lg_u32 s4, 2
	s_cselect_b32 s8, s8, 0
	v_lshl_add_u64 v[146:147], v[146:147], 0, v[148:149]
	s_add_i32 s8, s8, s45
	s_mov_b32 s9, m0
	s_mov_b32 m0, s8
	s_nop 0
	global_load_lds_dwordx4 v[146:147], off
	s_mov_b32 m0, s9
	s_and_b64 s[2:3], s[34:35], s[2:3]
	s_andn2_b64 vcc, exec, s[2:3]
	s_cbranch_vccz .LBB0_662

; #define ATT_WAIT_BAR() asm volatile("s_waitcnt vmcnt(0) lgkmcnt(0)\n\ts_barrier" ::: "memory")
; #define MF_ISSUE_K(t, s) do { glds16(ksrc + (long)(t) * 64 * 512, (unsigned)__builtin_amdgcn_readfirstlane(kdst + (s) * KSLOT)); \
;         if (wid < 4) glds16(krsrc + (long)(t) * 64 * 32, (unsigned)__builtin_amdgcn_readfirstlane(krdst + (s) * KSLOT)); } while (0)
; #define MF_ISSUE_V(t, s) glds16(vsrc + (long)(t) * 64 * 512, (unsigned)__builtin_amdgcn_readfirstlane(vdst + (s) * VSLOT))
; #define MF_ISSUE_K(t, s) glds16(ks8 + (long)(t) * kst8, (unsigned)__builtin_amdgcn_readfirstlane(kdst + (s) * KSLOT))
; #define MF_ISSUE_V(t, s) glds16(vsrc + (long)(t) * 64 * 512, (unsigned)__builtin_amdgcn_readfirstlane(vdst + (s) * VSLOT))
; #define MF_ISSUE_K(t, s) glds16(ks8 + (long)(t) * kst8, (unsigned)__builtin_amdgcn_readfirstlane(kdst + (s) * KSLOT))
; #define MF_ISSUE_V(t, s) do { if (wid < 4) glds16(vs8 + (long)(t) * 4096, (unsigned)__builtin_amdgcn_readfirstlane(vdst + (s) * 4096)); } while (0)
; __device__ __forceinline__ bool mla_unit_fast88(const Args& A, int b, int h, int qb, ALAS char* shm, const int tidb) {
;     ...
;     for (int t2 = 0; t2 < t_end; t2 += 2) {
; #pragma unroll
;         for (int p = 0; p < 2; ++p) {
;             const int t = t2 + p; f32x16 &C0 = cs[p][0], &C1 = cs[p][1], &N0 = cs[p ^ 1][0], &N1 = cs[p ^ 1][1];
;             const bool vis = !bailed && t <= cw;
;             const int ks1 = ks == 2 ? 0 : ks + 1, ks2 = ks1 == 2 ? 0 : ks1 + 1;
;             if (t + 2 < t_end) MF_ISSUE_K(t + 2, ks2);
;             if (t + 1 < t_end) MF_ISSUE_V(t + 1, vs ^ 1);
;     ...
;             ks = ks1; vs ^= 1;
;             ATT_WAIT_BAR();
.LBB0_659:
	s_waitcnt vmcnt(0) lgkmcnt(0)
	s_add_i32 s5, s5, 2
	v_lshl_add_u64 v[150:151], v[150:151], 0, s[80:81]
	s_cmp_ge_u32 s6, s0
	s_barrier
	s_cbranch_scc1 .LBB0_665
	v_mov_b64_e32 v[146:147], v[152:153]
	s_branch .LBB0_649

; #define PG8_STAGE(bufoff, gbase, voff) do { _Pragma("unroll") for (int _i = 0; _i < 2; ++_i) \
;         __builtin_amdgcn_global_load_lds((const unsigned*)((const char*)(gbase) + (voff)[_i]), (PG8_LAS unsigned*)(lds + (bufoff) + ldsw + _i * 8192), 16, 0, 0); } while (0)
; #define PG8_WAIT_V(n) asm volatile("s_waitcnt vmcnt(" #n ")" ::: "memory")
; #define PG8_WAIT_L(n) asm volatile("s_waitcnt lgkmcnt(" #n ")" ::: "memory")
; #define PG8_BAR __builtin_amdgcn_s_barrier()
; #define PG8_SCHED __builtin_amdgcn_sched_barrier(0)
; template <class Epi, class Sched, bool ALIGN_EPI = false, bool SP2 = false, bool F8 = false>
; __device__ __forceinline__ void gemm_phase(PG8_LAS unsigned char* lds, const Gemm g, const Sched& S, const Epi& E, const int tidb  ) {
;     ...
;             if constexpr (SP2) {
;             PG8_LDB(B0, 0, 0); PG8_LDB(B1, 0, 1); PG8_SCHED; PG8_LDA(At, 0, 0); PG8_STAGE(PG8_SA(1, 1), a1 + hstep, voffA);
;             PG8_WAIT_V(8); PG8_WAIT_L(0); PG8_BAR; PG8_MMA(0, 0, At, B0); PG8_MMA(0, 1, At, B1); PG8_BAR; PG8_SCHED;
;             PG8_LDA(At, 0, 1); PG8_STAGE(PG8_SB(0, 0), b2, voffB); PG8_STAGE(PG8_SB(0, 1), b2 + hstep, voffB); PG8_STAGE(PG8_SA(0, 0), a2, voffA);
;             PG8_WAIT_V(8); PG8_WAIT_L(0); PG8_BAR; PG8_MMA(1, 0, At, B0); PG8_MMA(1, 1, At, B1); PG8_BAR; PG8_SCHED;
.LBB0_943:
	s_add_i32 s60, s26, 2
	s_add_u32 s61, s24, 0x80
	s_addc_u32 s27, s25, 0
	s_add_i32 s65, 0, 0x10000
	s_cmp_eq_u32 s45, s26
	s_cselect_b32 s27, s7, s27
	s_cselect_b32 s26, s6, s61
	s_cselect_b32 s63, s23, s59
	s_cselect_b32 s62, s22, s58
	s_add_i32 s61, 0, 0x14000
	v_add_u32_e32 v142, s65, v196
	v_add_u32_e32 v158, s61, v196
	ds_read_b128 v[130:133], v142
	ds_read_b128 v[134:137], v142 offset:1024
	ds_read_b128 v[138:141], v142 offset:2048
	ds_read_b128 v[142:145], v142 offset:3072
	ds_read_b128 v[146:149], v158
	ds_read_b128 v[150:153], v158 offset:1024
	ds_read_b128 v[154:157], v158 offset:2048
	ds_read_b128 v[158:161], v158 offset:3072
	v_lshl_add_u64 v[198:199], s[24:25], 0, v[210:211]
	s_add_i32 m0, s1, 0xc000
	ds_read_b128 v[164:167], v200
	ds_read_b128 v[168:171], v200 offset:1024
	ds_read_b128 v[172:175], v200 offset:2048
	ds_read_b128 v[176:179], v200 offset:3072
	ds_read_b128 v[180:183], v200 offset:4096
	ds_read_b128 v[184:187], v200 offset:5120
	ds_read_b128 v[188:191], v200 offset:6144
	ds_read_b128 v[192:195], v200 offset:7168
	global_load_lds_dwordx4 v[198:199], off
	v_lshl_add_u64 v[198:199], s[24:25], 0, v[212:213]
	s_add_i32 m0, s1, 0xe000
	s_nop 0
	global_load_lds_dwordx4 v[198:199], off
	s_waitcnt vmcnt(8)
	s_waitcnt lgkmcnt(0)
	s_barrier
	s_setprio 1
	s_waitcnt lgkmcnt(0)
	v_mfma_f32_16x16x32_bf16 v[126:129], v[130:133], v[164:167], v[126:129]
	v_mfma_f32_16x16x32_bf16 v[122:125], v[138:141], v[164:167], v[122:125]
	v_mfma_f32_16x16x32_bf16 v[110:113], v[130:133], v[172:175], v[110:113]
	v_mfma_f32_16x16x32_bf16 v[106:109], v[138:141], v[172:175], v[106:109]
	v_mfma_f32_16x16x32_bf16 v[94:97], v[130:133], v[180:183], v[94:97]
	v_mfma_f32_16x16x32_bf16 v[90:93], v[138:141], v[180:183], v[90:93]
	v_mfma_f32_16x16x32_bf16 v[78:81], v[130:133], v[188:191], v[78:81]
	v_mfma_f32_16x16x32_bf16 v[74:77], v[138:141], v[188:191], v[74:77]
	v_mfma_f32_16x16x32_bf16 v[126:129], v[134:137], v[168:171], v[126:129]
	v_mfma_f32_16x16x32_bf16 v[122:125], v[142:145], v[168:171], v[122:125]
	v_mfma_f32_16x16x32_bf16 v[110:113], v[134:137], v[176:179], v[110:113]
	v_mfma_f32_16x16x32_bf16 v[106:109], v[142:145], v[176:179], v[106:109]
	v_mfma_f32_16x16x32_bf16 v[94:97], v[134:137], v[184:187], v[94:97]
	v_mfma_f32_16x16x32_bf16 v[90:93], v[142:145], v[184:187], v[90:93]
	v_mfma_f32_16x16x32_bf16 v[78:81], v[134:137], v[192:195], v[78:81]
	v_mfma_f32_16x16x32_bf16 v[74:77], v[142:145], v[192:195], v[74:77]
	s_setprio 0
	s_setprio 1
	v_mfma_f32_16x16x32_bf16 v[118:121], v[146:149], v[164:167], v[118:121]
	v_mfma_f32_16x16x32_bf16 v[114:117], v[154:157], v[164:167], v[114:117]
	v_mfma_f32_16x16x32_bf16 v[102:105], v[146:149], v[172:175], v[102:105]
	v_mfma_f32_16x16x32_bf16 v[98:101], v[154:157], v[172:175], v[98:101]
	v_mfma_f32_16x16x32_bf16 v[86:89], v[146:149], v[180:183], v[86:89]
	v_mfma_f32_16x16x32_bf16 v[82:85], v[154:157], v[180:183], v[82:85]
	v_mfma_f32_16x16x32_bf16 v[70:73], v[146:149], v[188:191], v[70:73]
	v_mfma_f32_16x16x32_bf16 v[66:69], v[154:157], v[188:191], v[66:69]
	v_mfma_f32_16x16x32_bf16 v[118:121], v[150:153], v[168:171], v[118:121]
	v_mfma_f32_16x16x32_bf16 v[114:117], v[158:161], v[168:171], v[114:117]
	v_mfma_f32_16x16x32_bf16 v[102:105], v[150:153], v[176:179], v[102:105]
	v_mfma_f32_16x16x32_bf16 v[98:101], v[158:161], v[176:179], v[98:101]
	v_mfma_f32_16x16x32_bf16 v[86:89], v[150:153], v[184:187], v[86:89]
	v_mfma_f32_16x16x32_bf16 v[82:85], v[158:161], v[184:187], v[82:85]
	v_mfma_f32_16x16x32_bf16 v[70:73], v[150:153], v[192:195], v[70:73]
	v_mfma_f32_16x16x32_bf16 v[66:69], v[158:161], v[192:195], v[66:69]
	s_setprio 0
	s_barrier
	s_add_i32 s65, s65, s0
	v_lshl_add_u64 v[198:199], s[62:63], 0, v[0:1]
	s_mov_b32 m0, s65
	ds_read_b128 v[164:167], v200 offset:16384
	ds_read_b128 v[168:171], v200 offset:17408
	ds_read_b128 v[172:175], v200 offset:18432
	ds_read_b128 v[176:179], v200 offset:19456
	ds_read_b128 v[180:183], v200 offset:20480
	ds_read_b128 v[184:187], v200 offset:21504
	ds_read_b128 v[188:191], v200 offset:22528
	ds_read_b128 v[192:195], v200 offset:23552
	global_load_lds_dwordx4 v[198:199], off
	s_add_i32 m0, s65, 0x2000
	v_lshl_add_u64 v[214:215], s[62:63], 0, v[208:209]
	s_add_u32 s62, s62, s10
	s_addc_u32 s63, s63, s11
	s_add_i32 s61, s61, s0
	global_load_lds_dwordx4 v[214:215], off
	v_lshl_add_u64 v[216:217], s[62:63], 0, v[0:1]
	s_mov_b32 m0, s61
	v_lshl_add_u64 v[218:219], s[62:63], 0, v[208:209]
	global_load_lds_dwordx4 v[216:217], off
	s_add_i32 m0, s61, 0x2000
	v_lshl_add_u64 v[220:221], s[26:27], 0, v[204:205]
	global_load_lds_dwordx4 v[218:219], off
	s_mov_b32 m0, s1
	v_lshl_add_u64 v[222:223], s[26:27], 0, v[206:207]
	global_load_lds_dwordx4 v[220:221], off
	s_mov_b32 m0, s28
	s_nop 0
	global_load_lds_dwordx4 v[222:223], off
	s_waitcnt vmcnt(8)
	s_waitcnt lgkmcnt(0)
	s_barrier
; #define PG8_STAGE(bufoff, gbase, voff) do { _Pragma("unroll") for (int _i = 0; _i < 2; ++_i) \
;         __builtin_amdgcn_global_load_lds((const unsigned*)((const char*)(gbase) + (voff)[_i]), (PG8_LAS unsigned*)(lds + (bufoff) + ldsw + _i * 8192), 16, 0, 0); } while (0)
; #define PG8_WAIT_V(n) asm volatile("s_waitcnt vmcnt(" #n ")" ::: "memory")
; #define PG8_WAIT_L(n) asm volatile("s_waitcnt lgkmcnt(" #n ")" ::: "memory")
; #define PG8_BAR __builtin_amdgcn_s_barrier()
; #define PG8_SCHED __builtin_amdgcn_sched_barrier(0)
; template <class Epi, class Sched, bool ALIGN_EPI = false, bool SP2 = false, bool F8 = false>
; __device__ __forceinline__ void gemm_phase(PG8_LAS unsigned char* lds, const Gemm g, const Sched& S, const Epi& E, const int tidb  ) {
;     ...
;             PG8_WAIT_V(8); PG8_WAIT_L(0); PG8_BAR; PG8_MMA(1, 0, At, B0); PG8_MMA(1, 1, At, B1); PG8_BAR; PG8_SCHED;
;             PG8_LDB(B0, 1, 0); PG8_LDB(B1, 1, 1); PG8_SCHED; PG8_LDA(At, 1, 0); PG8_STAGE(PG8_SA(0, 1), a2 + hstep, voffA);
;             PG8_WAIT_V(8); PG8_WAIT_L(0); PG8_BAR; PG8_MMA(0, 0, At, B0); PG8_MMA(0, 1, At, B1); PG8_BAR; PG8_SCHED;
	s_setprio 1
	s_waitcnt lgkmcnt(0)
	v_mfma_f32_16x16x32_bf16 v[62:65], v[130:133], v[164:167], v[62:65]
	v_mfma_f32_16x16x32_bf16 v[58:61], v[138:141], v[164:167], v[58:61]
	v_mfma_f32_16x16x32_bf16 v[46:49], v[130:133], v[172:175], v[46:49]
	v_mfma_f32_16x16x32_bf16 v[42:45], v[138:141], v[172:175], v[42:45]
	v_mfma_f32_16x16x32_bf16 v[30:33], v[130:133], v[180:183], v[30:33]
	v_mfma_f32_16x16x32_bf16 v[26:29], v[138:141], v[180:183], v[26:29]
	v_mfma_f32_16x16x32_bf16 v[14:17], v[130:133], v[188:191], v[14:17]
	v_mfma_f32_16x16x32_bf16 v[10:13], v[138:141], v[188:191], v[10:13]
	v_mfma_f32_16x16x32_bf16 v[62:65], v[134:137], v[168:171], v[62:65]
	v_mfma_f32_16x16x32_bf16 v[58:61], v[142:145], v[168:171], v[58:61]
	v_mfma_f32_16x16x32_bf16 v[46:49], v[134:137], v[176:179], v[46:49]
	v_mfma_f32_16x16x32_bf16 v[42:45], v[142:145], v[176:179], v[42:45]
	v_mfma_f32_16x16x32_bf16 v[30:33], v[134:137], v[184:187], v[30:33]
	v_mfma_f32_16x16x32_bf16 v[26:29], v[142:145], v[184:187], v[26:29]
	v_mfma_f32_16x16x32_bf16 v[14:17], v[134:137], v[192:195], v[14:17]
	v_mfma_f32_16x16x32_bf16 v[10:13], v[142:145], v[192:195], v[10:13]
	s_setprio 0
	s_setprio 1
	v_mfma_f32_16x16x32_bf16 v[54:57], v[146:149], v[164:167], v[54:57]
	v_mfma_f32_16x16x32_bf16 v[50:53], v[154:157], v[164:167], v[50:53]
	v_mfma_f32_16x16x32_bf16 v[38:41], v[146:149], v[172:175], v[38:41]
	v_mfma_f32_16x16x32_bf16 v[34:37], v[154:157], v[172:175], v[34:37]
	v_mfma_f32_16x16x32_bf16 v[22:25], v[146:149], v[180:183], v[22:25]
	v_mfma_f32_16x16x32_bf16 v[18:21], v[154:157], v[180:183], v[18:21]
	v_mfma_f32_16x16x32_bf16 v[6:9], v[146:149], v[188:191], v[6:9]
	v_mfma_f32_16x16x32_bf16 v[2:5], v[154:157], v[188:191], v[2:5]
	v_mfma_f32_16x16x32_bf16 v[54:57], v[150:153], v[168:171], v[54:57]
	v_mfma_f32_16x16x32_bf16 v[50:53], v[158:161], v[168:171], v[50:53]
	v_mfma_f32_16x16x32_bf16 v[38:41], v[150:153], v[176:179], v[38:41]
	v_mfma_f32_16x16x32_bf16 v[34:37], v[158:161], v[176:179], v[34:37]
	v_mfma_f32_16x16x32_bf16 v[22:25], v[150:153], v[184:187], v[22:25]
	v_mfma_f32_16x16x32_bf16 v[18:21], v[158:161], v[184:187], v[18:21]
	v_mfma_f32_16x16x32_bf16 v[6:9], v[150:153], v[192:195], v[6:9]
	v_mfma_f32_16x16x32_bf16 v[2:5], v[158:161], v[192:195], v[2:5]
	s_setprio 0
	s_barrier
	s_add_i32 s61, 0, 0x18000
	s_add_i32 s62, 0, 0x1c000
	v_add_u32_e32 v142, s61, v196
	v_add_u32_e32 v158, s62, v196
	ds_read_b128 v[130:133], v142
	ds_read_b128 v[134:137], v142 offset:1024
	ds_read_b128 v[138:141], v142 offset:2048
	ds_read_b128 v[142:145], v142 offset:3072
	ds_read_b128 v[146:149], v158
	ds_read_b128 v[150:153], v158 offset:1024
	ds_read_b128 v[154:157], v158 offset:2048
	ds_read_b128 v[158:161], v158 offset:3072
	s_add_u32 s26, s26, s10
	s_addc_u32 s27, s27, s11
	s_mov_b32 m0, s29
	v_lshl_add_u64 v[224:225], s[26:27], 0, v[204:205]
	ds_read_b128 v[164:167], v200 offset:32768
	ds_read_b128 v[168:171], v200 offset:33792
	ds_read_b128 v[172:175], v200 offset:34816
	ds_read_b128 v[176:179], v200 offset:35840
	ds_read_b128 v[180:183], v200 offset:36864
	ds_read_b128 v[184:187], v200 offset:37888
	ds_read_b128 v[188:191], v200 offset:38912
	ds_read_b128 v[192:195], v200 offset:39936
	global_load_lds_dwordx4 v[224:225], off
	v_lshl_add_u64 v[224:225], s[26:27], 0, v[206:207]
	s_mov_b32 m0, s36
	s_nop 0
	global_load_lds_dwordx4 v[224:225], off
	s_waitcnt vmcnt(8)
	s_waitcnt lgkmcnt(0)
	s_barrier
	s_setprio 1
	s_waitcnt lgkmcnt(0)
	v_mfma_f32_16x16x32_bf16 v[126:129], v[130:133], v[164:167], v[126:129]
	v_mfma_f32_16x16x32_bf16 v[122:125], v[138:141], v[164:167], v[122:125]
	v_mfma_f32_16x16x32_bf16 v[110:113], v[130:133], v[172:175], v[110:113]
	v_mfma_f32_16x16x32_bf16 v[106:109], v[138:141], v[172:175], v[106:109]
	v_mfma_f32_16x16x32_bf16 v[94:97], v[130:133], v[180:183], v[94:97]
	v_mfma_f32_16x16x32_bf16 v[90:93], v[138:141], v[180:183], v[90:93]
	v_mfma_f32_16x16x32_bf16 v[78:81], v[130:133], v[188:191], v[78:81]
	v_mfma_f32_16x16x32_bf16 v[74:77], v[138:141], v[188:191], v[74:77]
	v_mfma_f32_16x16x32_bf16 v[126:129], v[134:137], v[168:171], v[126:129]
	v_mfma_f32_16x16x32_bf16 v[122:125], v[142:145], v[168:171], v[122:125]
	v_mfma_f32_16x16x32_bf16 v[110:113], v[134:137], v[176:179], v[110:113]
	v_mfma_f32_16x16x32_bf16 v[106:109], v[142:145], v[176:179], v[106:109]
	v_mfma_f32_16x16x32_bf16 v[94:97], v[134:137], v[184:187], v[94:97]
	v_mfma_f32_16x16x32_bf16 v[90:93], v[142:145], v[184:187], v[90:93]
	v_mfma_f32_16x16x32_bf16 v[78:81], v[134:137], v[192:195], v[78:81]
	v_mfma_f32_16x16x32_bf16 v[74:77], v[142:145], v[192:195], v[74:77]
	s_setprio 0
	s_setprio 1
	v_mfma_f32_16x16x32_bf16 v[118:121], v[146:149], v[164:167], v[118:121]
	v_mfma_f32_16x16x32_bf16 v[114:117], v[154:157], v[164:167], v[114:117]
	v_mfma_f32_16x16x32_bf16 v[102:105], v[146:149], v[172:175], v[102:105]
	v_mfma_f32_16x16x32_bf16 v[98:101], v[154:157], v[172:175], v[98:101]
	v_mfma_f32_16x16x32_bf16 v[86:89], v[146:149], v[180:183], v[86:89]
	v_mfma_f32_16x16x32_bf16 v[82:85], v[154:157], v[180:183], v[82:85]
	v_mfma_f32_16x16x32_bf16 v[70:73], v[146:149], v[188:191], v[70:73]
	v_mfma_f32_16x16x32_bf16 v[66:69], v[154:157], v[188:191], v[66:69]
	v_mfma_f32_16x16x32_bf16 v[118:121], v[150:153], v[168:171], v[118:121]
	v_mfma_f32_16x16x32_bf16 v[114:117], v[158:161], v[168:171], v[114:117]
	v_mfma_f32_16x16x32_bf16 v[102:105], v[150:153], v[176:179], v[102:105]
	v_mfma_f32_16x16x32_bf16 v[98:101], v[158:161], v[176:179], v[98:101]
	v_mfma_f32_16x16x32_bf16 v[86:89], v[150:153], v[184:187], v[86:89]
	v_mfma_f32_16x16x32_bf16 v[82:85], v[158:161], v[184:187], v[82:85]
	v_mfma_f32_16x16x32_bf16 v[70:73], v[150:153], v[192:195], v[70:73]
	v_mfma_f32_16x16x32_bf16 v[66:69], v[158:161], v[192:195], v[66:69]
	s_setprio 0
	s_barrier
; #define PG8_STAGE(bufoff, gbase, voff) do { _Pragma("unroll") for (int _i = 0; _i < 2; ++_i) \
;         __builtin_amdgcn_global_load_lds((const unsigned*)((const char*)(gbase) + (voff)[_i]), (PG8_LAS unsigned*)(lds + (bufoff) + ldsw + _i * 8192), 16, 0, 0); } while (0)
; #define PG8_WAIT_V(n) asm volatile("s_waitcnt vmcnt(" #n ")" ::: "memory")
; #define PG8_WAIT_L(n) asm volatile("s_waitcnt lgkmcnt(" #n ")" ::: "memory")
; #define PG8_BAR __builtin_amdgcn_s_barrier()
; #define PG8_SCHED __builtin_amdgcn_sched_barrier(0)
; template <class Epi, class Sched, bool ALIGN_EPI = false, bool SP2 = false, bool F8 = false>
; __device__ __forceinline__ void gemm_phase(PG8_LAS unsigned char* lds, const Gemm g, const Sched& S, const Epi& E, const int tidb  ) {
;     ...
;         for (int t = 0; t < nt; t += 2) {
;             const bool last = (t == nt - 2);
;             if constexpr (Epi::PREFETCH) { if (t == 0) E.prefetch(cur, wid, lane); }
;             const char* a1 = cA + (size_t)(t + 1) * kstep;
;             const char* a2 = last ? nA : cA + (size_t)(t + 2) * kstep; const char* b2 = last ? nB : cB + (size_t)(t + 2) * kstep;
;             const char* a3 = a2 + kstep; const char* b3 = b2 + kstep;
;     ...
;             PG8_LDA(At, 1, 1); PG8_STAGE(PG8_SB(1, 0), b3, voffB); PG8_STAGE(PG8_SB(1, 1), b3 + hstep, voffB); PG8_STAGE(PG8_SA(1, 0), a3, voffA);
;             PG8_WAIT_V(8); PG8_WAIT_L(0); PG8_BAR; PG8_MMA(1, 0, At, B0); PG8_MMA(1, 1, At, B1); PG8_BAR; PG8_SCHED;
	s_add_i32 s26, s61, s0
	v_lshl_add_u64 v[198:199], v[198:199], 0, s[92:93]
	s_mov_b32 m0, s26
	ds_read_b128 v[164:167], v200 offset:49152
	ds_read_b128 v[168:171], v200 offset:50176
	ds_read_b128 v[172:175], v200 offset:51200
	ds_read_b128 v[176:179], v200 offset:52224
	ds_read_b128 v[180:183], v200 offset:53248
	ds_read_b128 v[184:187], v200 offset:54272
	ds_read_b128 v[188:191], v200 offset:55296
	ds_read_b128 v[192:195], v200 offset:56320
	global_load_lds_dwordx4 v[198:199], off
	v_lshl_add_u64 v[198:199], v[214:215], 0, s[92:93]
	s_add_i32 m0, s26, 0x2000
	s_add_i32 s26, s62, s0
	global_load_lds_dwordx4 v[198:199], off
	v_lshl_add_u64 v[198:199], v[216:217], 0, s[92:93]
	s_mov_b32 m0, s26
	s_nop 0
	global_load_lds_dwordx4 v[198:199], off
	v_lshl_add_u64 v[198:199], v[218:219], 0, s[92:93]
	s_add_i32 m0, s26, 0x2000
	s_nop 0
	global_load_lds_dwordx4 v[198:199], off
	v_lshl_add_u64 v[198:199], v[220:221], 0, s[92:93]
	s_mov_b32 m0, s37
	s_nop 0
	global_load_lds_dwordx4 v[198:199], off
	v_lshl_add_u64 v[198:199], v[222:223], 0, s[92:93]
	s_mov_b32 m0, s41
	s_nop 0
	global_load_lds_dwordx4 v[198:199], off
	s_waitcnt vmcnt(8)
	s_waitcnt lgkmcnt(0)
	s_barrier
	s_setprio 1
	s_waitcnt lgkmcnt(0)
	v_mfma_f32_16x16x32_bf16 v[62:65], v[130:133], v[164:167], v[62:65]
	v_mfma_f32_16x16x32_bf16 v[58:61], v[138:141], v[164:167], v[58:61]
	v_mfma_f32_16x16x32_bf16 v[46:49], v[130:133], v[172:175], v[46:49]
	v_mfma_f32_16x16x32_bf16 v[42:45], v[138:141], v[172:175], v[42:45]
	v_mfma_f32_16x16x32_bf16 v[30:33], v[130:133], v[180:183], v[30:33]
	v_mfma_f32_16x16x32_bf16 v[26:29], v[138:141], v[180:183], v[26:29]
	v_mfma_f32_16x16x32_bf16 v[14:17], v[130:133], v[188:191], v[14:17]
	v_mfma_f32_16x16x32_bf16 v[10:13], v[138:141], v[188:191], v[10:13]
	v_mfma_f32_16x16x32_bf16 v[62:65], v[134:137], v[168:171], v[62:65]
	v_mfma_f32_16x16x32_bf16 v[58:61], v[142:145], v[168:171], v[58:61]
	v_mfma_f32_16x16x32_bf16 v[46:49], v[134:137], v[176:179], v[46:49]
	v_mfma_f32_16x16x32_bf16 v[42:45], v[142:145], v[176:179], v[42:45]
	v_mfma_f32_16x16x32_bf16 v[30:33], v[134:137], v[184:187], v[30:33]
	v_mfma_f32_16x16x32_bf16 v[26:29], v[142:145], v[184:187], v[26:29]
	v_mfma_f32_16x16x32_bf16 v[14:17], v[134:137], v[192:195], v[14:17]
	v_mfma_f32_16x16x32_bf16 v[10:13], v[142:145], v[192:195], v[10:13]
	s_setprio 0
	s_setprio 1
	v_mfma_f32_16x16x32_bf16 v[54:57], v[146:149], v[164:167], v[54:57]
	v_mfma_f32_16x16x32_bf16 v[50:53], v[154:157], v[164:167], v[50:53]
	v_mfma_f32_16x16x32_bf16 v[38:41], v[146:149], v[172:175], v[38:41]
	v_mfma_f32_16x16x32_bf16 v[34:37], v[154:157], v[172:175], v[34:37]
	v_mfma_f32_16x16x32_bf16 v[22:25], v[146:149], v[180:183], v[22:25]
	v_mfma_f32_16x16x32_bf16 v[18:21], v[154:157], v[180:183], v[18:21]
	v_mfma_f32_16x16x32_bf16 v[6:9], v[146:149], v[188:191], v[6:9]
	v_mfma_f32_16x16x32_bf16 v[2:5], v[154:157], v[188:191], v[2:5]
	v_mfma_f32_16x16x32_bf16 v[54:57], v[150:153], v[168:171], v[54:57]
	v_mfma_f32_16x16x32_bf16 v[50:53], v[158:161], v[168:171], v[50:53]
	v_mfma_f32_16x16x32_bf16 v[38:41], v[150:153], v[176:179], v[38:41]
	v_mfma_f32_16x16x32_bf16 v[34:37], v[158:161], v[176:179], v[34:37]
	v_mfma_f32_16x16x32_bf16 v[22:25], v[150:153], v[184:187], v[22:25]
	v_mfma_f32_16x16x32_bf16 v[18:21], v[158:161], v[184:187], v[18:21]
	v_mfma_f32_16x16x32_bf16 v[6:9], v[150:153], v[192:195], v[6:9]
	v_mfma_f32_16x16x32_bf16 v[2:5], v[158:161], v[192:195], v[2:5]
	s_setprio 0
	s_add_u32 s24, s24, 0x100
	s_addc_u32 s25, s25, 0
	s_add_u32 s58, s58, 0x100
	s_addc_u32 s59, s59, 0
	s_cmp_ge_i32 s60, s43
	s_mov_b32 s26, s60
	s_barrier
	s_cbranch_scc0 .LBB0_943

;     __device__ __forceinline__ bool next(int i, Unit& u) const { return so.next(i, u); }
; #define PG8_STAGE(bufoff, gbase, voff) do { _Pragma("unroll") for (int _i = 0; _i < 2; ++_i) \
;         __builtin_amdgcn_global_load_lds((const unsigned*)((const char*)(gbase) + (voff)[_i]), (PG8_LAS unsigned*)(lds + (bufoff) + ldsw + _i * 8192), 16, 0, 0); } while (0)
; #define PG8_WAIT_V(n) asm volatile("s_waitcnt vmcnt(" #n ")" ::: "memory")
; #define PG8_WAIT_L(n) asm volatile("s_waitcnt lgkmcnt(" #n ")" ::: "memory")
; #define PG8_BAR __builtin_amdgcn_s_barrier()
; #define PG8_SCHED __builtin_amdgcn_sched_barrier(0)
; template <class Epi, class Sched, bool ALIGN_EPI = false, bool SP2 = false, bool F8 = false>
; __device__ __forceinline__ void gemm_phase(PG8_LAS unsigned char* lds, const Gemm g, const Sched& S, const Epi& E, const int tidb  ) {
;     ...
;         const bool has_next = S.next(ui + 1, nxt);
;         const char* nA = has_next ? (const char*)g.A + (size_t)nxt.pm * tstep : cA; const char* nB = has_next ? (const char*)g.Bt + S.boff(nxt) + (size_t)nxt.pn * tstep : cB;
;         for (int t = 0; t < nt; t += 2) {
;             const bool last = (t == nt - 2);
;             if constexpr (Epi::PREFETCH) { if (t == 0) E.prefetch(cur, wid, lane); }
;             const char* a1 = cA + (size_t)(t + 1) * kstep;
;             const char* a2 = last ? nA : cA + (size_t)(t + 2) * kstep; const char* b2 = last ? nB : cB + (size_t)(t + 2) * kstep;
;             const char* a3 = a2 + kstep; const char* b3 = b2 + kstep;
;             if (last && has_next) S.a_ready(nxt);
;             if constexpr (SP2) {
;             PG8_LDB(B0, 0, 0); PG8_LDB(B1, 0, 1); PG8_SCHED; PG8_LDA(At, 0, 0); PG8_STAGE(PG8_SA(1, 1), a1 + hstep, voffA);
;             PG8_WAIT_V(8); PG8_WAIT_L(0); PG8_BAR; PG8_MMA(0, 0, At, B0); PG8_MMA(0, 1, At, B1); PG8_BAR; PG8_SCHED;
;             PG8_LDA(At, 0, 1); PG8_STAGE(PG8_SB(0, 0), b2, voffB); PG8_STAGE(PG8_SB(0, 1), b2 + hstep, voffB); PG8_STAGE(PG8_SA(0, 0), a2, voffA);
;             PG8_WAIT_V(8); PG8_WAIT_L(0); PG8_BAR; PG8_MMA(1, 0, At, B0); PG8_MMA(1, 1, At, B1); PG8_BAR; PG8_SCHED;
.LBB0_993:
	s_add_i32 s62, s26, 2
	s_add_u32 s28, s24, 0x80
	s_addc_u32 s27, s25, 0
	s_add_i32 s63, 0, 0x10000
	s_cmp_eq_u32 s47, s26
	s_cselect_b32 s27, s7, s27
	s_cselect_b32 s26, s6, s28
	s_cselect_b32 s29, s23, s61
	s_cselect_b32 s28, s22, s60
	s_add_i32 s65, 0, 0x14000
	v_add_u32_e32 v2, s63, v200
	v_add_u32_e32 v14, s65, v200
	ds_read_b128 v[18:21], v2
	ds_read_b128 v[22:25], v2 offset:1024
	ds_read_b128 v[26:29], v2 offset:2048
	ds_read_b128 v[30:33], v2 offset:3072
	ds_read_b128 v[2:5], v14
	ds_read_b128 v[6:9], v14 offset:1024
	ds_read_b128 v[10:13], v14 offset:2048
	ds_read_b128 v[14:17], v14 offset:3072
	v_lshl_add_u64 v[198:199], s[24:25], 0, v[210:211]
	s_add_i32 m0, s1, 0xc000
	ds_read_b128 v[164:167], v196
	ds_read_b128 v[168:171], v196 offset:1024
	ds_read_b128 v[172:175], v196 offset:2048
	ds_read_b128 v[176:179], v196 offset:3072
	ds_read_b128 v[180:183], v196 offset:4096
	ds_read_b128 v[184:187], v196 offset:5120
	ds_read_b128 v[188:191], v196 offset:6144
	ds_read_b128 v[192:195], v196 offset:7168
	global_load_lds_dwordx4 v[198:199], off
	v_lshl_add_u64 v[198:199], s[24:25], 0, v[212:213]
	s_add_i32 m0, s1, 0xe000
	s_nop 0
	global_load_lds_dwordx4 v[198:199], off
	s_waitcnt vmcnt(8)
	s_waitcnt lgkmcnt(0)
	s_barrier
	s_setprio 1
	s_waitcnt lgkmcnt(0)
	v_mfma_scale_f32_16x16x128_f8f6f4 v[158:161], v[18:25], v[164:171], v[158:161], v246, v247 op_sel_hi:[0,0,0]
	v_mfma_scale_f32_16x16x128_f8f6f4 v[154:157], v[26:33], v[164:171], v[154:157], v246, v247 op_sel_hi:[0,0,0]
	v_mfma_scale_f32_16x16x128_f8f6f4 v[142:145], v[18:25], v[172:179], v[142:145], v246, v247 op_sel_hi:[0,0,0]
	v_mfma_scale_f32_16x16x128_f8f6f4 v[138:141], v[26:33], v[172:179], v[138:141], v246, v247 op_sel_hi:[0,0,0]
	v_mfma_scale_f32_16x16x128_f8f6f4 v[126:129], v[18:25], v[180:187], v[126:129], v246, v247 op_sel_hi:[0,0,0]
	v_mfma_scale_f32_16x16x128_f8f6f4 v[122:125], v[26:33], v[180:187], v[122:125], v246, v247 op_sel_hi:[0,0,0]
	v_mfma_scale_f32_16x16x128_f8f6f4 v[110:113], v[18:25], v[188:195], v[110:113], v246, v247 op_sel_hi:[0,0,0]
	v_mfma_scale_f32_16x16x128_f8f6f4 v[106:109], v[26:33], v[188:195], v[106:109], v246, v247 op_sel_hi:[0,0,0]
	s_setprio 0
	s_setprio 1
	v_mfma_scale_f32_16x16x128_f8f6f4 v[150:153], v[2:9], v[164:171], v[150:153], v246, v247 op_sel_hi:[0,0,0]
	v_mfma_scale_f32_16x16x128_f8f6f4 v[146:149], v[10:17], v[164:171], v[146:149], v246, v247 op_sel_hi:[0,0,0]
	v_mfma_scale_f32_16x16x128_f8f6f4 v[134:137], v[2:9], v[172:179], v[134:137], v246, v247 op_sel_hi:[0,0,0]
	v_mfma_scale_f32_16x16x128_f8f6f4 v[130:133], v[10:17], v[172:179], v[130:133], v246, v247 op_sel_hi:[0,0,0]
	v_mfma_scale_f32_16x16x128_f8f6f4 v[118:121], v[2:9], v[180:187], v[118:121], v246, v247 op_sel_hi:[0,0,0]
	v_mfma_scale_f32_16x16x128_f8f6f4 v[114:117], v[10:17], v[180:187], v[114:117], v246, v247 op_sel_hi:[0,0,0]
	v_mfma_scale_f32_16x16x128_f8f6f4 v[102:105], v[2:9], v[188:195], v[102:105], v246, v247 op_sel_hi:[0,0,0]
	v_mfma_scale_f32_16x16x128_f8f6f4 v[98:101], v[10:17], v[188:195], v[98:101], v246, v247 op_sel_hi:[0,0,0]
	s_setprio 0
	s_barrier
	s_add_i32 s63, s63, s0
	v_lshl_add_u64 v[164:165], s[28:29], 0, v[0:1]
	s_mov_b32 m0, s63
	ds_read_b128 v[176:179], v196 offset:16384
	ds_read_b128 v[180:183], v196 offset:17408
	ds_read_b128 v[184:187], v196 offset:18432
	ds_read_b128 v[188:191], v196 offset:19456
	ds_read_b128 v[214:217], v196 offset:20480
	ds_read_b128 v[218:221], v196 offset:21504
	ds_read_b128 v[222:225], v196 offset:22528
	ds_read_b128 v[226:229], v196 offset:23552
	global_load_lds_dwordx4 v[164:165], off
	s_add_i32 m0, s63, 0x2000
	v_lshl_add_u64 v[166:167], s[28:29], 0, v[208:209]
	s_add_u32 s28, s28, s10
	s_addc_u32 s29, s29, s11
	s_add_i32 s63, s65, s0
	global_load_lds_dwordx4 v[166:167], off
	v_lshl_add_u64 v[168:169], s[28:29], 0, v[0:1]
	s_mov_b32 m0, s63
	v_lshl_add_u64 v[170:171], s[28:29], 0, v[208:209]
	global_load_lds_dwordx4 v[168:169], off
	s_add_i32 m0, s63, 0x2000
	v_lshl_add_u64 v[172:173], s[26:27], 0, v[204:205]
	global_load_lds_dwordx4 v[170:171], off
	s_mov_b32 m0, s1
	v_lshl_add_u64 v[174:175], s[26:27], 0, v[206:207]
	global_load_lds_dwordx4 v[172:173], off
	s_mov_b32 m0, s36
	s_nop 0
	global_load_lds_dwordx4 v[174:175], off
	s_waitcnt vmcnt(8)
	s_waitcnt lgkmcnt(0)
	s_barrier
	s_setprio 1
	s_waitcnt lgkmcnt(0)
	v_mfma_scale_f32_16x16x128_f8f6f4 v[94:97], v[18:25], v[176:183], v[94:97], v246, v247 op_sel_hi:[0,0,0]
	v_mfma_scale_f32_16x16x128_f8f6f4 v[90:93], v[26:33], v[176:183], v[90:93], v246, v247 op_sel_hi:[0,0,0]
	v_mfma_scale_f32_16x16x128_f8f6f4 v[78:81], v[18:25], v[184:191], v[78:81], v246, v247 op_sel_hi:[0,0,0]
	v_mfma_scale_f32_16x16x128_f8f6f4 v[74:77], v[26:33], v[184:191], v[74:77], v246, v247 op_sel_hi:[0,0,0]
	v_mfma_scale_f32_16x16x128_f8f6f4 v[62:65], v[18:25], v[214:221], v[62:65], v246, v247 op_sel_hi:[0,0,0]
	v_mfma_scale_f32_16x16x128_f8f6f4 v[58:61], v[26:33], v[214:221], v[58:61], v246, v247 op_sel_hi:[0,0,0]
	v_mfma_scale_f32_16x16x128_f8f6f4 v[46:49], v[18:25], v[222:229], v[46:49], v246, v247 op_sel_hi:[0,0,0]
	v_mfma_scale_f32_16x16x128_f8f6f4 v[42:45], v[26:33], v[222:229], v[42:45], v246, v247 op_sel_hi:[0,0,0]
	s_setprio 0
	s_setprio 1
	v_mfma_scale_f32_16x16x128_f8f6f4 v[86:89], v[2:9], v[176:183], v[86:89], v246, v247 op_sel_hi:[0,0,0]
	v_mfma_scale_f32_16x16x128_f8f6f4 v[82:85], v[10:17], v[176:183], v[82:85], v246, v247 op_sel_hi:[0,0,0]
	v_mfma_scale_f32_16x16x128_f8f6f4 v[70:73], v[2:9], v[184:191], v[70:73], v246, v247 op_sel_hi:[0,0,0]
	v_mfma_scale_f32_16x16x128_f8f6f4 v[66:69], v[10:17], v[184:191], v[66:69], v246, v247 op_sel_hi:[0,0,0]
	v_mfma_scale_f32_16x16x128_f8f6f4 v[54:57], v[2:9], v[214:221], v[54:57], v246, v247 op_sel_hi:[0,0,0]
	v_mfma_scale_f32_16x16x128_f8f6f4 v[50:53], v[10:17], v[214:221], v[50:53], v246, v247 op_sel_hi:[0,0,0]
	v_mfma_scale_f32_16x16x128_f8f6f4 v[38:41], v[2:9], v[222:229], v[38:41], v246, v247 op_sel_hi:[0,0,0]
	v_mfma_scale_f32_16x16x128_f8f6f4 v[34:37], v[10:17], v[222:229], v[34:37], v246, v247 op_sel_hi:[0,0,0]
	s_setprio 0
	s_barrier
; #define PG8_STAGE(bufoff, gbase, voff) do { _Pragma("unroll") for (int _i = 0; _i < 2; ++_i) \
;         __builtin_amdgcn_global_load_lds((const unsigned*)((const char*)(gbase) + (voff)[_i]), (PG8_LAS unsigned*)(lds + (bufoff) + ldsw + _i * 8192), 16, 0, 0); } while (0)
; #define PG8_WAIT_V(n) asm volatile("s_waitcnt vmcnt(" #n ")" ::: "memory")
; #define PG8_WAIT_L(n) asm volatile("s_waitcnt lgkmcnt(" #n ")" ::: "memory")
; #define PG8_BAR __builtin_amdgcn_s_barrier()
; #define PG8_SCHED __builtin_amdgcn_sched_barrier(0)
; template <class Epi, class Sched, bool ALIGN_EPI = false, bool SP2 = false, bool F8 = false>
; __device__ __forceinline__ void gemm_phase(PG8_LAS unsigned char* lds, const Gemm g, const Sched& S, const Epi& E, const int tidb  ) {
;     ...
;             PG8_LDB(B0, 1, 0); PG8_LDB(B1, 1, 1); PG8_SCHED; PG8_LDA(At, 1, 0); PG8_STAGE(PG8_SA(0, 1), a2 + hstep, voffA);
;             PG8_WAIT_V(8); PG8_WAIT_L(0); PG8_BAR; PG8_MMA(0, 0, At, B0); PG8_MMA(0, 1, At, B1); PG8_BAR; PG8_SCHED;
;             PG8_LDA(At, 1, 1); PG8_STAGE(PG8_SB(1, 0), b3, voffB); PG8_STAGE(PG8_SB(1, 1), b3 + hstep, voffB); PG8_STAGE(PG8_SA(1, 0), a3, voffA);
;             PG8_WAIT_V(8); PG8_WAIT_L(0); PG8_BAR; PG8_MMA(1, 0, At, B0); PG8_MMA(1, 1, At, B1); PG8_BAR; PG8_SCHED;
	s_add_i32 s28, 0, 0x18000
	s_add_i32 s29, 0, 0x1c000
	v_add_u32_e32 v14, s28, v200
	v_add_u32_e32 v30, s29, v200
	ds_read_b128 v[2:5], v14
	ds_read_b128 v[6:9], v14 offset:1024
	ds_read_b128 v[10:13], v14 offset:2048
	ds_read_b128 v[14:17], v14 offset:3072
	ds_read_b128 v[18:21], v30
	ds_read_b128 v[22:25], v30 offset:1024
	ds_read_b128 v[26:29], v30 offset:2048
	ds_read_b128 v[30:33], v30 offset:3072
	s_add_u32 s26, s26, s10
	s_addc_u32 s27, s27, s11
	s_mov_b32 m0, s37
	v_lshl_add_u64 v[192:193], s[26:27], 0, v[204:205]
	ds_read_b128 v[176:179], v196 offset:32768
	ds_read_b128 v[180:183], v196 offset:33792
	ds_read_b128 v[184:187], v196 offset:34816
	ds_read_b128 v[188:191], v196 offset:35840
	ds_read_b128 v[214:217], v196 offset:36864
	ds_read_b128 v[218:221], v196 offset:37888
	ds_read_b128 v[222:225], v196 offset:38912
	ds_read_b128 v[226:229], v196 offset:39936
	global_load_lds_dwordx4 v[192:193], off
	v_lshl_add_u64 v[192:193], s[26:27], 0, v[206:207]
	s_mov_b32 m0, s41
	s_nop 0
	global_load_lds_dwordx4 v[192:193], off
	s_waitcnt vmcnt(8)
	s_waitcnt lgkmcnt(0)
	s_barrier
	s_setprio 1
	s_waitcnt lgkmcnt(0)
	v_mfma_scale_f32_16x16x128_f8f6f4 v[158:161], v[2:9], v[176:183], v[158:161], v246, v247 op_sel_hi:[0,0,0]
	v_mfma_scale_f32_16x16x128_f8f6f4 v[154:157], v[10:17], v[176:183], v[154:157], v246, v247 op_sel_hi:[0,0,0]
	v_mfma_scale_f32_16x16x128_f8f6f4 v[142:145], v[2:9], v[184:191], v[142:145], v246, v247 op_sel_hi:[0,0,0]
	v_mfma_scale_f32_16x16x128_f8f6f4 v[138:141], v[10:17], v[184:191], v[138:141], v246, v247 op_sel_hi:[0,0,0]
	v_mfma_scale_f32_16x16x128_f8f6f4 v[126:129], v[2:9], v[214:221], v[126:129], v246, v247 op_sel_hi:[0,0,0]
	v_mfma_scale_f32_16x16x128_f8f6f4 v[122:125], v[10:17], v[214:221], v[122:125], v246, v247 op_sel_hi:[0,0,0]
	v_mfma_scale_f32_16x16x128_f8f6f4 v[110:113], v[2:9], v[222:229], v[110:113], v246, v247 op_sel_hi:[0,0,0]
	v_mfma_scale_f32_16x16x128_f8f6f4 v[106:109], v[10:17], v[222:229], v[106:109], v246, v247 op_sel_hi:[0,0,0]
	s_setprio 0
	s_setprio 1
	v_mfma_scale_f32_16x16x128_f8f6f4 v[150:153], v[18:25], v[176:183], v[150:153], v246, v247 op_sel_hi:[0,0,0]
	v_mfma_scale_f32_16x16x128_f8f6f4 v[146:149], v[26:33], v[176:183], v[146:149], v246, v247 op_sel_hi:[0,0,0]
	v_mfma_scale_f32_16x16x128_f8f6f4 v[134:137], v[18:25], v[184:191], v[134:137], v246, v247 op_sel_hi:[0,0,0]
	v_mfma_scale_f32_16x16x128_f8f6f4 v[130:133], v[26:33], v[184:191], v[130:133], v246, v247 op_sel_hi:[0,0,0]
	v_mfma_scale_f32_16x16x128_f8f6f4 v[118:121], v[18:25], v[214:221], v[118:121], v246, v247 op_sel_hi:[0,0,0]
	v_mfma_scale_f32_16x16x128_f8f6f4 v[114:117], v[26:33], v[214:221], v[114:117], v246, v247 op_sel_hi:[0,0,0]
	v_mfma_scale_f32_16x16x128_f8f6f4 v[102:105], v[18:25], v[222:229], v[102:105], v246, v247 op_sel_hi:[0,0,0]
	v_mfma_scale_f32_16x16x128_f8f6f4 v[98:101], v[26:33], v[222:229], v[98:101], v246, v247 op_sel_hi:[0,0,0]
	s_setprio 0
	s_barrier
	s_add_i32 s26, s28, s0
	v_lshl_add_u64 v[164:165], v[164:165], 0, s[92:93]
	s_mov_b32 m0, s26
	ds_read_b128 v[176:179], v196 offset:49152
	ds_read_b128 v[180:183], v196 offset:50176
	ds_read_b128 v[184:187], v196 offset:51200
	ds_read_b128 v[188:191], v196 offset:52224
	ds_read_b128 v[214:217], v196 offset:53248
	ds_read_b128 v[218:221], v196 offset:54272
	ds_read_b128 v[222:225], v196 offset:55296
	ds_read_b128 v[226:229], v196 offset:56320
	global_load_lds_dwordx4 v[164:165], off
	v_lshl_add_u64 v[164:165], v[166:167], 0, s[92:93]
	s_add_i32 m0, s26, 0x2000
	s_add_i32 s26, s29, s0
	global_load_lds_dwordx4 v[164:165], off
	v_lshl_add_u64 v[164:165], v[168:169], 0, s[92:93]
	s_mov_b32 m0, s26
	s_nop 0
	global_load_lds_dwordx4 v[164:165], off
	v_lshl_add_u64 v[164:165], v[170:171], 0, s[92:93]
	s_add_i32 m0, s26, 0x2000
	s_nop 0
	global_load_lds_dwordx4 v[164:165], off
	v_lshl_add_u64 v[164:165], v[172:173], 0, s[92:93]
	s_mov_b32 m0, s43
	s_nop 0
	global_load_lds_dwordx4 v[164:165], off
	v_lshl_add_u64 v[164:165], v[174:175], 0, s[92:93]
	s_mov_b32 m0, s45
	s_nop 0
	global_load_lds_dwordx4 v[164:165], off
	s_waitcnt vmcnt(8)
	s_waitcnt lgkmcnt(0)
	s_barrier
	s_setprio 1
	s_waitcnt lgkmcnt(0)
	v_mfma_scale_f32_16x16x128_f8f6f4 v[94:97], v[2:9], v[176:183], v[94:97], v246, v247 op_sel_hi:[0,0,0]
	v_mfma_scale_f32_16x16x128_f8f6f4 v[90:93], v[10:17], v[176:183], v[90:93], v246, v247 op_sel_hi:[0,0,0]
	v_mfma_scale_f32_16x16x128_f8f6f4 v[78:81], v[2:9], v[184:191], v[78:81], v246, v247 op_sel_hi:[0,0,0]
	v_mfma_scale_f32_16x16x128_f8f6f4 v[74:77], v[10:17], v[184:191], v[74:77], v246, v247 op_sel_hi:[0,0,0]
	v_mfma_scale_f32_16x16x128_f8f6f4 v[62:65], v[2:9], v[214:221], v[62:65], v246, v247 op_sel_hi:[0,0,0]
	v_mfma_scale_f32_16x16x128_f8f6f4 v[58:61], v[10:17], v[214:221], v[58:61], v246, v247 op_sel_hi:[0,0,0]
	v_mfma_scale_f32_16x16x128_f8f6f4 v[46:49], v[2:9], v[222:229], v[46:49], v246, v247 op_sel_hi:[0,0,0]
	v_mfma_scale_f32_16x16x128_f8f6f4 v[42:45], v[10:17], v[222:229], v[42:45], v246, v247 op_sel_hi:[0,0,0]
	s_setprio 0
	s_setprio 1
	v_mfma_scale_f32_16x16x128_f8f6f4 v[86:89], v[18:25], v[176:183], v[86:89], v246, v247 op_sel_hi:[0,0,0]
	v_mfma_scale_f32_16x16x128_f8f6f4 v[82:85], v[26:33], v[176:183], v[82:85], v246, v247 op_sel_hi:[0,0,0]
	v_mfma_scale_f32_16x16x128_f8f6f4 v[70:73], v[18:25], v[184:191], v[70:73], v246, v247 op_sel_hi:[0,0,0]
	v_mfma_scale_f32_16x16x128_f8f6f4 v[66:69], v[26:33], v[184:191], v[66:69], v246, v247 op_sel_hi:[0,0,0]
	v_mfma_scale_f32_16x16x128_f8f6f4 v[54:57], v[18:25], v[214:221], v[54:57], v246, v247 op_sel_hi:[0,0,0]
	v_mfma_scale_f32_16x16x128_f8f6f4 v[50:53], v[26:33], v[214:221], v[50:53], v246, v247 op_sel_hi:[0,0,0]
	v_mfma_scale_f32_16x16x128_f8f6f4 v[38:41], v[18:25], v[222:229], v[38:41], v246, v247 op_sel_hi:[0,0,0]
	v_mfma_scale_f32_16x16x128_f8f6f4 v[34:37], v[26:33], v[222:229], v[34:37], v246, v247 op_sel_hi:[0,0,0]
	s_setprio 0
	s_add_u32 s24, s24, 0x100
	s_addc_u32 s25, s25, 0
	s_add_u32 s60, s60, 0x100
	s_addc_u32 s61, s61, 0
	s_cmp_ge_i32 s62, s46
	s_mov_b32 s26, s62
	s_barrier
	s_cbranch_scc0 .LBB0_993

;     __device__ __forceinline__ bool next(int i, Unit& u) const { return so.next(i, u); }
; #define PG8_STAGE(bufoff, gbase, voff) do { _Pragma("unroll") for (int _i = 0; _i < 2; ++_i) \
;         __builtin_amdgcn_global_load_lds((const unsigned*)((const char*)(gbase) + (voff)[_i]), (PG8_LAS unsigned*)(lds + (bufoff) + ldsw + _i * 8192), 16, 0, 0); } while (0)
; #define PG8_WAIT_V(n) asm volatile("s_waitcnt vmcnt(" #n ")" ::: "memory")
; #define PG8_WAIT_L(n) asm volatile("s_waitcnt lgkmcnt(" #n ")" ::: "memory")
; #define PG8_BAR __builtin_amdgcn_s_barrier()
; #define PG8_SCHED __builtin_amdgcn_sched_barrier(0)
; template <class Epi, class Sched, bool ALIGN_EPI = false, bool SP2 = false, bool F8 = false>
; __device__ __forceinline__ void gemm_phase(PG8_LAS unsigned char* lds, const Gemm g, const Sched& S, const Epi& E, const int tidb  ) {
;     ...
;         const bool has_next = S.next(ui + 1, nxt);
;         const char* nA = has_next ? (const char*)g.A + (size_t)nxt.pm * tstep : cA; const char* nB = has_next ? (const char*)g.Bt + S.boff(nxt) + (size_t)nxt.pn * tstep : cB;
;         for (int t = 0; t < nt; t += 2) {
;             const bool last = (t == nt - 2);
;             if constexpr (Epi::PREFETCH) { if (t == 0) E.prefetch(cur, wid, lane); }
;             const char* a1 = cA + (size_t)(t + 1) * kstep;
;             const char* a2 = last ? nA : cA + (size_t)(t + 2) * kstep; const char* b2 = last ? nB : cB + (size_t)(t + 2) * kstep;
;             const char* a3 = a2 + kstep; const char* b3 = b2 + kstep;
;             if (last && has_next) S.a_ready(nxt);
;             if constexpr (SP2) {
;             PG8_LDB(B0, 0, 0); PG8_LDB(B1, 0, 1); PG8_SCHED; PG8_LDA(At, 0, 0); PG8_STAGE(PG8_SA(1, 1), a1 + hstep, voffA);
;             PG8_WAIT_V(8); PG8_WAIT_L(0); PG8_BAR; PG8_MMA(0, 0, At, B0); PG8_MMA(0, 1, At, B1); PG8_BAR; PG8_SCHED;
;             PG8_LDA(At, 0, 1); PG8_STAGE(PG8_SB(0, 0), b2, voffB); PG8_STAGE(PG8_SB(0, 1), b2 + hstep, voffB); PG8_STAGE(PG8_SA(0, 0), a2, voffA);
;             PG8_WAIT_V(8); PG8_WAIT_L(0); PG8_BAR; PG8_MMA(1, 0, At, B0); PG8_MMA(1, 1, At, B1); PG8_BAR; PG8_SCHED;
.LBB0_1042:
	s_add_i32 s62, s26, 2
	s_add_u32 s28, s24, 0x80
	s_addc_u32 s27, s25, 0
	s_add_i32 s63, 0, 0x10000
	s_cmp_eq_u32 s47, s26
	s_cselect_b32 s27, s7, s27
	s_cselect_b32 s26, s6, s28
	s_cselect_b32 s29, s9, s61
	s_cselect_b32 s28, s8, s60
	s_add_i32 s65, 0, 0x14000
	v_add_u32_e32 v2, s63, v192
	v_add_u32_e32 v14, s65, v192
	ds_read_b128 v[18:21], v2
	ds_read_b128 v[22:25], v2 offset:1024
	ds_read_b128 v[26:29], v2 offset:2048
	ds_read_b128 v[30:33], v2 offset:3072
	ds_read_b128 v[2:5], v14
	ds_read_b128 v[6:9], v14 offset:1024
	ds_read_b128 v[10:13], v14 offset:2048
	ds_read_b128 v[14:17], v14 offset:3072
	v_lshl_add_u64 v[190:191], s[24:25], 0, v[170:171]
	s_add_i32 m0, s1, 0xc000
	ds_read_b128 v[174:177], v194
	ds_read_b128 v[178:181], v194 offset:1024
	ds_read_b128 v[182:185], v194 offset:2048
	ds_read_b128 v[186:189], v194 offset:3072
	ds_read_b128 v[204:207], v194 offset:4096
	ds_read_b128 v[208:211], v194 offset:5120
	ds_read_b128 v[212:215], v194 offset:6144
	ds_read_b128 v[216:219], v194 offset:7168
	global_load_lds_dwordx4 v[190:191], off
	v_lshl_add_u64 v[190:191], s[24:25], 0, v[172:173]
	s_add_i32 m0, s1, 0xe000
	s_nop 0
	global_load_lds_dwordx4 v[190:191], off
	s_waitcnt vmcnt(8)
	s_waitcnt lgkmcnt(0)
	s_barrier
	s_setprio 1
	s_waitcnt lgkmcnt(0)
	v_mfma_scale_f32_16x16x128_f8f6f4 v[158:161], v[18:25], v[174:181], v[158:161], v246, v247 op_sel_hi:[0,0,0]
	v_mfma_scale_f32_16x16x128_f8f6f4 v[154:157], v[26:33], v[174:181], v[154:157], v246, v247 op_sel_hi:[0,0,0]
	v_mfma_scale_f32_16x16x128_f8f6f4 v[142:145], v[18:25], v[182:189], v[142:145], v246, v247 op_sel_hi:[0,0,0]
	v_mfma_scale_f32_16x16x128_f8f6f4 v[138:141], v[26:33], v[182:189], v[138:141], v246, v247 op_sel_hi:[0,0,0]
	v_mfma_scale_f32_16x16x128_f8f6f4 v[126:129], v[18:25], v[204:211], v[126:129], v246, v247 op_sel_hi:[0,0,0]
	v_mfma_scale_f32_16x16x128_f8f6f4 v[122:125], v[26:33], v[204:211], v[122:125], v246, v247 op_sel_hi:[0,0,0]
	v_mfma_scale_f32_16x16x128_f8f6f4 v[110:113], v[18:25], v[212:219], v[110:113], v246, v247 op_sel_hi:[0,0,0]
	v_mfma_scale_f32_16x16x128_f8f6f4 v[106:109], v[26:33], v[212:219], v[106:109], v246, v247 op_sel_hi:[0,0,0]
	s_setprio 0
	s_setprio 1
	v_mfma_scale_f32_16x16x128_f8f6f4 v[150:153], v[2:9], v[174:181], v[150:153], v246, v247 op_sel_hi:[0,0,0]
	v_mfma_scale_f32_16x16x128_f8f6f4 v[146:149], v[10:17], v[174:181], v[146:149], v246, v247 op_sel_hi:[0,0,0]
	v_mfma_scale_f32_16x16x128_f8f6f4 v[134:137], v[2:9], v[182:189], v[134:137], v246, v247 op_sel_hi:[0,0,0]
	v_mfma_scale_f32_16x16x128_f8f6f4 v[130:133], v[10:17], v[182:189], v[130:133], v246, v247 op_sel_hi:[0,0,0]
	v_mfma_scale_f32_16x16x128_f8f6f4 v[118:121], v[2:9], v[204:211], v[118:121], v246, v247 op_sel_hi:[0,0,0]
	v_mfma_scale_f32_16x16x128_f8f6f4 v[114:117], v[10:17], v[204:211], v[114:117], v246, v247 op_sel_hi:[0,0,0]
	v_mfma_scale_f32_16x16x128_f8f6f4 v[102:105], v[2:9], v[212:219], v[102:105], v246, v247 op_sel_hi:[0,0,0]
	v_mfma_scale_f32_16x16x128_f8f6f4 v[98:101], v[10:17], v[212:219], v[98:101], v246, v247 op_sel_hi:[0,0,0]
	s_setprio 0
	s_barrier
	s_add_i32 s63, s63, s0
	v_lshl_add_u64 v[174:175], s[28:29], 0, v[0:1]
	s_mov_b32 m0, s63
	ds_read_b128 v[204:207], v194 offset:16384
	ds_read_b128 v[208:211], v194 offset:17408
	ds_read_b128 v[212:215], v194 offset:18432
	ds_read_b128 v[216:219], v194 offset:19456
	ds_read_b128 v[220:223], v194 offset:20480
	ds_read_b128 v[224:227], v194 offset:21504
	ds_read_b128 v[228:231], v194 offset:22528
	ds_read_b128 v[232:235], v194 offset:23552
	global_load_lds_dwordx4 v[174:175], off
	s_add_i32 m0, s63, 0x2000
	v_lshl_add_u64 v[176:177], s[28:29], 0, v[168:169]
	s_add_u32 s28, s28, s10
	s_addc_u32 s29, s29, s11
	s_add_i32 s63, s65, s0
	global_load_lds_dwordx4 v[176:177], off
	v_lshl_add_u64 v[178:179], s[28:29], 0, v[0:1]
	s_mov_b32 m0, s63
	v_lshl_add_u64 v[180:181], s[28:29], 0, v[168:169]
	global_load_lds_dwordx4 v[178:179], off
	s_add_i32 m0, s63, 0x2000
	v_lshl_add_u64 v[182:183], s[26:27], 0, v[164:165]
	global_load_lds_dwordx4 v[180:181], off
	s_mov_b32 m0, s1
	v_lshl_add_u64 v[184:185], s[26:27], 0, v[166:167]
	global_load_lds_dwordx4 v[182:183], off
	s_mov_b32 m0, s36
	s_nop 0
	global_load_lds_dwordx4 v[184:185], off
	s_waitcnt vmcnt(8)
	s_waitcnt lgkmcnt(0)
	s_barrier
	s_setprio 1
	s_waitcnt lgkmcnt(0)
	v_mfma_scale_f32_16x16x128_f8f6f4 v[94:97], v[18:25], v[204:211], v[94:97], v246, v247 op_sel_hi:[0,0,0]
	v_mfma_scale_f32_16x16x128_f8f6f4 v[90:93], v[26:33], v[204:211], v[90:93], v246, v247 op_sel_hi:[0,0,0]
	v_mfma_scale_f32_16x16x128_f8f6f4 v[78:81], v[18:25], v[212:219], v[78:81], v246, v247 op_sel_hi:[0,0,0]
	v_mfma_scale_f32_16x16x128_f8f6f4 v[74:77], v[26:33], v[212:219], v[74:77], v246, v247 op_sel_hi:[0,0,0]
	v_mfma_scale_f32_16x16x128_f8f6f4 v[62:65], v[18:25], v[220:227], v[62:65], v246, v247 op_sel_hi:[0,0,0]
	v_mfma_scale_f32_16x16x128_f8f6f4 v[58:61], v[26:33], v[220:227], v[58:61], v246, v247 op_sel_hi:[0,0,0]
	v_mfma_scale_f32_16x16x128_f8f6f4 v[46:49], v[18:25], v[228:235], v[46:49], v246, v247 op_sel_hi:[0,0,0]
	v_mfma_scale_f32_16x16x128_f8f6f4 v[42:45], v[26:33], v[228:235], v[42:45], v246, v247 op_sel_hi:[0,0,0]
	s_setprio 0
	s_setprio 1
	v_mfma_scale_f32_16x16x128_f8f6f4 v[86:89], v[2:9], v[204:211], v[86:89], v246, v247 op_sel_hi:[0,0,0]
	v_mfma_scale_f32_16x16x128_f8f6f4 v[82:85], v[10:17], v[204:211], v[82:85], v246, v247 op_sel_hi:[0,0,0]
	v_mfma_scale_f32_16x16x128_f8f6f4 v[70:73], v[2:9], v[212:219], v[70:73], v246, v247 op_sel_hi:[0,0,0]
	v_mfma_scale_f32_16x16x128_f8f6f4 v[66:69], v[10:17], v[212:219], v[66:69], v246, v247 op_sel_hi:[0,0,0]
	v_mfma_scale_f32_16x16x128_f8f6f4 v[54:57], v[2:9], v[220:227], v[54:57], v246, v247 op_sel_hi:[0,0,0]
	v_mfma_scale_f32_16x16x128_f8f6f4 v[50:53], v[10:17], v[220:227], v[50:53], v246, v247 op_sel_hi:[0,0,0]
	v_mfma_scale_f32_16x16x128_f8f6f4 v[38:41], v[2:9], v[228:235], v[38:41], v246, v247 op_sel_hi:[0,0,0]
	v_mfma_scale_f32_16x16x128_f8f6f4 v[34:37], v[10:17], v[228:235], v[34:37], v246, v247 op_sel_hi:[0,0,0]
	s_setprio 0
	s_barrier
; #define PG8_STAGE(bufoff, gbase, voff) do { _Pragma("unroll") for (int _i = 0; _i < 2; ++_i) \
;         __builtin_amdgcn_global_load_lds((const unsigned*)((const char*)(gbase) + (voff)[_i]), (PG8_LAS unsigned*)(lds + (bufoff) + ldsw + _i * 8192), 16, 0, 0); } while (0)
; #define PG8_WAIT_V(n) asm volatile("s_waitcnt vmcnt(" #n ")" ::: "memory")
; #define PG8_WAIT_L(n) asm volatile("s_waitcnt lgkmcnt(" #n ")" ::: "memory")
; #define PG8_BAR __builtin_amdgcn_s_barrier()
; #define PG8_SCHED __builtin_amdgcn_sched_barrier(0)
; template <class Epi, class Sched, bool ALIGN_EPI = false, bool SP2 = false, bool F8 = false>
; __device__ __forceinline__ void gemm_phase(PG8_LAS unsigned char* lds, const Gemm g, const Sched& S, const Epi& E, const int tidb  ) {
;     ...
;             PG8_LDB(B0, 1, 0); PG8_LDB(B1, 1, 1); PG8_SCHED; PG8_LDA(At, 1, 0); PG8_STAGE(PG8_SA(0, 1), a2 + hstep, voffA);
;             PG8_WAIT_V(8); PG8_WAIT_L(0); PG8_BAR; PG8_MMA(0, 0, At, B0); PG8_MMA(0, 1, At, B1); PG8_BAR; PG8_SCHED;
;             PG8_LDA(At, 1, 1); PG8_STAGE(PG8_SB(1, 0), b3, voffB); PG8_STAGE(PG8_SB(1, 1), b3 + hstep, voffB); PG8_STAGE(PG8_SA(1, 0), a3, voffA);
;             PG8_WAIT_V(8); PG8_WAIT_L(0); PG8_BAR; PG8_MMA(1, 0, At, B0); PG8_MMA(1, 1, At, B1); PG8_BAR; PG8_SCHED;
	s_add_i32 s28, 0, 0x18000
	s_add_i32 s29, 0, 0x1c000
	v_add_u32_e32 v14, s28, v192
	v_add_u32_e32 v30, s29, v192
	ds_read_b128 v[2:5], v14
	ds_read_b128 v[6:9], v14 offset:1024
	ds_read_b128 v[10:13], v14 offset:2048
	ds_read_b128 v[14:17], v14 offset:3072
	ds_read_b128 v[18:21], v30
	ds_read_b128 v[22:25], v30 offset:1024
	ds_read_b128 v[26:29], v30 offset:2048
	ds_read_b128 v[30:33], v30 offset:3072
	s_add_u32 s26, s26, s10
	s_addc_u32 s27, s27, s11
	s_mov_b32 m0, s37
	v_lshl_add_u64 v[186:187], s[26:27], 0, v[164:165]
	ds_read_b128 v[204:207], v194 offset:32768
	ds_read_b128 v[208:211], v194 offset:33792
	ds_read_b128 v[212:215], v194 offset:34816
	ds_read_b128 v[216:219], v194 offset:35840
	ds_read_b128 v[220:223], v194 offset:36864
	ds_read_b128 v[224:227], v194 offset:37888
	ds_read_b128 v[228:231], v194 offset:38912
	ds_read_b128 v[232:235], v194 offset:39936
	global_load_lds_dwordx4 v[186:187], off
	v_lshl_add_u64 v[186:187], s[26:27], 0, v[166:167]
	s_mov_b32 m0, s41
	s_nop 0
	global_load_lds_dwordx4 v[186:187], off
	s_waitcnt vmcnt(8)
	s_waitcnt lgkmcnt(0)
	s_barrier
	s_setprio 1
	s_waitcnt lgkmcnt(0)
	v_mfma_scale_f32_16x16x128_f8f6f4 v[158:161], v[2:9], v[204:211], v[158:161], v246, v247 op_sel_hi:[0,0,0]
	v_mfma_scale_f32_16x16x128_f8f6f4 v[154:157], v[10:17], v[204:211], v[154:157], v246, v247 op_sel_hi:[0,0,0]
	v_mfma_scale_f32_16x16x128_f8f6f4 v[142:145], v[2:9], v[212:219], v[142:145], v246, v247 op_sel_hi:[0,0,0]
	v_mfma_scale_f32_16x16x128_f8f6f4 v[138:141], v[10:17], v[212:219], v[138:141], v246, v247 op_sel_hi:[0,0,0]
	v_mfma_scale_f32_16x16x128_f8f6f4 v[126:129], v[2:9], v[220:227], v[126:129], v246, v247 op_sel_hi:[0,0,0]
	v_mfma_scale_f32_16x16x128_f8f6f4 v[122:125], v[10:17], v[220:227], v[122:125], v246, v247 op_sel_hi:[0,0,0]
	v_mfma_scale_f32_16x16x128_f8f6f4 v[110:113], v[2:9], v[228:235], v[110:113], v246, v247 op_sel_hi:[0,0,0]
	v_mfma_scale_f32_16x16x128_f8f6f4 v[106:109], v[10:17], v[228:235], v[106:109], v246, v247 op_sel_hi:[0,0,0]
	s_setprio 0
	s_setprio 1
	v_mfma_scale_f32_16x16x128_f8f6f4 v[150:153], v[18:25], v[204:211], v[150:153], v246, v247 op_sel_hi:[0,0,0]
	v_mfma_scale_f32_16x16x128_f8f6f4 v[146:149], v[26:33], v[204:211], v[146:149], v246, v247 op_sel_hi:[0,0,0]
	v_mfma_scale_f32_16x16x128_f8f6f4 v[134:137], v[18:25], v[212:219], v[134:137], v246, v247 op_sel_hi:[0,0,0]
	v_mfma_scale_f32_16x16x128_f8f6f4 v[130:133], v[26:33], v[212:219], v[130:133], v246, v247 op_sel_hi:[0,0,0]
	v_mfma_scale_f32_16x16x128_f8f6f4 v[118:121], v[18:25], v[220:227], v[118:121], v246, v247 op_sel_hi:[0,0,0]
	v_mfma_scale_f32_16x16x128_f8f6f4 v[114:117], v[26:33], v[220:227], v[114:117], v246, v247 op_sel_hi:[0,0,0]
	v_mfma_scale_f32_16x16x128_f8f6f4 v[102:105], v[18:25], v[228:235], v[102:105], v246, v247 op_sel_hi:[0,0,0]
	v_mfma_scale_f32_16x16x128_f8f6f4 v[98:101], v[26:33], v[228:235], v[98:101], v246, v247 op_sel_hi:[0,0,0]
	s_setprio 0
	s_barrier
	s_add_i32 s26, s28, s0
	v_lshl_add_u64 v[174:175], v[174:175], 0, s[92:93]
	s_mov_b32 m0, s26
	ds_read_b128 v[204:207], v194 offset:49152
	ds_read_b128 v[208:211], v194 offset:50176
	ds_read_b128 v[212:215], v194 offset:51200
	ds_read_b128 v[216:219], v194 offset:52224
	ds_read_b128 v[220:223], v194 offset:53248
	ds_read_b128 v[224:227], v194 offset:54272
	ds_read_b128 v[228:231], v194 offset:55296
	ds_read_b128 v[232:235], v194 offset:56320
	global_load_lds_dwordx4 v[174:175], off
	v_lshl_add_u64 v[174:175], v[176:177], 0, s[92:93]
	s_add_i32 m0, s26, 0x2000
	s_add_i32 s26, s29, s0
	global_load_lds_dwordx4 v[174:175], off
	v_lshl_add_u64 v[174:175], v[178:179], 0, s[92:93]
	s_mov_b32 m0, s26
	s_nop 0
	global_load_lds_dwordx4 v[174:175], off
	v_lshl_add_u64 v[174:175], v[180:181], 0, s[92:93]
	s_add_i32 m0, s26, 0x2000
	s_nop 0
	global_load_lds_dwordx4 v[174:175], off
	v_lshl_add_u64 v[174:175], v[182:183], 0, s[92:93]
	s_mov_b32 m0, s43
	s_nop 0
	global_load_lds_dwordx4 v[174:175], off
	v_lshl_add_u64 v[174:175], v[184:185], 0, s[92:93]
	s_mov_b32 m0, s45
	s_nop 0
	global_load_lds_dwordx4 v[174:175], off
	s_waitcnt vmcnt(8)
	s_waitcnt lgkmcnt(0)
	s_barrier
	s_setprio 1
	s_waitcnt lgkmcnt(0)
	v_mfma_scale_f32_16x16x128_f8f6f4 v[94:97], v[2:9], v[204:211], v[94:97], v246, v247 op_sel_hi:[0,0,0]
	v_mfma_scale_f32_16x16x128_f8f6f4 v[90:93], v[10:17], v[204:211], v[90:93], v246, v247 op_sel_hi:[0,0,0]
	v_mfma_scale_f32_16x16x128_f8f6f4 v[78:81], v[2:9], v[212:219], v[78:81], v246, v247 op_sel_hi:[0,0,0]
	v_mfma_scale_f32_16x16x128_f8f6f4 v[74:77], v[10:17], v[212:219], v[74:77], v246, v247 op_sel_hi:[0,0,0]
	v_mfma_scale_f32_16x16x128_f8f6f4 v[62:65], v[2:9], v[220:227], v[62:65], v246, v247 op_sel_hi:[0,0,0]
	v_mfma_scale_f32_16x16x128_f8f6f4 v[58:61], v[10:17], v[220:227], v[58:61], v246, v247 op_sel_hi:[0,0,0]
	v_mfma_scale_f32_16x16x128_f8f6f4 v[46:49], v[2:9], v[228:235], v[46:49], v246, v247 op_sel_hi:[0,0,0]
	v_mfma_scale_f32_16x16x128_f8f6f4 v[42:45], v[10:17], v[228:235], v[42:45], v246, v247 op_sel_hi:[0,0,0]
	s_setprio 0
	s_setprio 1
	v_mfma_scale_f32_16x16x128_f8f6f4 v[86:89], v[18:25], v[204:211], v[86:89], v246, v247 op_sel_hi:[0,0,0]
	v_mfma_scale_f32_16x16x128_f8f6f4 v[82:85], v[26:33], v[204:211], v[82:85], v246, v247 op_sel_hi:[0,0,0]
	v_mfma_scale_f32_16x16x128_f8f6f4 v[70:73], v[18:25], v[212:219], v[70:73], v246, v247 op_sel_hi:[0,0,0]
	v_mfma_scale_f32_16x16x128_f8f6f4 v[66:69], v[26:33], v[212:219], v[66:69], v246, v247 op_sel_hi:[0,0,0]
	v_mfma_scale_f32_16x16x128_f8f6f4 v[54:57], v[18:25], v[220:227], v[54:57], v246, v247 op_sel_hi:[0,0,0]
	v_mfma_scale_f32_16x16x128_f8f6f4 v[50:53], v[26:33], v[220:227], v[50:53], v246, v247 op_sel_hi:[0,0,0]
	v_mfma_scale_f32_16x16x128_f8f6f4 v[38:41], v[18:25], v[228:235], v[38:41], v246, v247 op_sel_hi:[0,0,0]
	v_mfma_scale_f32_16x16x128_f8f6f4 v[34:37], v[26:33], v[228:235], v[34:37], v246, v247 op_sel_hi:[0,0,0]
	s_setprio 0
	s_add_u32 s24, s24, 0x100
	s_addc_u32 s25, s25, 0
	s_add_u32 s60, s60, 0x100
	s_addc_u32 s61, s61, 0
	s_cmp_ge_i32 s62, s46
	s_mov_b32 s26, s62
	s_barrier
	s_cbranch_scc0 .LBB0_1042

;     __device__ __forceinline__ bool next(int i, Unit& u) const { return so.next(i, u); }
; #define PG8_STAGE(bufoff, gbase, voff) do { _Pragma("unroll") for (int _i = 0; _i < 2; ++_i) \
;         __builtin_amdgcn_global_load_lds((const unsigned*)((const char*)(gbase) + (voff)[_i]), (PG8_LAS unsigned*)(lds + (bufoff) + ldsw + _i * 8192), 16, 0, 0); } while (0)
; #define PG8_WAIT_V(n) asm volatile("s_waitcnt vmcnt(" #n ")" ::: "memory")
; #define PG8_WAIT_L(n) asm volatile("s_waitcnt lgkmcnt(" #n ")" ::: "memory")
; #define PG8_BAR __builtin_amdgcn_s_barrier()
; #define PG8_SCHED __builtin_amdgcn_sched_barrier(0)
; template <class Epi, class Sched, bool ALIGN_EPI = false, bool SP2 = false, bool F8 = false>
; __device__ __forceinline__ void gemm_phase(PG8_LAS unsigned char* lds, const Gemm g, const Sched& S, const Epi& E, const int tidb  ) {
;     ...
;         const bool has_next = S.next(ui + 1, nxt);
;         const char* nA = has_next ? (const char*)g.A + (size_t)nxt.pm * tstep : cA; const char* nB = has_next ? (const char*)g.Bt + S.boff(nxt) + (size_t)nxt.pn * tstep : cB;
;         for (int t = 0; t < nt; t += 2) {
;             const bool last = (t == nt - 2);
;             if constexpr (Epi::PREFETCH) { if (t == 0) E.prefetch(cur, wid, lane); }
;             const char* a1 = cA + (size_t)(t + 1) * kstep;
;             const char* a2 = last ? nA : cA + (size_t)(t + 2) * kstep; const char* b2 = last ? nB : cB + (size_t)(t + 2) * kstep;
;             const char* a3 = a2 + kstep; const char* b3 = b2 + kstep;
;             if (last && has_next) S.a_ready(nxt);
;             if constexpr (SP2) {
;             PG8_LDB(B0, 0, 0); PG8_LDB(B1, 0, 1); PG8_SCHED; PG8_LDA(At, 0, 0); PG8_STAGE(PG8_SA(1, 1), a1 + hstep, voffA);
;             PG8_WAIT_V(8); PG8_WAIT_L(0); PG8_BAR; PG8_MMA(0, 0, At, B0); PG8_MMA(0, 1, At, B1); PG8_BAR; PG8_SCHED;
;             PG8_LDA(At, 0, 1); PG8_STAGE(PG8_SB(0, 0), b2, voffB); PG8_STAGE(PG8_SB(0, 1), b2 + hstep, voffB); PG8_STAGE(PG8_SA(0, 0), a2, voffA);
;             PG8_WAIT_V(8); PG8_WAIT_L(0); PG8_BAR; PG8_MMA(1, 0, At, B0); PG8_MMA(1, 1, At, B1); PG8_BAR; PG8_SCHED;
.LBB0_1371:
	s_add_i32 s65, s24, 2
	s_add_u32 s67, s22, 0x80
	s_addc_u32 s25, s23, 0
	s_add_i32 s66, 0, 0x10000
	s_cmp_eq_u32 s57, s24
	s_cselect_b32 s25, s5, s25
	s_cselect_b32 s24, s4, s67
	v_add_u32_e32 v0, s66, v192
	s_cselect_b64 vcc, -1, 0
	s_add_i32 s67, 0, 0x14000
	ds_read_b128 v[18:21], v0
	ds_read_b128 v[22:25], v0 offset:1024
	ds_read_b128 v[26:29], v0 offset:2048
	ds_read_b128 v[30:33], v0 offset:3072
	v_add_u32_e32 v0, s67, v192
	ds_read_b128 v[2:5], v0
	ds_read_b128 v[6:9], v0 offset:1024
	ds_read_b128 v[10:13], v0 offset:2048
	ds_read_b128 v[14:17], v0 offset:3072
	v_cndmask_b32_e32 v189, v179, v177, vcc
	v_cndmask_b32_e32 v188, v178, v176, vcc
	v_lshl_add_u64 v[190:191], s[22:23], 0, v[172:173]
	s_add_i32 m0, s50, 0xc000
	ds_read_b128 v[180:183], v194
	ds_read_b128 v[184:187], v194 offset:1024
	ds_read_b128 v[204:207], v194 offset:2048
	ds_read_b128 v[208:211], v194 offset:3072
	ds_read_b128 v[212:215], v194 offset:4096
	ds_read_b128 v[216:219], v194 offset:5120
	ds_read_b128 v[220:223], v194 offset:6144
	ds_read_b128 v[224:227], v194 offset:7168
	global_load_lds_dwordx4 v[190:191], off
	v_lshl_add_u64 v[190:191], s[22:23], 0, v[174:175]
	s_add_i32 m0, s50, 0xe000
	s_nop 0
	global_load_lds_dwordx4 v[190:191], off
	s_waitcnt vmcnt(8)
	s_waitcnt lgkmcnt(0)
	s_barrier
	s_setprio 1
	s_waitcnt lgkmcnt(0)
	v_mfma_scale_f32_16x16x128_f8f6f4 v[154:157], v[18:25], v[180:187], v[154:157], v246, v253 op_sel_hi:[0,0,0]
	v_mfma_scale_f32_16x16x128_f8f6f4 v[150:153], v[26:33], v[180:187], v[150:153], v246, v253 op_sel_hi:[0,0,0]
	v_mfma_scale_f32_16x16x128_f8f6f4 v[142:145], v[18:25], v[204:211], v[142:145], v246, v253 op_sel_hi:[0,0,0]
	v_mfma_scale_f32_16x16x128_f8f6f4 v[134:137], v[26:33], v[204:211], v[134:137], v246, v253 op_sel_hi:[0,0,0]
	v_mfma_scale_f32_16x16x128_f8f6f4 v[126:129], v[18:25], v[212:219], v[126:129], v246, v253 op_sel_hi:[0,0,0]
	v_mfma_scale_f32_16x16x128_f8f6f4 v[118:121], v[26:33], v[212:219], v[118:121], v246, v253 op_sel_hi:[0,0,0]
	v_mfma_scale_f32_16x16x128_f8f6f4 v[110:113], v[18:25], v[220:227], v[110:113], v246, v253 op_sel_hi:[0,0,0]
	v_mfma_scale_f32_16x16x128_f8f6f4 v[102:105], v[26:33], v[220:227], v[102:105], v246, v253 op_sel_hi:[0,0,0]
	s_setprio 0
	s_setprio 1
	v_mfma_scale_f32_16x16x128_f8f6f4 v[158:161], v[2:9], v[180:187], v[158:161], v247, v253 op_sel_hi:[0,0,0]
	v_mfma_scale_f32_16x16x128_f8f6f4 v[146:149], v[10:17], v[180:187], v[146:149], v247, v253 op_sel_hi:[0,0,0]
	v_mfma_scale_f32_16x16x128_f8f6f4 v[138:141], v[2:9], v[204:211], v[138:141], v247, v253 op_sel_hi:[0,0,0]
	v_mfma_scale_f32_16x16x128_f8f6f4 v[130:133], v[10:17], v[204:211], v[130:133], v247, v253 op_sel_hi:[0,0,0]
	v_mfma_scale_f32_16x16x128_f8f6f4 v[122:125], v[2:9], v[212:219], v[122:125], v247, v253 op_sel_hi:[0,0,0]
	v_mfma_scale_f32_16x16x128_f8f6f4 v[114:117], v[10:17], v[212:219], v[114:117], v247, v253 op_sel_hi:[0,0,0]
	v_mfma_scale_f32_16x16x128_f8f6f4 v[106:109], v[2:9], v[220:227], v[106:109], v247, v253 op_sel_hi:[0,0,0]
	v_mfma_scale_f32_16x16x128_f8f6f4 v[98:101], v[10:17], v[220:227], v[98:101], v247, v253 op_sel_hi:[0,0,0]
	s_setprio 0
	s_barrier
	s_add_i32 s66, s66, s49
	v_lshl_add_u64 v[180:181], v[188:189], 0, v[166:167]
	s_mov_b32 m0, s66
	ds_read_b128 v[204:207], v194 offset:16384
	ds_read_b128 v[208:211], v194 offset:17408
	ds_read_b128 v[212:215], v194 offset:18432
	ds_read_b128 v[216:219], v194 offset:19456
	ds_read_b128 v[220:223], v194 offset:20480
	ds_read_b128 v[224:227], v194 offset:21504
	ds_read_b128 v[228:231], v194 offset:22528
	ds_read_b128 v[232:235], v194 offset:23552
	global_load_lds_dwordx4 v[180:181], off
	v_lshl_add_u64 v[182:183], v[188:189], 0, v[170:171]
	s_add_i32 m0, s66, 0x2000
	v_lshl_add_u64 v[186:187], v[188:189], 0, s[10:11]
	s_add_i32 s66, s67, s49
	global_load_lds_dwordx4 v[182:183], off
	v_lshl_add_u64 v[184:185], v[186:187], 0, v[166:167]
	s_mov_b32 m0, s66
	v_lshl_add_u64 v[186:187], v[186:187], 0, v[170:171]
	global_load_lds_dwordx4 v[184:185], off
	s_add_i32 m0, s66, 0x2000
	v_lshl_add_u64 v[188:189], s[24:25], 0, v[164:165]
	global_load_lds_dwordx4 v[186:187], off
	s_mov_b32 m0, s50
	v_lshl_add_u64 v[190:191], s[24:25], 0, v[168:169]
	global_load_lds_dwordx4 v[188:189], off
	s_mov_b32 m0, s51
	s_nop 0
	global_load_lds_dwordx4 v[190:191], off
	s_waitcnt vmcnt(8)
	s_waitcnt lgkmcnt(0)
	s_barrier
	s_setprio 1
	s_waitcnt lgkmcnt(0)
	v_mfma_scale_f32_16x16x128_f8f6f4 v[94:97], v[18:25], v[204:211], v[94:97], v246, v253 op_sel_hi:[0,0,0]
	v_mfma_scale_f32_16x16x128_f8f6f4 v[86:89], v[26:33], v[204:211], v[86:89], v246, v253 op_sel_hi:[0,0,0]
	v_mfma_scale_f32_16x16x128_f8f6f4 v[78:81], v[18:25], v[212:219], v[78:81], v246, v253 op_sel_hi:[0,0,0]
	v_mfma_scale_f32_16x16x128_f8f6f4 v[70:73], v[26:33], v[212:219], v[70:73], v246, v253 op_sel_hi:[0,0,0]
	v_mfma_scale_f32_16x16x128_f8f6f4 v[62:65], v[18:25], v[220:227], v[62:65], v246, v253 op_sel_hi:[0,0,0]
	v_mfma_scale_f32_16x16x128_f8f6f4 v[54:57], v[26:33], v[220:227], v[54:57], v246, v253 op_sel_hi:[0,0,0]
	v_mfma_scale_f32_16x16x128_f8f6f4 v[46:49], v[18:25], v[228:235], v[46:49], v246, v253 op_sel_hi:[0,0,0]
	v_mfma_scale_f32_16x16x128_f8f6f4 v[38:41], v[26:33], v[228:235], v[38:41], v246, v253 op_sel_hi:[0,0,0]
	s_setprio 0
	s_setprio 1
	v_mfma_scale_f32_16x16x128_f8f6f4 v[90:93], v[2:9], v[204:211], v[90:93], v247, v253 op_sel_hi:[0,0,0]
	v_mfma_scale_f32_16x16x128_f8f6f4 v[82:85], v[10:17], v[204:211], v[82:85], v247, v253 op_sel_hi:[0,0,0]
	v_mfma_scale_f32_16x16x128_f8f6f4 v[74:77], v[2:9], v[212:219], v[74:77], v247, v253 op_sel_hi:[0,0,0]
	v_mfma_scale_f32_16x16x128_f8f6f4 v[66:69], v[10:17], v[212:219], v[66:69], v247, v253 op_sel_hi:[0,0,0]
	v_mfma_scale_f32_16x16x128_f8f6f4 v[58:61], v[2:9], v[220:227], v[58:61], v247, v253 op_sel_hi:[0,0,0]
	v_mfma_scale_f32_16x16x128_f8f6f4 v[50:53], v[10:17], v[220:227], v[50:53], v247, v253 op_sel_hi:[0,0,0]
	v_mfma_scale_f32_16x16x128_f8f6f4 v[42:45], v[2:9], v[228:235], v[42:45], v247, v253 op_sel_hi:[0,0,0]
	v_mfma_scale_f32_16x16x128_f8f6f4 v[34:37], v[10:17], v[228:235], v[34:37], v247, v253 op_sel_hi:[0,0,0]
	s_setprio 0
	s_barrier
; #define PG8_STAGE(bufoff, gbase, voff) do { _Pragma("unroll") for (int _i = 0; _i < 2; ++_i) \
;         __builtin_amdgcn_global_load_lds((const unsigned*)((const char*)(gbase) + (voff)[_i]), (PG8_LAS unsigned*)(lds + (bufoff) + ldsw + _i * 8192), 16, 0, 0); } while (0)
; #define PG8_WAIT_V(n) asm volatile("s_waitcnt vmcnt(" #n ")" ::: "memory")
; #define PG8_WAIT_L(n) asm volatile("s_waitcnt lgkmcnt(" #n ")" ::: "memory")
; #define PG8_BAR __builtin_amdgcn_s_barrier()
; #define PG8_SCHED __builtin_amdgcn_sched_barrier(0)
; template <class Epi, class Sched, bool ALIGN_EPI = false, bool SP2 = false, bool F8 = false>
; __device__ __forceinline__ void gemm_phase(PG8_LAS unsigned char* lds, const Gemm g, const Sched& S, const Epi& E, const int tidb  ) {
;     ...
;             PG8_LDB(B0, 1, 0); PG8_LDB(B1, 1, 1); PG8_SCHED; PG8_LDA(At, 1, 0); PG8_STAGE(PG8_SA(0, 1), a2 + hstep, voffA);
;             PG8_WAIT_V(8); PG8_WAIT_L(0); PG8_BAR; PG8_MMA(0, 0, At, B0); PG8_MMA(0, 1, At, B1); PG8_BAR; PG8_SCHED;
;             PG8_LDA(At, 1, 1); PG8_STAGE(PG8_SB(1, 0), b3, voffB); PG8_STAGE(PG8_SB(1, 1), b3 + hstep, voffB); PG8_STAGE(PG8_SA(1, 0), a3, voffA);
;             PG8_WAIT_V(8); PG8_WAIT_L(0); PG8_BAR; PG8_MMA(1, 0, At, B0); PG8_MMA(1, 1, At, B1); PG8_BAR; PG8_SCHED;
	s_add_i32 s66, 0, 0x18000
	v_add_u32_e32 v0, s66, v192
	s_add_i32 s67, 0, 0x1c000
	ds_read_b128 v[2:5], v0
	ds_read_b128 v[6:9], v0 offset:1024
	ds_read_b128 v[10:13], v0 offset:2048
	ds_read_b128 v[14:17], v0 offset:3072
	v_add_u32_e32 v0, s67, v192
	ds_read_b128 v[18:21], v0
	ds_read_b128 v[22:25], v0 offset:1024
	ds_read_b128 v[26:29], v0 offset:2048
	ds_read_b128 v[30:33], v0 offset:3072
	s_add_u32 s24, s24, s10
	s_addc_u32 s25, s25, s11
	s_mov_b32 m0, s52
	v_lshl_add_u64 v[196:197], s[24:25], 0, v[164:165]
	ds_read_b128 v[204:207], v194 offset:32768
	ds_read_b128 v[208:211], v194 offset:33792
	ds_read_b128 v[212:215], v194 offset:34816
	ds_read_b128 v[216:219], v194 offset:35840
	ds_read_b128 v[220:223], v194 offset:36864
	ds_read_b128 v[224:227], v194 offset:37888
	ds_read_b128 v[228:231], v194 offset:38912
	ds_read_b128 v[232:235], v194 offset:39936
	global_load_lds_dwordx4 v[196:197], off
	v_lshl_add_u64 v[196:197], s[24:25], 0, v[168:169]
	s_mov_b32 m0, s53
	s_nop 0
	global_load_lds_dwordx4 v[196:197], off
	s_waitcnt vmcnt(8)
	s_waitcnt lgkmcnt(0)
	s_barrier
	s_setprio 1
	s_waitcnt lgkmcnt(0)
	v_mfma_scale_f32_16x16x128_f8f6f4 v[154:157], v[2:9], v[204:211], v[154:157], v246, v253 op_sel_hi:[0,0,0]
	v_mfma_scale_f32_16x16x128_f8f6f4 v[150:153], v[10:17], v[204:211], v[150:153], v246, v253 op_sel_hi:[0,0,0]
	v_mfma_scale_f32_16x16x128_f8f6f4 v[142:145], v[2:9], v[212:219], v[142:145], v246, v253 op_sel_hi:[0,0,0]
	v_mfma_scale_f32_16x16x128_f8f6f4 v[134:137], v[10:17], v[212:219], v[134:137], v246, v253 op_sel_hi:[0,0,0]
	v_mfma_scale_f32_16x16x128_f8f6f4 v[126:129], v[2:9], v[220:227], v[126:129], v246, v253 op_sel_hi:[0,0,0]
	v_mfma_scale_f32_16x16x128_f8f6f4 v[118:121], v[10:17], v[220:227], v[118:121], v246, v253 op_sel_hi:[0,0,0]
	v_mfma_scale_f32_16x16x128_f8f6f4 v[110:113], v[2:9], v[228:235], v[110:113], v246, v253 op_sel_hi:[0,0,0]
	v_mfma_scale_f32_16x16x128_f8f6f4 v[102:105], v[10:17], v[228:235], v[102:105], v246, v253 op_sel_hi:[0,0,0]
	s_setprio 0
	s_setprio 1
	v_mfma_scale_f32_16x16x128_f8f6f4 v[158:161], v[18:25], v[204:211], v[158:161], v247, v253 op_sel_hi:[0,0,0]
	v_mfma_scale_f32_16x16x128_f8f6f4 v[146:149], v[26:33], v[204:211], v[146:149], v247, v253 op_sel_hi:[0,0,0]
	v_mfma_scale_f32_16x16x128_f8f6f4 v[138:141], v[18:25], v[212:219], v[138:141], v247, v253 op_sel_hi:[0,0,0]
	v_mfma_scale_f32_16x16x128_f8f6f4 v[130:133], v[26:33], v[212:219], v[130:133], v247, v253 op_sel_hi:[0,0,0]
	v_mfma_scale_f32_16x16x128_f8f6f4 v[122:125], v[18:25], v[220:227], v[122:125], v247, v253 op_sel_hi:[0,0,0]
	v_mfma_scale_f32_16x16x128_f8f6f4 v[114:117], v[26:33], v[220:227], v[114:117], v247, v253 op_sel_hi:[0,0,0]
	v_mfma_scale_f32_16x16x128_f8f6f4 v[106:109], v[18:25], v[228:235], v[106:109], v247, v253 op_sel_hi:[0,0,0]
	v_mfma_scale_f32_16x16x128_f8f6f4 v[98:101], v[26:33], v[228:235], v[98:101], v247, v253 op_sel_hi:[0,0,0]
	s_setprio 0
	s_barrier
	s_add_i32 s24, s66, s49
	v_lshl_add_u64 v[180:181], v[180:181], 0, s[92:93]
	s_mov_b32 m0, s24
	ds_read_b128 v[204:207], v194 offset:49152
	ds_read_b128 v[208:211], v194 offset:50176
	ds_read_b128 v[212:215], v194 offset:51200
	ds_read_b128 v[216:219], v194 offset:52224
	ds_read_b128 v[220:223], v194 offset:53248
	ds_read_b128 v[224:227], v194 offset:54272
	ds_read_b128 v[228:231], v194 offset:55296
	ds_read_b128 v[232:235], v194 offset:56320
	global_load_lds_dwordx4 v[180:181], off
	v_lshl_add_u64 v[180:181], v[182:183], 0, s[92:93]
	s_add_i32 m0, s24, 0x2000
	s_add_i32 s24, s67, s49
	global_load_lds_dwordx4 v[180:181], off
	v_lshl_add_u64 v[180:181], v[184:185], 0, s[92:93]
	s_mov_b32 m0, s24
	s_nop 0
	global_load_lds_dwordx4 v[180:181], off
	v_lshl_add_u64 v[180:181], v[186:187], 0, s[92:93]
	s_add_i32 m0, s24, 0x2000
	s_nop 0
	global_load_lds_dwordx4 v[180:181], off
	v_lshl_add_u64 v[180:181], v[188:189], 0, s[92:93]
	s_mov_b32 m0, s54
	s_nop 0
	global_load_lds_dwordx4 v[180:181], off
	v_lshl_add_u64 v[180:181], v[190:191], 0, s[92:93]
	s_mov_b32 m0, s55
	s_nop 0
	global_load_lds_dwordx4 v[180:181], off
	s_waitcnt vmcnt(8)
	s_waitcnt lgkmcnt(0)
	s_barrier
	s_setprio 1
	s_waitcnt lgkmcnt(0)
	v_mfma_scale_f32_16x16x128_f8f6f4 v[94:97], v[2:9], v[204:211], v[94:97], v246, v253 op_sel_hi:[0,0,0]
	v_mfma_scale_f32_16x16x128_f8f6f4 v[86:89], v[10:17], v[204:211], v[86:89], v246, v253 op_sel_hi:[0,0,0]
	v_mfma_scale_f32_16x16x128_f8f6f4 v[78:81], v[2:9], v[212:219], v[78:81], v246, v253 op_sel_hi:[0,0,0]
	v_mfma_scale_f32_16x16x128_f8f6f4 v[70:73], v[10:17], v[212:219], v[70:73], v246, v253 op_sel_hi:[0,0,0]
	v_mfma_scale_f32_16x16x128_f8f6f4 v[62:65], v[2:9], v[220:227], v[62:65], v246, v253 op_sel_hi:[0,0,0]
	v_mfma_scale_f32_16x16x128_f8f6f4 v[54:57], v[10:17], v[220:227], v[54:57], v246, v253 op_sel_hi:[0,0,0]
	v_mfma_scale_f32_16x16x128_f8f6f4 v[46:49], v[2:9], v[228:235], v[46:49], v246, v253 op_sel_hi:[0,0,0]
	v_mfma_scale_f32_16x16x128_f8f6f4 v[38:41], v[10:17], v[228:235], v[38:41], v246, v253 op_sel_hi:[0,0,0]
	s_setprio 0
	s_setprio 1
	v_mfma_scale_f32_16x16x128_f8f6f4 v[90:93], v[18:25], v[204:211], v[90:93], v247, v253 op_sel_hi:[0,0,0]
	v_mfma_scale_f32_16x16x128_f8f6f4 v[82:85], v[26:33], v[204:211], v[82:85], v247, v253 op_sel_hi:[0,0,0]
	v_mfma_scale_f32_16x16x128_f8f6f4 v[74:77], v[18:25], v[212:219], v[74:77], v247, v253 op_sel_hi:[0,0,0]
	v_mfma_scale_f32_16x16x128_f8f6f4 v[66:69], v[26:33], v[212:219], v[66:69], v247, v253 op_sel_hi:[0,0,0]
	v_mfma_scale_f32_16x16x128_f8f6f4 v[58:61], v[18:25], v[220:227], v[58:61], v247, v253 op_sel_hi:[0,0,0]
	v_mfma_scale_f32_16x16x128_f8f6f4 v[50:53], v[26:33], v[220:227], v[50:53], v247, v253 op_sel_hi:[0,0,0]
	v_mfma_scale_f32_16x16x128_f8f6f4 v[42:45], v[18:25], v[228:235], v[42:45], v247, v253 op_sel_hi:[0,0,0]
	v_mfma_scale_f32_16x16x128_f8f6f4 v[34:37], v[26:33], v[228:235], v[34:37], v247, v253 op_sel_hi:[0,0,0]
	s_setprio 0
	s_add_u32 s22, s22, 0x100
	s_addc_u32 s23, s23, 0
	v_lshl_add_u64 v[178:179], v[178:179], 0, s[84:85]
	s_cmp_ge_i32 s65, s56
	s_mov_b32 s24, s65
	s_barrier
	s_cbranch_scc0 .LBB0_1371
	s_movk_i32 s67, 0x300

;     __device__ __forceinline__ bool next(int i, Unit& u) const { return so.next(i, u); }
; #define PG8_STAGE(bufoff, gbase, voff) do { _Pragma("unroll") for (int _i = 0; _i < 2; ++_i) \
;         __builtin_amdgcn_global_load_lds((const unsigned*)((const char*)(gbase) + (voff)[_i]), (PG8_LAS unsigned*)(lds + (bufoff) + ldsw + _i * 8192), 16, 0, 0); } while (0)
; #define PG8_WAIT_V(n) asm volatile("s_waitcnt vmcnt(" #n ")" ::: "memory")
; #define PG8_WAIT_L(n) asm volatile("s_waitcnt lgkmcnt(" #n ")" ::: "memory")
; #define PG8_BAR __builtin_amdgcn_s_barrier()
; #define PG8_SCHED __builtin_amdgcn_sched_barrier(0)
; template <class Epi, class Sched, bool ALIGN_EPI = false, bool SP2 = false, bool F8 = false>
; __device__ __forceinline__ void gemm_phase(PG8_LAS unsigned char* lds, const Gemm g, const Sched& S, const Epi& E, const int tidb  ) {
;     ...
;         const bool has_next = S.next(ui + 1, nxt);
;         const char* nA = has_next ? (const char*)g.A + (size_t)nxt.pm * tstep : cA; const char* nB = has_next ? (const char*)g.Bt + S.boff(nxt) + (size_t)nxt.pn * tstep : cB;
;         for (int t = 0; t < nt; t += 2) {
;             const bool last = (t == nt - 2);
;             if constexpr (Epi::PREFETCH) { if (t == 0) E.prefetch(cur, wid, lane); }
;             const char* a1 = cA + (size_t)(t + 1) * kstep;
;             const char* a2 = last ? nA : cA + (size_t)(t + 2) * kstep; const char* b2 = last ? nB : cB + (size_t)(t + 2) * kstep;
;             const char* a3 = a2 + kstep; const char* b3 = b2 + kstep;
;             if (last && has_next) S.a_ready(nxt);
;             if constexpr (SP2) {
;             PG8_LDB(B0, 0, 0); PG8_LDB(B1, 0, 1); PG8_SCHED; PG8_LDA(At, 0, 0); PG8_STAGE(PG8_SA(1, 1), a1 + hstep, voffA);
;             PG8_WAIT_V(8); PG8_WAIT_L(0); PG8_BAR; PG8_MMA(0, 0, At, B0); PG8_MMA(0, 1, At, B1); PG8_BAR; PG8_SCHED;
;             PG8_LDA(At, 0, 1); PG8_STAGE(PG8_SB(0, 0), b2, voffB); PG8_STAGE(PG8_SB(0, 1), b2 + hstep, voffB); PG8_STAGE(PG8_SA(0, 0), a2, voffA);
;             PG8_WAIT_V(8); PG8_WAIT_L(0); PG8_BAR; PG8_MMA(1, 0, At, B0); PG8_MMA(1, 1, At, B1); PG8_BAR; PG8_SCHED;
.LBB0_1452:
	ds_read_b128 v[6:9], v175 offset:3072
	ds_read_b128 v[2:5], v175 offset:2048
	ds_read_b128 v[182:185], v175 offset:1024
	ds_read_b128 v[178:181], v175
	ds_read_b128 v[190:193], v0 offset:3072
	ds_read_b128 v[186:189], v0 offset:2048
	ds_read_b128 v[208:211], v0 offset:1024
	ds_read_b128 v[204:207], v0
	s_add_u32 s54, s52, 0x80
	s_addc_u32 s55, s53, 0
	s_cmp_eq_u32 s66, s72
	s_cselect_b64 vcc, -1, 0
	s_cselect_b32 s55, s7, s55
	s_cselect_b32 s54, s6, s54
	v_cndmask_b32_e32 v161, v155, v153, vcc
	v_cndmask_b32_e32 v160, v154, v152, vcc
	s_mov_b32 m0, s35
	v_lshl_add_u64 v[156:157], s[52:53], 0, v[148:149]
	ds_read_b128 v[212:215], v174
	ds_read_b128 v[216:219], v174 offset:1024
	ds_read_b128 v[220:223], v174 offset:2048
	ds_read_b128 v[224:227], v174 offset:3072
	ds_read_b128 v[228:231], v174 offset:4096
	ds_read_b128 v[232:235], v174 offset:5120
	ds_read_b128 v[236:239], v174 offset:6144
	ds_read_b128 v[240:243], v174 offset:7168
	global_load_lds_dwordx4 v[156:157], off
	v_lshl_add_u64 v[156:157], s[52:53], 0, v[150:151]
	s_mov_b32 m0, s56
	s_nop 0
	global_load_lds_dwordx4 v[156:157], off
	s_waitcnt vmcnt(8)
	s_waitcnt lgkmcnt(0)
	s_barrier
	s_setprio 1
	s_waitcnt lgkmcnt(0)
	v_mfma_scale_f32_16x16x128_f8f6f4 v[134:137], v[204:211], v[212:219], v[134:137], v246, v247 op_sel_hi:[0,0,0]
	v_mfma_scale_f32_16x16x128_f8f6f4 v[130:133], v[186:193], v[212:219], v[130:133], v246, v247 op_sel_hi:[0,0,0]
	v_mfma_scale_f32_16x16x128_f8f6f4 v[118:121], v[204:211], v[220:227], v[118:121], v246, v247 op_sel_hi:[0,0,0]
	v_mfma_scale_f32_16x16x128_f8f6f4 v[114:117], v[186:193], v[220:227], v[114:117], v246, v247 op_sel_hi:[0,0,0]
	v_mfma_scale_f32_16x16x128_f8f6f4 v[102:105], v[204:211], v[228:235], v[102:105], v246, v247 op_sel_hi:[0,0,0]
	v_mfma_scale_f32_16x16x128_f8f6f4 v[98:101], v[186:193], v[228:235], v[98:101], v246, v247 op_sel_hi:[0,0,0]
	v_mfma_scale_f32_16x16x128_f8f6f4 v[86:89], v[204:211], v[236:243], v[86:89], v246, v247 op_sel_hi:[0,0,0]
	v_mfma_scale_f32_16x16x128_f8f6f4 v[82:85], v[186:193], v[236:243], v[82:85], v246, v247 op_sel_hi:[0,0,0]
	s_setprio 0
	s_setprio 1
	v_mfma_scale_f32_16x16x128_f8f6f4 v[126:129], v[178:185], v[212:219], v[126:129], v246, v247 op_sel_hi:[0,0,0]
	v_mfma_scale_f32_16x16x128_f8f6f4 v[122:125], v[2:9], v[212:219], v[122:125], v246, v247 op_sel_hi:[0,0,0]
	v_mfma_scale_f32_16x16x128_f8f6f4 v[110:113], v[178:185], v[220:227], v[110:113], v246, v247 op_sel_hi:[0,0,0]
	v_mfma_scale_f32_16x16x128_f8f6f4 v[106:109], v[2:9], v[220:227], v[106:109], v246, v247 op_sel_hi:[0,0,0]
	v_mfma_scale_f32_16x16x128_f8f6f4 v[94:97], v[178:185], v[228:235], v[94:97], v246, v247 op_sel_hi:[0,0,0]
	v_mfma_scale_f32_16x16x128_f8f6f4 v[90:93], v[2:9], v[228:235], v[90:93], v246, v247 op_sel_hi:[0,0,0]
	v_mfma_scale_f32_16x16x128_f8f6f4 v[78:81], v[178:185], v[236:243], v[78:81], v246, v247 op_sel_hi:[0,0,0]
	v_mfma_scale_f32_16x16x128_f8f6f4 v[70:73], v[2:9], v[236:243], v[70:73], v246, v247 op_sel_hi:[0,0,0]
	s_setprio 0
	s_barrier
	s_mov_b32 m0, s57
	v_lshl_add_u64 v[156:157], v[160:161], 0, v[140:141]
	ds_read_b128 v[212:215], v174 offset:16384
	ds_read_b128 v[216:219], v174 offset:17408
	ds_read_b128 v[220:223], v174 offset:18432
	ds_read_b128 v[224:227], v174 offset:19456
	ds_read_b128 v[228:231], v174 offset:20480
	ds_read_b128 v[232:235], v174 offset:21504
	ds_read_b128 v[236:239], v174 offset:22528
	ds_read_b128 v[240:243], v174 offset:23552
	global_load_lds_dwordx4 v[156:157], off
	v_lshl_add_u64 v[158:159], v[160:161], 0, v[144:145]
	s_mov_b32 m0, s68
	v_lshl_add_u64 v[164:165], v[160:161], 0, s[16:17]
	global_load_lds_dwordx4 v[158:159], off
	v_lshl_add_u64 v[160:161], v[164:165], 0, v[140:141]
	s_mov_b32 m0, s70
	v_lshl_add_u64 v[164:165], v[164:165], 0, v[144:145]
	global_load_lds_dwordx4 v[160:161], off
	s_mov_b32 m0, s71
	v_lshl_add_u64 v[166:167], s[54:55], 0, v[138:139]
	global_load_lds_dwordx4 v[164:165], off
	s_mov_b32 m0, s59
	v_lshl_add_u64 v[168:169], s[54:55], 0, v[142:143]
	global_load_lds_dwordx4 v[166:167], off
	s_mov_b32 m0, s60
	s_nop 0
	global_load_lds_dwordx4 v[168:169], off
	s_waitcnt vmcnt(8)
	s_waitcnt lgkmcnt(0)
	s_barrier
	s_setprio 1
	s_waitcnt lgkmcnt(0)
	v_mfma_scale_f32_16x16x128_f8f6f4 v[74:77], v[204:211], v[212:219], v[74:77], v246, v247 op_sel_hi:[0,0,0]
	v_mfma_scale_f32_16x16x128_f8f6f4 v[66:69], v[186:193], v[212:219], v[66:69], v246, v247 op_sel_hi:[0,0,0]
	v_mfma_scale_f32_16x16x128_f8f6f4 v[54:57], v[204:211], v[220:227], v[54:57], v246, v247 op_sel_hi:[0,0,0]
	v_mfma_scale_f32_16x16x128_f8f6f4 v[50:53], v[186:193], v[220:227], v[50:53], v246, v247 op_sel_hi:[0,0,0]
	v_mfma_scale_f32_16x16x128_f8f6f4 v[38:41], v[204:211], v[228:235], v[38:41], v246, v247 op_sel_hi:[0,0,0]
	v_mfma_scale_f32_16x16x128_f8f6f4 v[34:37], v[186:193], v[228:235], v[34:37], v246, v247 op_sel_hi:[0,0,0]
	v_mfma_scale_f32_16x16x128_f8f6f4 v[22:25], v[204:211], v[236:243], v[22:25], v246, v247 op_sel_hi:[0,0,0]
	v_mfma_scale_f32_16x16x128_f8f6f4 v[18:21], v[186:193], v[236:243], v[18:21], v246, v247 op_sel_hi:[0,0,0]
	s_setprio 0
	s_setprio 1
	v_mfma_scale_f32_16x16x128_f8f6f4 v[62:65], v[178:185], v[212:219], v[62:65], v246, v247 op_sel_hi:[0,0,0]
	v_mfma_scale_f32_16x16x128_f8f6f4 v[58:61], v[2:9], v[212:219], v[58:61], v246, v247 op_sel_hi:[0,0,0]
	v_mfma_scale_f32_16x16x128_f8f6f4 v[46:49], v[178:185], v[220:227], v[46:49], v246, v247 op_sel_hi:[0,0,0]
	v_mfma_scale_f32_16x16x128_f8f6f4 v[42:45], v[2:9], v[220:227], v[42:45], v246, v247 op_sel_hi:[0,0,0]
	v_mfma_scale_f32_16x16x128_f8f6f4 v[30:33], v[178:185], v[228:235], v[30:33], v246, v247 op_sel_hi:[0,0,0]
	v_mfma_scale_f32_16x16x128_f8f6f4 v[26:29], v[2:9], v[228:235], v[26:29], v246, v247 op_sel_hi:[0,0,0]
	v_mfma_scale_f32_16x16x128_f8f6f4 v[14:17], v[178:185], v[236:243], v[14:17], v246, v247 op_sel_hi:[0,0,0]
	v_mfma_scale_f32_16x16x128_f8f6f4 v[10:13], v[2:9], v[236:243], v[10:13], v246, v247 op_sel_hi:[0,0,0]
	s_setprio 0
	s_barrier
; #define PG8_STAGE(bufoff, gbase, voff) do { _Pragma("unroll") for (int _i = 0; _i < 2; ++_i) \
;         __builtin_amdgcn_global_load_lds((const unsigned*)((const char*)(gbase) + (voff)[_i]), (PG8_LAS unsigned*)(lds + (bufoff) + ldsw + _i * 8192), 16, 0, 0); } while (0)
; #define PG8_WAIT_V(n) asm volatile("s_waitcnt vmcnt(" #n ")" ::: "memory")
; #define PG8_WAIT_L(n) asm volatile("s_waitcnt lgkmcnt(" #n ")" ::: "memory")
; #define PG8_BAR __builtin_amdgcn_s_barrier()
; #define PG8_SCHED __builtin_amdgcn_sched_barrier(0)
; template <class Epi, class Sched, bool ALIGN_EPI = false, bool SP2 = false, bool F8 = false>
; __device__ __forceinline__ void gemm_phase(PG8_LAS unsigned char* lds, const Gemm g, const Sched& S, const Epi& E, const int tidb  ) {
;     ...
;         for (int t = 0; t < nt; t += 2) {
;     ...
;             PG8_LDB(B0, 1, 0); PG8_LDB(B1, 1, 1); PG8_SCHED; PG8_LDA(At, 1, 0); PG8_STAGE(PG8_SA(0, 1), a2 + hstep, voffA);
;             PG8_WAIT_V(8); PG8_WAIT_L(0); PG8_BAR; PG8_MMA(0, 0, At, B0); PG8_MMA(0, 1, At, B1); PG8_BAR; PG8_SCHED;
;             PG8_LDA(At, 1, 1); PG8_STAGE(PG8_SB(1, 0), b3, voffB); PG8_STAGE(PG8_SB(1, 1), b3 + hstep, voffB); PG8_STAGE(PG8_SA(1, 0), a3, voffA);
;             PG8_WAIT_V(8); PG8_WAIT_L(0); PG8_BAR; PG8_MMA(1, 0, At, B0); PG8_MMA(1, 1, At, B1); PG8_BAR; PG8_SCHED;
	ds_read_b128 v[178:181], v176
	ds_read_b128 v[182:185], v176 offset:1024
	ds_read_b128 v[186:189], v176 offset:2048
	ds_read_b128 v[190:193], v176 offset:3072
	ds_read_b128 v[2:5], v177
	ds_read_b128 v[6:9], v177 offset:1024
	ds_read_b128 v[204:207], v177 offset:2048
	ds_read_b128 v[208:211], v177 offset:3072
	s_add_u32 s54, s54, s16
	s_addc_u32 s55, s55, s17
	s_mov_b32 m0, s61
	v_lshl_add_u64 v[194:195], s[54:55], 0, v[138:139]
	ds_read_b128 v[212:215], v174 offset:32768
	ds_read_b128 v[216:219], v174 offset:33792
	ds_read_b128 v[220:223], v174 offset:34816
	ds_read_b128 v[224:227], v174 offset:35840
	ds_read_b128 v[228:231], v174 offset:36864
	ds_read_b128 v[232:235], v174 offset:37888
	ds_read_b128 v[236:239], v174 offset:38912
	ds_read_b128 v[240:243], v174 offset:39936
	global_load_lds_dwordx4 v[194:195], off
	v_lshl_add_u64 v[194:195], s[54:55], 0, v[142:143]
	s_mov_b32 m0, s62
	s_nop 0
	global_load_lds_dwordx4 v[194:195], off
	s_waitcnt vmcnt(8)
	s_waitcnt lgkmcnt(0)
	s_barrier
	s_setprio 1
	s_waitcnt lgkmcnt(0)
	v_mfma_scale_f32_16x16x128_f8f6f4 v[134:137], v[178:185], v[212:219], v[134:137], v246, v247 op_sel_hi:[0,0,0]
	v_mfma_scale_f32_16x16x128_f8f6f4 v[130:133], v[186:193], v[212:219], v[130:133], v246, v247 op_sel_hi:[0,0,0]
	v_mfma_scale_f32_16x16x128_f8f6f4 v[118:121], v[178:185], v[220:227], v[118:121], v246, v247 op_sel_hi:[0,0,0]
	v_mfma_scale_f32_16x16x128_f8f6f4 v[114:117], v[186:193], v[220:227], v[114:117], v246, v247 op_sel_hi:[0,0,0]
	v_mfma_scale_f32_16x16x128_f8f6f4 v[102:105], v[178:185], v[228:235], v[102:105], v246, v247 op_sel_hi:[0,0,0]
	v_mfma_scale_f32_16x16x128_f8f6f4 v[98:101], v[186:193], v[228:235], v[98:101], v246, v247 op_sel_hi:[0,0,0]
	v_mfma_scale_f32_16x16x128_f8f6f4 v[86:89], v[178:185], v[236:243], v[86:89], v246, v247 op_sel_hi:[0,0,0]
	v_mfma_scale_f32_16x16x128_f8f6f4 v[82:85], v[186:193], v[236:243], v[82:85], v246, v247 op_sel_hi:[0,0,0]
	s_setprio 0
	s_setprio 1
	v_mfma_scale_f32_16x16x128_f8f6f4 v[126:129], v[2:9], v[212:219], v[126:129], v246, v247 op_sel_hi:[0,0,0]
	v_mfma_scale_f32_16x16x128_f8f6f4 v[122:125], v[204:211], v[212:219], v[122:125], v246, v247 op_sel_hi:[0,0,0]
	v_mfma_scale_f32_16x16x128_f8f6f4 v[110:113], v[2:9], v[220:227], v[110:113], v246, v247 op_sel_hi:[0,0,0]
	v_mfma_scale_f32_16x16x128_f8f6f4 v[106:109], v[204:211], v[220:227], v[106:109], v246, v247 op_sel_hi:[0,0,0]
	v_mfma_scale_f32_16x16x128_f8f6f4 v[94:97], v[2:9], v[228:235], v[94:97], v246, v247 op_sel_hi:[0,0,0]
	v_mfma_scale_f32_16x16x128_f8f6f4 v[90:93], v[204:211], v[228:235], v[90:93], v246, v247 op_sel_hi:[0,0,0]
	v_mfma_scale_f32_16x16x128_f8f6f4 v[78:81], v[2:9], v[236:243], v[78:81], v246, v247 op_sel_hi:[0,0,0]
	v_mfma_scale_f32_16x16x128_f8f6f4 v[70:73], v[204:211], v[236:243], v[70:73], v246, v247 op_sel_hi:[0,0,0]
	s_setprio 0
	s_barrier
	s_mov_b32 m0, s91
	v_lshl_add_u64 v[156:157], v[156:157], 0, s[92:93]
	ds_read_b128 v[212:215], v174 offset:49152
	ds_read_b128 v[216:219], v174 offset:50176
	ds_read_b128 v[220:223], v174 offset:51200
	ds_read_b128 v[224:227], v174 offset:52224
	ds_read_b128 v[228:231], v174 offset:53248
	ds_read_b128 v[232:235], v174 offset:54272
	ds_read_b128 v[236:239], v174 offset:55296
	ds_read_b128 v[240:243], v174 offset:56320
	global_load_lds_dwordx4 v[156:157], off
	v_lshl_add_u64 v[156:157], v[158:159], 0, s[92:93]
	s_mov_b32 m0, s94
	s_nop 0
	global_load_lds_dwordx4 v[156:157], off
	v_lshl_add_u64 v[156:157], v[160:161], 0, s[92:93]
	s_mov_b32 m0, s95
	s_nop 0
	global_load_lds_dwordx4 v[156:157], off
	v_lshl_add_u64 v[156:157], v[164:165], 0, s[92:93]
	s_mov_b32 m0, s97
	s_nop 0
	global_load_lds_dwordx4 v[156:157], off
	v_lshl_add_u64 v[156:157], v[166:167], 0, s[92:93]
	s_mov_b32 m0, s63
	s_nop 0
	global_load_lds_dwordx4 v[156:157], off
	v_lshl_add_u64 v[156:157], v[168:169], 0, s[92:93]
	s_mov_b32 m0, s65
	s_nop 0
	global_load_lds_dwordx4 v[156:157], off
	s_waitcnt vmcnt(8)
	s_waitcnt lgkmcnt(0)
	s_barrier
	s_setprio 1
	s_waitcnt lgkmcnt(0)
	v_mfma_scale_f32_16x16x128_f8f6f4 v[74:77], v[178:185], v[212:219], v[74:77], v246, v247 op_sel_hi:[0,0,0]
	v_mfma_scale_f32_16x16x128_f8f6f4 v[66:69], v[186:193], v[212:219], v[66:69], v246, v247 op_sel_hi:[0,0,0]
	v_mfma_scale_f32_16x16x128_f8f6f4 v[54:57], v[178:185], v[220:227], v[54:57], v246, v247 op_sel_hi:[0,0,0]
	v_mfma_scale_f32_16x16x128_f8f6f4 v[50:53], v[186:193], v[220:227], v[50:53], v246, v247 op_sel_hi:[0,0,0]
	v_mfma_scale_f32_16x16x128_f8f6f4 v[38:41], v[178:185], v[228:235], v[38:41], v246, v247 op_sel_hi:[0,0,0]
	v_mfma_scale_f32_16x16x128_f8f6f4 v[34:37], v[186:193], v[228:235], v[34:37], v246, v247 op_sel_hi:[0,0,0]
	v_mfma_scale_f32_16x16x128_f8f6f4 v[22:25], v[178:185], v[236:243], v[22:25], v246, v247 op_sel_hi:[0,0,0]
	v_mfma_scale_f32_16x16x128_f8f6f4 v[18:21], v[186:193], v[236:243], v[18:21], v246, v247 op_sel_hi:[0,0,0]
	s_setprio 0
	s_setprio 1
	v_mfma_scale_f32_16x16x128_f8f6f4 v[62:65], v[2:9], v[212:219], v[62:65], v246, v247 op_sel_hi:[0,0,0]
	v_mfma_scale_f32_16x16x128_f8f6f4 v[58:61], v[204:211], v[212:219], v[58:61], v246, v247 op_sel_hi:[0,0,0]
	v_mfma_scale_f32_16x16x128_f8f6f4 v[46:49], v[2:9], v[220:227], v[46:49], v246, v247 op_sel_hi:[0,0,0]
	v_mfma_scale_f32_16x16x128_f8f6f4 v[42:45], v[204:211], v[220:227], v[42:45], v246, v247 op_sel_hi:[0,0,0]
	v_mfma_scale_f32_16x16x128_f8f6f4 v[30:33], v[2:9], v[228:235], v[30:33], v246, v247 op_sel_hi:[0,0,0]
	v_mfma_scale_f32_16x16x128_f8f6f4 v[26:29], v[204:211], v[228:235], v[26:29], v246, v247 op_sel_hi:[0,0,0]
	v_mfma_scale_f32_16x16x128_f8f6f4 v[14:17], v[2:9], v[236:243], v[14:17], v246, v247 op_sel_hi:[0,0,0]
	v_mfma_scale_f32_16x16x128_f8f6f4 v[10:13], v[204:211], v[236:243], v[10:13], v246, v247 op_sel_hi:[0,0,0]
	s_setprio 0
	s_add_i32 s54, s72, 2
	s_add_u32 s52, s52, 0x100
	s_addc_u32 s53, s53, 0
	v_lshl_add_u64 v[154:155], v[154:155], 0, s[10:11]
	s_cmp_ge_i32 s72, s66
	s_mov_b32 s72, s54
	s_barrier
	s_cbranch_scc0 .LBB0_1452

;     __device__ __forceinline__ bool next(int i, Unit& u) const { return so.next(i, u); }
; #define PG8_STAGE(bufoff, gbase, voff) do { _Pragma("unroll") for (int _i = 0; _i < 2; ++_i) \
;         __builtin_amdgcn_global_load_lds((const unsigned*)((const char*)(gbase) + (voff)[_i]), (PG8_LAS unsigned*)(lds + (bufoff) + ldsw + _i * 8192), 16, 0, 0); } while (0)
; #define PG8_WAIT_V(n) asm volatile("s_waitcnt vmcnt(" #n ")" ::: "memory")
; #define PG8_WAIT_L(n) asm volatile("s_waitcnt lgkmcnt(" #n ")" ::: "memory")
; #define PG8_BAR __builtin_amdgcn_s_barrier()
; #define PG8_SCHED __builtin_amdgcn_sched_barrier(0)
; template <class Epi, class Sched, bool ALIGN_EPI = false, bool SP2 = false, bool F8 = false>
; __device__ __forceinline__ void gemm_phase(PG8_LAS unsigned char* lds, const Gemm g, const Sched& S, const Epi& E, const int tidb  ) {
;     ...
;         const bool has_next = S.next(ui + 1, nxt);
;         const char* nA = has_next ? (const char*)g.A + (size_t)nxt.pm * tstep : cA; const char* nB = has_next ? (const char*)g.Bt + S.boff(nxt) + (size_t)nxt.pn * tstep : cB;
;         for (int t = 0; t < nt; t += 2) {
;             const bool last = (t == nt - 2);
;             if constexpr (Epi::PREFETCH) { if (t == 0) E.prefetch(cur, wid, lane); }
;             const char* a1 = cA + (size_t)(t + 1) * kstep;
;             const char* a2 = last ? nA : cA + (size_t)(t + 2) * kstep; const char* b2 = last ? nB : cB + (size_t)(t + 2) * kstep;
;             const char* a3 = a2 + kstep; const char* b3 = b2 + kstep;
;             if (last && has_next) S.a_ready(nxt);
;             if constexpr (SP2) {
;             PG8_LDB(B0, 0, 0); PG8_LDB(B1, 0, 1); PG8_SCHED; PG8_LDA(At, 0, 0); PG8_STAGE(PG8_SA(1, 1), a1 + hstep, voffA);
;             PG8_WAIT_V(8); PG8_WAIT_L(0); PG8_BAR; PG8_MMA(0, 0, At, B0); PG8_MMA(0, 1, At, B1); PG8_BAR; PG8_SCHED;
;             PG8_LDA(At, 0, 1); PG8_STAGE(PG8_SB(0, 0), b2, voffB); PG8_STAGE(PG8_SB(0, 1), b2 + hstep, voffB); PG8_STAGE(PG8_SA(0, 0), a2, voffA);
;             PG8_WAIT_V(8); PG8_WAIT_L(0); PG8_BAR; PG8_MMA(1, 0, At, B0); PG8_MMA(1, 1, At, B1); PG8_BAR; PG8_SCHED;
.LBB0_1705:
	s_add_i32 s60, s28, 2
	s_add_u32 s61, s26, 0x80
	s_addc_u32 s29, s27, 0
	s_add_i32 s65, 0, 0x10000
	s_cmp_eq_u32 s51, s28
	s_cselect_b32 s29, s5, s29
	s_cselect_b32 s28, s4, s61
	v_add_u32_e32 v148, s65, v151
	s_cselect_b32 s63, s25, s59
	s_cselect_b32 s62, s24, s58
	s_add_i32 s61, 0, 0x14000
	ds_read_b128 v[140:143], v148
	ds_read_b128 v[144:147], v148 offset:1024
	ds_read_b128 v[158:161], v148 offset:2048
	ds_read_b128 v[164:167], v148 offset:3072
	v_add_u32_e32 v148, s61, v151
	ds_read_b128 v[168:171], v148
	ds_read_b128 v[172:175], v148 offset:1024
	ds_read_b128 v[176:179], v148 offset:2048
	ds_read_b128 v[180:183], v148 offset:3072
	v_lshl_add_u64 v[148:149], s[26:27], 0, v[136:137]
	s_add_i32 m0, s41, 0xc000
	ds_read_b128 v[184:187], v156
	ds_read_b128 v[188:191], v156 offset:1024
	ds_read_b128 v[192:195], v156 offset:2048
	ds_read_b128 v[204:207], v156 offset:3072
	ds_read_b128 v[208:211], v156 offset:4096
	ds_read_b128 v[212:215], v156 offset:5120
	ds_read_b128 v[216:219], v156 offset:6144
	ds_read_b128 v[220:223], v156 offset:7168
	global_load_lds_dwordx4 v[148:149], off
	v_lshl_add_u64 v[148:149], s[26:27], 0, v[138:139]
	s_add_i32 m0, s41, 0xe000
	s_nop 0
	global_load_lds_dwordx4 v[148:149], off
	s_waitcnt vmcnt(8)
	s_waitcnt lgkmcnt(0)
	s_barrier
	s_setprio 1
	s_waitcnt lgkmcnt(0)
	v_mfma_f32_16x16x32_bf16 v[122:125], v[140:143], v[184:187], v[122:125]
	v_mfma_f32_16x16x32_bf16 v[118:121], v[158:161], v[184:187], v[118:121]
	v_mfma_f32_16x16x32_bf16 v[110:113], v[140:143], v[192:195], v[110:113]
	v_mfma_f32_16x16x32_bf16 v[102:105], v[158:161], v[192:195], v[102:105]
	v_mfma_f32_16x16x32_bf16 v[94:97], v[140:143], v[208:211], v[94:97]
	v_mfma_f32_16x16x32_bf16 v[86:89], v[158:161], v[208:211], v[86:89]
	v_mfma_f32_16x16x32_bf16 v[78:81], v[140:143], v[216:219], v[78:81]
	v_mfma_f32_16x16x32_bf16 v[70:73], v[158:161], v[216:219], v[70:73]
	v_mfma_f32_16x16x32_bf16 v[122:125], v[144:147], v[188:191], v[122:125]
	v_mfma_f32_16x16x32_bf16 v[118:121], v[164:167], v[188:191], v[118:121]
	v_mfma_f32_16x16x32_bf16 v[110:113], v[144:147], v[204:207], v[110:113]
	v_mfma_f32_16x16x32_bf16 v[102:105], v[164:167], v[204:207], v[102:105]
	v_mfma_f32_16x16x32_bf16 v[94:97], v[144:147], v[212:215], v[94:97]
	v_mfma_f32_16x16x32_bf16 v[86:89], v[164:167], v[212:215], v[86:89]
	v_mfma_f32_16x16x32_bf16 v[78:81], v[144:147], v[220:223], v[78:81]
	v_mfma_f32_16x16x32_bf16 v[70:73], v[164:167], v[220:223], v[70:73]
	s_setprio 0
	s_setprio 1
	v_mfma_f32_16x16x32_bf16 v[126:129], v[168:171], v[184:187], v[126:129]
	v_mfma_f32_16x16x32_bf16 v[114:117], v[176:179], v[184:187], v[114:117]
	v_mfma_f32_16x16x32_bf16 v[106:109], v[168:171], v[192:195], v[106:109]
	v_mfma_f32_16x16x32_bf16 v[98:101], v[176:179], v[192:195], v[98:101]
	v_mfma_f32_16x16x32_bf16 v[90:93], v[168:171], v[208:211], v[90:93]
	v_mfma_f32_16x16x32_bf16 v[82:85], v[176:179], v[208:211], v[82:85]
	v_mfma_f32_16x16x32_bf16 v[74:77], v[168:171], v[216:219], v[74:77]
	v_mfma_f32_16x16x32_bf16 v[66:69], v[176:179], v[216:219], v[66:69]
	v_mfma_f32_16x16x32_bf16 v[126:129], v[172:175], v[188:191], v[126:129]
	v_mfma_f32_16x16x32_bf16 v[114:117], v[180:183], v[188:191], v[114:117]
	v_mfma_f32_16x16x32_bf16 v[106:109], v[172:175], v[204:207], v[106:109]
	v_mfma_f32_16x16x32_bf16 v[98:101], v[180:183], v[204:207], v[98:101]
	v_mfma_f32_16x16x32_bf16 v[90:93], v[172:175], v[212:215], v[90:93]
	v_mfma_f32_16x16x32_bf16 v[82:85], v[180:183], v[212:215], v[82:85]
	v_mfma_f32_16x16x32_bf16 v[74:77], v[172:175], v[220:223], v[74:77]
	v_mfma_f32_16x16x32_bf16 v[66:69], v[180:183], v[220:223], v[66:69]
	s_setprio 0
	s_barrier
	s_add_i32 s65, s65, s0
	v_lshl_add_u64 v[148:149], s[62:63], 0, v[0:1]
	s_mov_b32 m0, s65
	ds_read_b128 v[184:187], v156 offset:16384
	ds_read_b128 v[188:191], v156 offset:17408
	ds_read_b128 v[192:195], v156 offset:18432
	ds_read_b128 v[204:207], v156 offset:19456
	ds_read_b128 v[208:211], v156 offset:20480
	ds_read_b128 v[212:215], v156 offset:21504
	ds_read_b128 v[216:219], v156 offset:22528
	ds_read_b128 v[220:223], v156 offset:23552
	global_load_lds_dwordx4 v[148:149], off
	s_add_i32 m0, s65, 0x2000
	v_lshl_add_u64 v[196:197], s[62:63], 0, v[130:131]
	s_add_u32 s62, s62, s6
	s_addc_u32 s63, s63, s7
	s_add_i32 s61, s61, s0
	global_load_lds_dwordx4 v[196:197], off
	v_lshl_add_u64 v[198:199], s[62:63], 0, v[0:1]
	s_mov_b32 m0, s61
	v_lshl_add_u64 v[200:201], s[62:63], 0, v[130:131]
	global_load_lds_dwordx4 v[198:199], off
	s_add_i32 m0, s61, 0x2000
	v_lshl_add_u64 v[224:225], s[28:29], 0, v[134:135]
	global_load_lds_dwordx4 v[200:201], off
	s_mov_b32 m0, s41
	v_lshl_add_u64 v[226:227], s[28:29], 0, v[132:133]
	global_load_lds_dwordx4 v[224:225], off
	s_mov_b32 m0, s43
	s_nop 0
	global_load_lds_dwordx4 v[226:227], off
	s_waitcnt vmcnt(8)
	s_waitcnt lgkmcnt(0)
	s_barrier
; #define PG8_STAGE(bufoff, gbase, voff) do { _Pragma("unroll") for (int _i = 0; _i < 2; ++_i) \
;         __builtin_amdgcn_global_load_lds((const unsigned*)((const char*)(gbase) + (voff)[_i]), (PG8_LAS unsigned*)(lds + (bufoff) + ldsw + _i * 8192), 16, 0, 0); } while (0)
; #define PG8_WAIT_V(n) asm volatile("s_waitcnt vmcnt(" #n ")" ::: "memory")
; #define PG8_WAIT_L(n) asm volatile("s_waitcnt lgkmcnt(" #n ")" ::: "memory")
; #define PG8_BAR __builtin_amdgcn_s_barrier()
; #define PG8_SCHED __builtin_amdgcn_sched_barrier(0)
; template <class Epi, class Sched, bool ALIGN_EPI = false, bool SP2 = false, bool F8 = false>
; __device__ __forceinline__ void gemm_phase(PG8_LAS unsigned char* lds, const Gemm g, const Sched& S, const Epi& E, const int tidb  ) {
;     ...
;             PG8_WAIT_V(8); PG8_WAIT_L(0); PG8_BAR; PG8_MMA(1, 0, At, B0); PG8_MMA(1, 1, At, B1); PG8_BAR; PG8_SCHED;
;             PG8_LDB(B0, 1, 0); PG8_LDB(B1, 1, 1); PG8_SCHED; PG8_LDA(At, 1, 0); PG8_STAGE(PG8_SA(0, 1), a2 + hstep, voffA);
;             PG8_WAIT_V(8); PG8_WAIT_L(0); PG8_BAR; PG8_MMA(0, 0, At, B0); PG8_MMA(0, 1, At, B1); PG8_BAR; PG8_SCHED;
	s_setprio 1
	s_waitcnt lgkmcnt(0)
	v_mfma_f32_16x16x32_bf16 v[62:65], v[140:143], v[184:187], v[62:65]
	v_mfma_f32_16x16x32_bf16 v[54:57], v[158:161], v[184:187], v[54:57]
	v_mfma_f32_16x16x32_bf16 v[46:49], v[140:143], v[192:195], v[46:49]
	v_mfma_f32_16x16x32_bf16 v[38:41], v[158:161], v[192:195], v[38:41]
	v_mfma_f32_16x16x32_bf16 v[30:33], v[140:143], v[208:211], v[30:33]
	v_mfma_f32_16x16x32_bf16 v[22:25], v[158:161], v[208:211], v[22:25]
	v_mfma_f32_16x16x32_bf16 v[14:17], v[140:143], v[216:219], v[14:17]
	v_mfma_f32_16x16x32_bf16 v[6:9], v[158:161], v[216:219], v[6:9]
	v_mfma_f32_16x16x32_bf16 v[62:65], v[144:147], v[188:191], v[62:65]
	v_mfma_f32_16x16x32_bf16 v[54:57], v[164:167], v[188:191], v[54:57]
	v_mfma_f32_16x16x32_bf16 v[46:49], v[144:147], v[204:207], v[46:49]
	v_mfma_f32_16x16x32_bf16 v[38:41], v[164:167], v[204:207], v[38:41]
	v_mfma_f32_16x16x32_bf16 v[30:33], v[144:147], v[212:215], v[30:33]
	v_mfma_f32_16x16x32_bf16 v[22:25], v[164:167], v[212:215], v[22:25]
	v_mfma_f32_16x16x32_bf16 v[14:17], v[144:147], v[220:223], v[14:17]
	v_mfma_f32_16x16x32_bf16 v[6:9], v[164:167], v[220:223], v[6:9]
	s_setprio 0
	s_setprio 1
	v_mfma_f32_16x16x32_bf16 v[58:61], v[168:171], v[184:187], v[58:61]
	v_mfma_f32_16x16x32_bf16 v[50:53], v[176:179], v[184:187], v[50:53]
	v_mfma_f32_16x16x32_bf16 v[42:45], v[168:171], v[192:195], v[42:45]
	v_mfma_f32_16x16x32_bf16 v[34:37], v[176:179], v[192:195], v[34:37]
	v_mfma_f32_16x16x32_bf16 v[26:29], v[168:171], v[208:211], v[26:29]
	v_mfma_f32_16x16x32_bf16 v[18:21], v[176:179], v[208:211], v[18:21]
	v_mfma_f32_16x16x32_bf16 v[10:13], v[168:171], v[216:219], v[10:13]
	v_mfma_f32_16x16x32_bf16 v[2:5], v[176:179], v[216:219], v[2:5]
	v_mfma_f32_16x16x32_bf16 v[58:61], v[172:175], v[188:191], v[58:61]
	v_mfma_f32_16x16x32_bf16 v[50:53], v[180:183], v[188:191], v[50:53]
	v_mfma_f32_16x16x32_bf16 v[42:45], v[172:175], v[204:207], v[42:45]
	v_mfma_f32_16x16x32_bf16 v[34:37], v[180:183], v[204:207], v[34:37]
	v_mfma_f32_16x16x32_bf16 v[26:29], v[172:175], v[212:215], v[26:29]
	v_mfma_f32_16x16x32_bf16 v[18:21], v[180:183], v[212:215], v[18:21]
	v_mfma_f32_16x16x32_bf16 v[10:13], v[172:175], v[220:223], v[10:13]
	v_mfma_f32_16x16x32_bf16 v[2:5], v[180:183], v[220:223], v[2:5]
	s_setprio 0
	s_barrier
	s_add_i32 s61, 0, 0x18000
	v_add_u32_e32 v157, s61, v151
	s_add_i32 s62, 0, 0x1c000
	ds_read_b128 v[140:143], v157
	ds_read_b128 v[144:147], v157 offset:1024
	ds_read_b128 v[158:161], v157 offset:2048
	ds_read_b128 v[164:167], v157 offset:3072
	v_add_u32_e32 v157, s62, v151
	ds_read_b128 v[168:171], v157
	ds_read_b128 v[172:175], v157 offset:1024
	ds_read_b128 v[176:179], v157 offset:2048
	ds_read_b128 v[180:183], v157 offset:3072
	s_add_u32 s28, s28, s6
	s_addc_u32 s29, s29, s7
	s_mov_b32 m0, s45
	v_lshl_add_u64 v[228:229], s[28:29], 0, v[134:135]
	ds_read_b128 v[184:187], v156 offset:32768
	ds_read_b128 v[188:191], v156 offset:33792
	ds_read_b128 v[192:195], v156 offset:34816
	ds_read_b128 v[204:207], v156 offset:35840
	ds_read_b128 v[208:211], v156 offset:36864
	ds_read_b128 v[212:215], v156 offset:37888
	ds_read_b128 v[216:219], v156 offset:38912
	ds_read_b128 v[220:223], v156 offset:39936
	global_load_lds_dwordx4 v[228:229], off
	v_lshl_add_u64 v[228:229], s[28:29], 0, v[132:133]
	s_mov_b32 m0, s46
	s_nop 0
	global_load_lds_dwordx4 v[228:229], off
	s_waitcnt vmcnt(8)
	s_waitcnt lgkmcnt(0)
	s_barrier
	s_setprio 1
	s_waitcnt lgkmcnt(0)
	v_mfma_f32_16x16x32_bf16 v[122:125], v[140:143], v[184:187], v[122:125]
	v_mfma_f32_16x16x32_bf16 v[118:121], v[158:161], v[184:187], v[118:121]
	v_mfma_f32_16x16x32_bf16 v[110:113], v[140:143], v[192:195], v[110:113]
	v_mfma_f32_16x16x32_bf16 v[102:105], v[158:161], v[192:195], v[102:105]
	v_mfma_f32_16x16x32_bf16 v[94:97], v[140:143], v[208:211], v[94:97]
	v_mfma_f32_16x16x32_bf16 v[86:89], v[158:161], v[208:211], v[86:89]
	v_mfma_f32_16x16x32_bf16 v[78:81], v[140:143], v[216:219], v[78:81]
	v_mfma_f32_16x16x32_bf16 v[70:73], v[158:161], v[216:219], v[70:73]
	v_mfma_f32_16x16x32_bf16 v[122:125], v[144:147], v[188:191], v[122:125]
	v_mfma_f32_16x16x32_bf16 v[118:121], v[164:167], v[188:191], v[118:121]
	v_mfma_f32_16x16x32_bf16 v[110:113], v[144:147], v[204:207], v[110:113]
	v_mfma_f32_16x16x32_bf16 v[102:105], v[164:167], v[204:207], v[102:105]
	v_mfma_f32_16x16x32_bf16 v[94:97], v[144:147], v[212:215], v[94:97]
	v_mfma_f32_16x16x32_bf16 v[86:89], v[164:167], v[212:215], v[86:89]
	v_mfma_f32_16x16x32_bf16 v[78:81], v[144:147], v[220:223], v[78:81]
	v_mfma_f32_16x16x32_bf16 v[70:73], v[164:167], v[220:223], v[70:73]
	s_setprio 0
	s_setprio 1
	v_mfma_f32_16x16x32_bf16 v[126:129], v[168:171], v[184:187], v[126:129]
	v_mfma_f32_16x16x32_bf16 v[114:117], v[176:179], v[184:187], v[114:117]
	v_mfma_f32_16x16x32_bf16 v[106:109], v[168:171], v[192:195], v[106:109]
	v_mfma_f32_16x16x32_bf16 v[98:101], v[176:179], v[192:195], v[98:101]
	v_mfma_f32_16x16x32_bf16 v[90:93], v[168:171], v[208:211], v[90:93]
	v_mfma_f32_16x16x32_bf16 v[82:85], v[176:179], v[208:211], v[82:85]
	v_mfma_f32_16x16x32_bf16 v[74:77], v[168:171], v[216:219], v[74:77]
	v_mfma_f32_16x16x32_bf16 v[66:69], v[176:179], v[216:219], v[66:69]
	v_mfma_f32_16x16x32_bf16 v[126:129], v[172:175], v[188:191], v[126:129]
	v_mfma_f32_16x16x32_bf16 v[114:117], v[180:183], v[188:191], v[114:117]
	v_mfma_f32_16x16x32_bf16 v[106:109], v[172:175], v[204:207], v[106:109]
	v_mfma_f32_16x16x32_bf16 v[98:101], v[180:183], v[204:207], v[98:101]
	v_mfma_f32_16x16x32_bf16 v[90:93], v[172:175], v[212:215], v[90:93]
	v_mfma_f32_16x16x32_bf16 v[82:85], v[180:183], v[212:215], v[82:85]
	v_mfma_f32_16x16x32_bf16 v[74:77], v[172:175], v[220:223], v[74:77]
	v_mfma_f32_16x16x32_bf16 v[66:69], v[180:183], v[220:223], v[66:69]
	s_setprio 0
	s_barrier
; #define PG8_STAGE(bufoff, gbase, voff) do { _Pragma("unroll") for (int _i = 0; _i < 2; ++_i) \
;         __builtin_amdgcn_global_load_lds((const unsigned*)((const char*)(gbase) + (voff)[_i]), (PG8_LAS unsigned*)(lds + (bufoff) + ldsw + _i * 8192), 16, 0, 0); } while (0)
; #define PG8_WAIT_V(n) asm volatile("s_waitcnt vmcnt(" #n ")" ::: "memory")
; #define PG8_WAIT_L(n) asm volatile("s_waitcnt lgkmcnt(" #n ")" ::: "memory")
; #define PG8_BAR __builtin_amdgcn_s_barrier()
; #define PG8_SCHED __builtin_amdgcn_sched_barrier(0)
; template <class Epi, class Sched, bool ALIGN_EPI = false, bool SP2 = false, bool F8 = false>
; __device__ __forceinline__ void gemm_phase(PG8_LAS unsigned char* lds, const Gemm g, const Sched& S, const Epi& E, const int tidb  ) {
;     ...
;         for (int t = 0; t < nt; t += 2) {
;             const bool last = (t == nt - 2);
;             if constexpr (Epi::PREFETCH) { if (t == 0) E.prefetch(cur, wid, lane); }
;             const char* a1 = cA + (size_t)(t + 1) * kstep;
;             const char* a2 = last ? nA : cA + (size_t)(t + 2) * kstep; const char* b2 = last ? nB : cB + (size_t)(t + 2) * kstep;
;             const char* a3 = a2 + kstep; const char* b3 = b2 + kstep;
;     ...
;             PG8_LDA(At, 1, 1); PG8_STAGE(PG8_SB(1, 0), b3, voffB); PG8_STAGE(PG8_SB(1, 1), b3 + hstep, voffB); PG8_STAGE(PG8_SA(1, 0), a3, voffA);
;             PG8_WAIT_V(8); PG8_WAIT_L(0); PG8_BAR; PG8_MMA(1, 0, At, B0); PG8_MMA(1, 1, At, B1); PG8_BAR; PG8_SCHED;
	s_add_i32 s28, s61, s0
	v_lshl_add_u64 v[148:149], v[148:149], 0, s[92:93]
	s_mov_b32 m0, s28
	ds_read_b128 v[184:187], v156 offset:49152
	ds_read_b128 v[188:191], v156 offset:50176
	ds_read_b128 v[192:195], v156 offset:51200
	ds_read_b128 v[204:207], v156 offset:52224
	ds_read_b128 v[208:211], v156 offset:53248
	ds_read_b128 v[212:215], v156 offset:54272
	ds_read_b128 v[216:219], v156 offset:55296
	ds_read_b128 v[220:223], v156 offset:56320
	global_load_lds_dwordx4 v[148:149], off
	v_lshl_add_u64 v[148:149], v[196:197], 0, s[92:93]
	s_add_i32 m0, s28, 0x2000
	s_add_i32 s28, s62, s0
	global_load_lds_dwordx4 v[148:149], off
	v_lshl_add_u64 v[148:149], v[198:199], 0, s[92:93]
	s_mov_b32 m0, s28
	s_nop 0
	global_load_lds_dwordx4 v[148:149], off
	v_lshl_add_u64 v[148:149], v[200:201], 0, s[92:93]
	s_add_i32 m0, s28, 0x2000
	s_nop 0
	global_load_lds_dwordx4 v[148:149], off
	v_lshl_add_u64 v[148:149], v[224:225], 0, s[92:93]
	s_mov_b32 m0, s47
	s_nop 0
	global_load_lds_dwordx4 v[148:149], off
	v_lshl_add_u64 v[148:149], v[226:227], 0, s[92:93]
	s_mov_b32 m0, s48
	s_nop 0
	global_load_lds_dwordx4 v[148:149], off
	s_waitcnt vmcnt(8)
	s_waitcnt lgkmcnt(0)
	s_barrier
	s_setprio 1
	s_waitcnt lgkmcnt(0)
	v_mfma_f32_16x16x32_bf16 v[62:65], v[140:143], v[184:187], v[62:65]
	v_mfma_f32_16x16x32_bf16 v[54:57], v[158:161], v[184:187], v[54:57]
	v_mfma_f32_16x16x32_bf16 v[46:49], v[140:143], v[192:195], v[46:49]
	v_mfma_f32_16x16x32_bf16 v[38:41], v[158:161], v[192:195], v[38:41]
	v_mfma_f32_16x16x32_bf16 v[30:33], v[140:143], v[208:211], v[30:33]
	v_mfma_f32_16x16x32_bf16 v[22:25], v[158:161], v[208:211], v[22:25]
	v_mfma_f32_16x16x32_bf16 v[14:17], v[140:143], v[216:219], v[14:17]
	v_mfma_f32_16x16x32_bf16 v[6:9], v[158:161], v[216:219], v[6:9]
	v_mfma_f32_16x16x32_bf16 v[62:65], v[144:147], v[188:191], v[62:65]
	v_mfma_f32_16x16x32_bf16 v[54:57], v[164:167], v[188:191], v[54:57]
	v_mfma_f32_16x16x32_bf16 v[46:49], v[144:147], v[204:207], v[46:49]
	v_mfma_f32_16x16x32_bf16 v[38:41], v[164:167], v[204:207], v[38:41]
	v_mfma_f32_16x16x32_bf16 v[30:33], v[144:147], v[212:215], v[30:33]
	v_mfma_f32_16x16x32_bf16 v[22:25], v[164:167], v[212:215], v[22:25]
	v_mfma_f32_16x16x32_bf16 v[14:17], v[144:147], v[220:223], v[14:17]
	v_mfma_f32_16x16x32_bf16 v[6:9], v[164:167], v[220:223], v[6:9]
	s_setprio 0
	s_setprio 1
	v_mfma_f32_16x16x32_bf16 v[58:61], v[168:171], v[184:187], v[58:61]
	v_mfma_f32_16x16x32_bf16 v[50:53], v[176:179], v[184:187], v[50:53]
	v_mfma_f32_16x16x32_bf16 v[42:45], v[168:171], v[192:195], v[42:45]
	v_mfma_f32_16x16x32_bf16 v[34:37], v[176:179], v[192:195], v[34:37]
	v_mfma_f32_16x16x32_bf16 v[26:29], v[168:171], v[208:211], v[26:29]
	v_mfma_f32_16x16x32_bf16 v[18:21], v[176:179], v[208:211], v[18:21]
	v_mfma_f32_16x16x32_bf16 v[10:13], v[168:171], v[216:219], v[10:13]
	v_mfma_f32_16x16x32_bf16 v[2:5], v[176:179], v[216:219], v[2:5]
	v_mfma_f32_16x16x32_bf16 v[58:61], v[172:175], v[188:191], v[58:61]
	v_mfma_f32_16x16x32_bf16 v[50:53], v[180:183], v[188:191], v[50:53]
	v_mfma_f32_16x16x32_bf16 v[42:45], v[172:175], v[204:207], v[42:45]
	v_mfma_f32_16x16x32_bf16 v[34:37], v[180:183], v[204:207], v[34:37]
	v_mfma_f32_16x16x32_bf16 v[26:29], v[172:175], v[212:215], v[26:29]
	v_mfma_f32_16x16x32_bf16 v[18:21], v[180:183], v[212:215], v[18:21]
	v_mfma_f32_16x16x32_bf16 v[10:13], v[172:175], v[220:223], v[10:13]
	v_mfma_f32_16x16x32_bf16 v[2:5], v[180:183], v[220:223], v[2:5]
	s_setprio 0
	s_add_u32 s26, s26, 0x100
	s_addc_u32 s27, s27, 0
	s_add_u32 s58, s58, 0x100
	s_addc_u32 s59, s59, 0
	s_cmp_ge_i32 s60, s49
	s_mov_b32 s28, s60
	s_barrier
	s_cbranch_scc0 .LBB0_1705

;     __device__ __forceinline__ bool next(int i, Unit& u) const { return so.next(i, u); }
; #define PG8_STAGE(bufoff, gbase, voff) do { _Pragma("unroll") for (int _i = 0; _i < 2; ++_i) \
;         __builtin_amdgcn_global_load_lds((const unsigned*)((const char*)(gbase) + (voff)[_i]), (PG8_LAS unsigned*)(lds + (bufoff) + ldsw + _i * 8192), 16, 0, 0); } while (0)
; #define PG8_WAIT_V(n) asm volatile("s_waitcnt vmcnt(" #n ")" ::: "memory")
; #define PG8_WAIT_L(n) asm volatile("s_waitcnt lgkmcnt(" #n ")" ::: "memory")
; #define PG8_BAR __builtin_amdgcn_s_barrier()
; #define PG8_SCHED __builtin_amdgcn_sched_barrier(0)
; template <class Epi, class Sched, bool ALIGN_EPI = false, bool SP2 = false, bool F8 = false>
; __device__ __forceinline__ void gemm_phase(PG8_LAS unsigned char* lds, const Gemm g, const Sched& S, const Epi& E, const int tidb  ) {
;     ...
;         const bool has_next = S.next(ui + 1, nxt);
;         const char* nA = has_next ? (const char*)g.A + (size_t)nxt.pm * tstep : cA; const char* nB = has_next ? (const char*)g.Bt + S.boff(nxt) + (size_t)nxt.pn * tstep : cB;
;         for (int t = 0; t < nt; t += 2) {
;             const bool last = (t == nt - 2);
;             if constexpr (Epi::PREFETCH) { if (t == 0) E.prefetch(cur, wid, lane); }
;             const char* a1 = cA + (size_t)(t + 1) * kstep;
;             const char* a2 = last ? nA : cA + (size_t)(t + 2) * kstep; const char* b2 = last ? nB : cB + (size_t)(t + 2) * kstep;
;             const char* a3 = a2 + kstep; const char* b3 = b2 + kstep;
;             if (last && has_next) S.a_ready(nxt);
;             if constexpr (SP2) {
;             PG8_LDB(B0, 0, 0); PG8_LDB(B1, 0, 1); PG8_SCHED; PG8_LDA(At, 0, 0); PG8_STAGE(PG8_SA(1, 1), a1 + hstep, voffA);
;             PG8_WAIT_V(8); PG8_WAIT_L(0); PG8_BAR; PG8_MMA(0, 0, At, B0); PG8_MMA(0, 1, At, B1); PG8_BAR; PG8_SCHED;
;             PG8_LDA(At, 0, 1); PG8_STAGE(PG8_SB(0, 0), b2, voffB); PG8_STAGE(PG8_SB(0, 1), b2 + hstep, voffB); PG8_STAGE(PG8_SA(0, 0), a2, voffA);
;             PG8_WAIT_V(8); PG8_WAIT_L(0); PG8_BAR; PG8_MMA(1, 0, At, B0); PG8_MMA(1, 1, At, B1); PG8_BAR; PG8_SCHED;
.LBB0_1728:
	s_add_i32 s60, s26, 2
	s_add_u32 s28, s24, 0x80
	s_addc_u32 s27, s25, 0
	s_add_i32 s61, 0, 0x10000
	s_cmp_eq_u32 s51, s26
	s_cselect_b32 s27, s5, s27
	s_cselect_b32 s26, s4, s28
	s_cselect_b32 s29, s23, s59
	s_cselect_b32 s28, s22, s58
	s_add_i32 s62, 0, 0x14000
	v_add_u32_e32 v2, s61, v186
	v_add_u32_e32 v14, s62, v186
	ds_read_b128 v[18:21], v2
	ds_read_b128 v[22:25], v2 offset:1024
	ds_read_b128 v[26:29], v2 offset:2048
	ds_read_b128 v[30:33], v2 offset:3072
	ds_read_b128 v[2:5], v14
	ds_read_b128 v[6:9], v14 offset:1024
	ds_read_b128 v[10:13], v14 offset:2048
	ds_read_b128 v[14:17], v14 offset:3072
	v_lshl_add_u64 v[182:183], s[24:25], 0, v[170:171]
	s_add_i32 m0, s41, 0xc000
	ds_read_b128 v[174:177], v191
	ds_read_b128 v[178:181], v191 offset:1024
	ds_read_b128 v[204:207], v191 offset:2048
	ds_read_b128 v[208:211], v191 offset:3072
	ds_read_b128 v[212:215], v191 offset:4096
	ds_read_b128 v[216:219], v191 offset:5120
	ds_read_b128 v[220:223], v191 offset:6144
	ds_read_b128 v[224:227], v191 offset:7168
	global_load_lds_dwordx4 v[182:183], off
	v_lshl_add_u64 v[182:183], s[24:25], 0, v[172:173]
	s_add_i32 m0, s41, 0xe000
	s_nop 0
	global_load_lds_dwordx4 v[182:183], off
	s_waitcnt vmcnt(8)
	s_waitcnt lgkmcnt(0)
	s_barrier
	s_setprio 1
	s_waitcnt lgkmcnt(0)
	v_mfma_scale_f32_16x16x128_f8f6f4 v[154:157], v[18:25], v[174:181], v[154:157], v246, v247 op_sel_hi:[0,0,0]
	v_mfma_scale_f32_16x16x128_f8f6f4 v[150:153], v[26:33], v[174:181], v[150:153], v246, v247 op_sel_hi:[0,0,0]
	v_mfma_scale_f32_16x16x128_f8f6f4 v[142:145], v[18:25], v[204:211], v[142:145], v246, v247 op_sel_hi:[0,0,0]
	v_mfma_scale_f32_16x16x128_f8f6f4 v[134:137], v[26:33], v[204:211], v[134:137], v246, v247 op_sel_hi:[0,0,0]
	v_mfma_scale_f32_16x16x128_f8f6f4 v[126:129], v[18:25], v[212:219], v[126:129], v246, v247 op_sel_hi:[0,0,0]
	v_mfma_scale_f32_16x16x128_f8f6f4 v[118:121], v[26:33], v[212:219], v[118:121], v246, v247 op_sel_hi:[0,0,0]
	v_mfma_scale_f32_16x16x128_f8f6f4 v[110:113], v[18:25], v[220:227], v[110:113], v246, v247 op_sel_hi:[0,0,0]
	v_mfma_scale_f32_16x16x128_f8f6f4 v[102:105], v[26:33], v[220:227], v[102:105], v246, v247 op_sel_hi:[0,0,0]
	s_setprio 0
	s_setprio 1
	v_mfma_scale_f32_16x16x128_f8f6f4 v[158:161], v[2:9], v[174:181], v[158:161], v246, v247 op_sel_hi:[0,0,0]
	v_mfma_scale_f32_16x16x128_f8f6f4 v[146:149], v[10:17], v[174:181], v[146:149], v246, v247 op_sel_hi:[0,0,0]
	v_mfma_scale_f32_16x16x128_f8f6f4 v[138:141], v[2:9], v[204:211], v[138:141], v246, v247 op_sel_hi:[0,0,0]
	v_mfma_scale_f32_16x16x128_f8f6f4 v[130:133], v[10:17], v[204:211], v[130:133], v246, v247 op_sel_hi:[0,0,0]
	v_mfma_scale_f32_16x16x128_f8f6f4 v[122:125], v[2:9], v[212:219], v[122:125], v246, v247 op_sel_hi:[0,0,0]
	v_mfma_scale_f32_16x16x128_f8f6f4 v[114:117], v[10:17], v[212:219], v[114:117], v246, v247 op_sel_hi:[0,0,0]
	v_mfma_scale_f32_16x16x128_f8f6f4 v[106:109], v[2:9], v[220:227], v[106:109], v246, v247 op_sel_hi:[0,0,0]
	v_mfma_scale_f32_16x16x128_f8f6f4 v[98:101], v[10:17], v[220:227], v[98:101], v246, v247 op_sel_hi:[0,0,0]
	s_setprio 0
	s_barrier
	s_add_i32 s61, s61, s36
	v_lshl_add_u64 v[174:175], s[28:29], 0, v[0:1]
	s_mov_b32 m0, s61
	ds_read_b128 v[204:207], v191 offset:16384
	ds_read_b128 v[208:211], v191 offset:17408
	ds_read_b128 v[212:215], v191 offset:18432
	ds_read_b128 v[216:219], v191 offset:19456
	ds_read_b128 v[220:223], v191 offset:20480
	ds_read_b128 v[224:227], v191 offset:21504
	ds_read_b128 v[228:231], v191 offset:22528
	ds_read_b128 v[232:235], v191 offset:23552
	global_load_lds_dwordx4 v[174:175], off
	s_add_i32 m0, s61, 0x2000
	v_lshl_add_u64 v[176:177], s[28:29], 0, v[164:165]
	s_add_u32 s28, s28, s6
	s_addc_u32 s29, s29, s7
	s_add_i32 s61, s62, s36
	global_load_lds_dwordx4 v[176:177], off
	v_lshl_add_u64 v[178:179], s[28:29], 0, v[0:1]
	s_mov_b32 m0, s61
	v_lshl_add_u64 v[180:181], s[28:29], 0, v[164:165]
	global_load_lds_dwordx4 v[178:179], off
	s_add_i32 m0, s61, 0x2000
	v_lshl_add_u64 v[182:183], s[26:27], 0, v[168:169]
	global_load_lds_dwordx4 v[180:181], off
	s_mov_b32 m0, s41
	v_lshl_add_u64 v[184:185], s[26:27], 0, v[166:167]
	global_load_lds_dwordx4 v[182:183], off
	s_mov_b32 m0, s43
	s_nop 0
	global_load_lds_dwordx4 v[184:185], off
	s_waitcnt vmcnt(8)
	s_waitcnt lgkmcnt(0)
	s_barrier
	s_setprio 1
	s_waitcnt lgkmcnt(0)
	v_mfma_scale_f32_16x16x128_f8f6f4 v[94:97], v[18:25], v[204:211], v[94:97], v246, v247 op_sel_hi:[0,0,0]
	v_mfma_scale_f32_16x16x128_f8f6f4 v[86:89], v[26:33], v[204:211], v[86:89], v246, v247 op_sel_hi:[0,0,0]
	v_mfma_scale_f32_16x16x128_f8f6f4 v[78:81], v[18:25], v[212:219], v[78:81], v246, v247 op_sel_hi:[0,0,0]
	v_mfma_scale_f32_16x16x128_f8f6f4 v[70:73], v[26:33], v[212:219], v[70:73], v246, v247 op_sel_hi:[0,0,0]
	v_mfma_scale_f32_16x16x128_f8f6f4 v[62:65], v[18:25], v[220:227], v[62:65], v246, v247 op_sel_hi:[0,0,0]
	v_mfma_scale_f32_16x16x128_f8f6f4 v[54:57], v[26:33], v[220:227], v[54:57], v246, v247 op_sel_hi:[0,0,0]
	v_mfma_scale_f32_16x16x128_f8f6f4 v[46:49], v[18:25], v[228:235], v[46:49], v246, v247 op_sel_hi:[0,0,0]
	v_mfma_scale_f32_16x16x128_f8f6f4 v[38:41], v[26:33], v[228:235], v[38:41], v246, v247 op_sel_hi:[0,0,0]
	s_setprio 0
	s_setprio 1
	v_mfma_scale_f32_16x16x128_f8f6f4 v[90:93], v[2:9], v[204:211], v[90:93], v246, v247 op_sel_hi:[0,0,0]
	v_mfma_scale_f32_16x16x128_f8f6f4 v[82:85], v[10:17], v[204:211], v[82:85], v246, v247 op_sel_hi:[0,0,0]
	v_mfma_scale_f32_16x16x128_f8f6f4 v[74:77], v[2:9], v[212:219], v[74:77], v246, v247 op_sel_hi:[0,0,0]
	v_mfma_scale_f32_16x16x128_f8f6f4 v[66:69], v[10:17], v[212:219], v[66:69], v246, v247 op_sel_hi:[0,0,0]
	v_mfma_scale_f32_16x16x128_f8f6f4 v[58:61], v[2:9], v[220:227], v[58:61], v246, v247 op_sel_hi:[0,0,0]
	v_mfma_scale_f32_16x16x128_f8f6f4 v[50:53], v[10:17], v[220:227], v[50:53], v246, v247 op_sel_hi:[0,0,0]
	v_mfma_scale_f32_16x16x128_f8f6f4 v[42:45], v[2:9], v[228:235], v[42:45], v246, v247 op_sel_hi:[0,0,0]
	v_mfma_scale_f32_16x16x128_f8f6f4 v[34:37], v[10:17], v[228:235], v[34:37], v246, v247 op_sel_hi:[0,0,0]
	s_setprio 0
	s_barrier
; #define PG8_STAGE(bufoff, gbase, voff) do { _Pragma("unroll") for (int _i = 0; _i < 2; ++_i) \
;         __builtin_amdgcn_global_load_lds((const unsigned*)((const char*)(gbase) + (voff)[_i]), (PG8_LAS unsigned*)(lds + (bufoff) + ldsw + _i * 8192), 16, 0, 0); } while (0)
; #define PG8_WAIT_V(n) asm volatile("s_waitcnt vmcnt(" #n ")" ::: "memory")
; #define PG8_WAIT_L(n) asm volatile("s_waitcnt lgkmcnt(" #n ")" ::: "memory")
; #define PG8_BAR __builtin_amdgcn_s_barrier()
; #define PG8_SCHED __builtin_amdgcn_sched_barrier(0)
; template <class Epi, class Sched, bool ALIGN_EPI = false, bool SP2 = false, bool F8 = false>
; __device__ __forceinline__ void gemm_phase(PG8_LAS unsigned char* lds, const Gemm g, const Sched& S, const Epi& E, const int tidb  ) {
;     ...
;             PG8_LDB(B0, 1, 0); PG8_LDB(B1, 1, 1); PG8_SCHED; PG8_LDA(At, 1, 0); PG8_STAGE(PG8_SA(0, 1), a2 + hstep, voffA);
;             PG8_WAIT_V(8); PG8_WAIT_L(0); PG8_BAR; PG8_MMA(0, 0, At, B0); PG8_MMA(0, 1, At, B1); PG8_BAR; PG8_SCHED;
;             PG8_LDA(At, 1, 1); PG8_STAGE(PG8_SB(1, 0), b3, voffB); PG8_STAGE(PG8_SB(1, 1), b3 + hstep, voffB); PG8_STAGE(PG8_SA(1, 0), a3, voffA);
;             PG8_WAIT_V(8); PG8_WAIT_L(0); PG8_BAR; PG8_MMA(1, 0, At, B0); PG8_MMA(1, 1, At, B1); PG8_BAR; PG8_SCHED;
	s_add_i32 s28, 0, 0x18000
	s_add_i32 s29, 0, 0x1c000
	v_add_u32_e32 v14, s28, v186
	v_add_u32_e32 v30, s29, v186
	ds_read_b128 v[2:5], v14
	ds_read_b128 v[6:9], v14 offset:1024
	ds_read_b128 v[10:13], v14 offset:2048
	ds_read_b128 v[14:17], v14 offset:3072
	ds_read_b128 v[18:21], v30
	ds_read_b128 v[22:25], v30 offset:1024
	ds_read_b128 v[26:29], v30 offset:2048
	ds_read_b128 v[30:33], v30 offset:3072
	s_add_u32 s26, s26, s6
	s_addc_u32 s27, s27, s7
	s_mov_b32 m0, s45
	v_lshl_add_u64 v[192:193], s[26:27], 0, v[168:169]
	ds_read_b128 v[204:207], v191 offset:32768
	ds_read_b128 v[208:211], v191 offset:33792
	ds_read_b128 v[212:215], v191 offset:34816
	ds_read_b128 v[216:219], v191 offset:35840
	ds_read_b128 v[220:223], v191 offset:36864
	ds_read_b128 v[224:227], v191 offset:37888
	ds_read_b128 v[228:231], v191 offset:38912
	ds_read_b128 v[232:235], v191 offset:39936
	global_load_lds_dwordx4 v[192:193], off
	v_lshl_add_u64 v[192:193], s[26:27], 0, v[166:167]
	s_mov_b32 m0, s46
	s_nop 0
	global_load_lds_dwordx4 v[192:193], off
	s_waitcnt vmcnt(8)
	s_waitcnt lgkmcnt(0)
	s_barrier
	s_setprio 1
	s_waitcnt lgkmcnt(0)
	v_mfma_scale_f32_16x16x128_f8f6f4 v[154:157], v[2:9], v[204:211], v[154:157], v246, v247 op_sel_hi:[0,0,0]
	v_mfma_scale_f32_16x16x128_f8f6f4 v[150:153], v[10:17], v[204:211], v[150:153], v246, v247 op_sel_hi:[0,0,0]
	v_mfma_scale_f32_16x16x128_f8f6f4 v[142:145], v[2:9], v[212:219], v[142:145], v246, v247 op_sel_hi:[0,0,0]
	v_mfma_scale_f32_16x16x128_f8f6f4 v[134:137], v[10:17], v[212:219], v[134:137], v246, v247 op_sel_hi:[0,0,0]
	v_mfma_scale_f32_16x16x128_f8f6f4 v[126:129], v[2:9], v[220:227], v[126:129], v246, v247 op_sel_hi:[0,0,0]
	v_mfma_scale_f32_16x16x128_f8f6f4 v[118:121], v[10:17], v[220:227], v[118:121], v246, v247 op_sel_hi:[0,0,0]
	v_mfma_scale_f32_16x16x128_f8f6f4 v[110:113], v[2:9], v[228:235], v[110:113], v246, v247 op_sel_hi:[0,0,0]
	v_mfma_scale_f32_16x16x128_f8f6f4 v[102:105], v[10:17], v[228:235], v[102:105], v246, v247 op_sel_hi:[0,0,0]
	s_setprio 0
	s_setprio 1
	v_mfma_scale_f32_16x16x128_f8f6f4 v[158:161], v[18:25], v[204:211], v[158:161], v246, v247 op_sel_hi:[0,0,0]
	v_mfma_scale_f32_16x16x128_f8f6f4 v[146:149], v[26:33], v[204:211], v[146:149], v246, v247 op_sel_hi:[0,0,0]
	v_mfma_scale_f32_16x16x128_f8f6f4 v[138:141], v[18:25], v[212:219], v[138:141], v246, v247 op_sel_hi:[0,0,0]
	v_mfma_scale_f32_16x16x128_f8f6f4 v[130:133], v[26:33], v[212:219], v[130:133], v246, v247 op_sel_hi:[0,0,0]
	v_mfma_scale_f32_16x16x128_f8f6f4 v[122:125], v[18:25], v[220:227], v[122:125], v246, v247 op_sel_hi:[0,0,0]
	v_mfma_scale_f32_16x16x128_f8f6f4 v[114:117], v[26:33], v[220:227], v[114:117], v246, v247 op_sel_hi:[0,0,0]
	v_mfma_scale_f32_16x16x128_f8f6f4 v[106:109], v[18:25], v[228:235], v[106:109], v246, v247 op_sel_hi:[0,0,0]
	v_mfma_scale_f32_16x16x128_f8f6f4 v[98:101], v[26:33], v[228:235], v[98:101], v246, v247 op_sel_hi:[0,0,0]
	s_setprio 0
	s_barrier
	s_add_i32 s26, s28, s36
	v_lshl_add_u64 v[174:175], v[174:175], 0, s[92:93]
	s_mov_b32 m0, s26
	ds_read_b128 v[204:207], v191 offset:49152
	ds_read_b128 v[208:211], v191 offset:50176
	ds_read_b128 v[212:215], v191 offset:51200
	ds_read_b128 v[216:219], v191 offset:52224
	ds_read_b128 v[220:223], v191 offset:53248
	ds_read_b128 v[224:227], v191 offset:54272
	ds_read_b128 v[228:231], v191 offset:55296
	ds_read_b128 v[232:235], v191 offset:56320
	global_load_lds_dwordx4 v[174:175], off
	v_lshl_add_u64 v[174:175], v[176:177], 0, s[92:93]
	s_add_i32 m0, s26, 0x2000
	s_add_i32 s26, s29, s36
	global_load_lds_dwordx4 v[174:175], off
	v_lshl_add_u64 v[174:175], v[178:179], 0, s[92:93]
	s_mov_b32 m0, s26
	s_nop 0
	global_load_lds_dwordx4 v[174:175], off
	v_lshl_add_u64 v[174:175], v[180:181], 0, s[92:93]
	s_add_i32 m0, s26, 0x2000
	s_nop 0
	global_load_lds_dwordx4 v[174:175], off
	v_lshl_add_u64 v[174:175], v[182:183], 0, s[92:93]
	s_mov_b32 m0, s47
	s_nop 0
	global_load_lds_dwordx4 v[174:175], off
	v_lshl_add_u64 v[174:175], v[184:185], 0, s[92:93]
	s_mov_b32 m0, s48
	s_nop 0
	global_load_lds_dwordx4 v[174:175], off
	s_waitcnt vmcnt(8)
	s_waitcnt lgkmcnt(0)
	s_barrier
	s_setprio 1
	s_waitcnt lgkmcnt(0)
	v_mfma_scale_f32_16x16x128_f8f6f4 v[94:97], v[2:9], v[204:211], v[94:97], v246, v247 op_sel_hi:[0,0,0]
	v_mfma_scale_f32_16x16x128_f8f6f4 v[86:89], v[10:17], v[204:211], v[86:89], v246, v247 op_sel_hi:[0,0,0]
	v_mfma_scale_f32_16x16x128_f8f6f4 v[78:81], v[2:9], v[212:219], v[78:81], v246, v247 op_sel_hi:[0,0,0]
	v_mfma_scale_f32_16x16x128_f8f6f4 v[70:73], v[10:17], v[212:219], v[70:73], v246, v247 op_sel_hi:[0,0,0]
	v_mfma_scale_f32_16x16x128_f8f6f4 v[62:65], v[2:9], v[220:227], v[62:65], v246, v247 op_sel_hi:[0,0,0]
	v_mfma_scale_f32_16x16x128_f8f6f4 v[54:57], v[10:17], v[220:227], v[54:57], v246, v247 op_sel_hi:[0,0,0]
	v_mfma_scale_f32_16x16x128_f8f6f4 v[46:49], v[2:9], v[228:235], v[46:49], v246, v247 op_sel_hi:[0,0,0]
	v_mfma_scale_f32_16x16x128_f8f6f4 v[38:41], v[10:17], v[228:235], v[38:41], v246, v247 op_sel_hi:[0,0,0]
	s_setprio 0
	s_setprio 1
	v_mfma_scale_f32_16x16x128_f8f6f4 v[90:93], v[18:25], v[204:211], v[90:93], v246, v247 op_sel_hi:[0,0,0]
	v_mfma_scale_f32_16x16x128_f8f6f4 v[82:85], v[26:33], v[204:211], v[82:85], v246, v247 op_sel_hi:[0,0,0]
	v_mfma_scale_f32_16x16x128_f8f6f4 v[74:77], v[18:25], v[212:219], v[74:77], v246, v247 op_sel_hi:[0,0,0]
	v_mfma_scale_f32_16x16x128_f8f6f4 v[66:69], v[26:33], v[212:219], v[66:69], v246, v247 op_sel_hi:[0,0,0]
	v_mfma_scale_f32_16x16x128_f8f6f4 v[58:61], v[18:25], v[220:227], v[58:61], v246, v247 op_sel_hi:[0,0,0]
	v_mfma_scale_f32_16x16x128_f8f6f4 v[50:53], v[26:33], v[220:227], v[50:53], v246, v247 op_sel_hi:[0,0,0]
	v_mfma_scale_f32_16x16x128_f8f6f4 v[42:45], v[18:25], v[228:235], v[42:45], v246, v247 op_sel_hi:[0,0,0]
	v_mfma_scale_f32_16x16x128_f8f6f4 v[34:37], v[26:33], v[228:235], v[34:37], v246, v247 op_sel_hi:[0,0,0]
	s_setprio 0
	s_add_u32 s24, s24, 0x100
	s_addc_u32 s25, s25, 0
	s_add_u32 s58, s58, 0x100
	s_addc_u32 s59, s59, 0
	s_cmp_ge_i32 s60, s49
	s_mov_b32 s26, s60
	s_barrier
	s_cbranch_scc0 .LBB0_1728

;     __device__ __forceinline__ bool next(int i, Unit& u) const { return so.next(i, u); }
; #define PG8_STAGE(bufoff, gbase, voff) do { _Pragma("unroll") for (int _i = 0; _i < 2; ++_i) \
;         __builtin_amdgcn_global_load_lds((const unsigned*)((const char*)(gbase) + (voff)[_i]), (PG8_LAS unsigned*)(lds + (bufoff) + ldsw + _i * 8192), 16, 0, 0); } while (0)
; #define PG8_WAIT_V(n) asm volatile("s_waitcnt vmcnt(" #n ")" ::: "memory")
; #define PG8_WAIT_L(n) asm volatile("s_waitcnt lgkmcnt(" #n ")" ::: "memory")
; #define PG8_BAR __builtin_amdgcn_s_barrier()
; #define PG8_SCHED __builtin_amdgcn_sched_barrier(0)
; template <class Epi, class Sched, bool ALIGN_EPI = false, bool SP2 = false, bool F8 = false>
; __device__ __forceinline__ void gemm_phase(PG8_LAS unsigned char* lds, const Gemm g, const Sched& S, const Epi& E, const int tidb  ) {
;     ...
;         const bool has_next = S.next(ui + 1, nxt);
;         const char* nA = has_next ? (const char*)g.A + (size_t)nxt.pm * tstep : cA; const char* nB = has_next ? (const char*)g.Bt + S.boff(nxt) + (size_t)nxt.pn * tstep : cB;
;         for (int t = 0; t < nt; t += 2) {
;             const bool last = (t == nt - 2);
;             if constexpr (Epi::PREFETCH) { if (t == 0) E.prefetch(cur, wid, lane); }
;             const char* a1 = cA + (size_t)(t + 1) * kstep;
;             const char* a2 = last ? nA : cA + (size_t)(t + 2) * kstep; const char* b2 = last ? nB : cB + (size_t)(t + 2) * kstep;
;             const char* a3 = a2 + kstep; const char* b3 = b2 + kstep;
;             if (last && has_next) S.a_ready(nxt);
;             if constexpr (SP2) {
;             PG8_LDB(B0, 0, 0); PG8_LDB(B1, 0, 1); PG8_SCHED; PG8_LDA(At, 0, 0); PG8_STAGE(PG8_SA(1, 1), a1 + hstep, voffA);
;             PG8_WAIT_V(8); PG8_WAIT_L(0); PG8_BAR; PG8_MMA(0, 0, At, B0); PG8_MMA(0, 1, At, B1); PG8_BAR; PG8_SCHED;
;             PG8_LDA(At, 0, 1); PG8_STAGE(PG8_SB(0, 0), b2, voffB); PG8_STAGE(PG8_SB(0, 1), b2 + hstep, voffB); PG8_STAGE(PG8_SA(0, 0), a2, voffA);
;             PG8_WAIT_V(8); PG8_WAIT_L(0); PG8_BAR; PG8_MMA(1, 0, At, B0); PG8_MMA(1, 1, At, B1); PG8_BAR; PG8_SCHED;
.LBB0_1807:
	s_add_i32 s65, s30, 2
	s_add_u32 s66, s28, 0x80
	s_addc_u32 s31, s29, 0
	s_add_i32 s68, 0, 0x10000
	s_cmp_eq_u32 s47, s30
	s_cselect_b32 s31, s7, s31
	s_cselect_b32 s30, s6, s66
	s_cselect_b32 s67, s27, s63
	s_cselect_b32 s66, s26, s62
	s_add_i32 s70, 0, 0x14000
	v_add_u32_e32 v142, s68, v192
	v_add_u32_e32 v170, s70, v192
	ds_read_b128 v[122:125], v142
	ds_read_b128 v[126:129], v142 offset:1024
	ds_read_b128 v[138:141], v142 offset:2048
	ds_read_b128 v[142:145], v142 offset:3072
	ds_read_b128 v[146:149], v170
	ds_read_b128 v[150:153], v170 offset:1024
	ds_read_b128 v[154:157], v170 offset:2048
	ds_read_b128 v[170:173], v170 offset:3072
	v_lshl_add_u64 v[190:191], s[28:29], 0, v[166:167]
	s_add_i32 m0, s1, 0xc000
	ds_read_b128 v[174:177], v194
	ds_read_b128 v[178:181], v194 offset:1024
	ds_read_b128 v[182:185], v194 offset:2048
	ds_read_b128 v[186:189], v194 offset:3072
	ds_read_b128 v[204:207], v194 offset:4096
	ds_read_b128 v[208:211], v194 offset:5120
	ds_read_b128 v[212:215], v194 offset:6144
	ds_read_b128 v[216:219], v194 offset:7168
	global_load_lds_dwordx4 v[190:191], off
	v_lshl_add_u64 v[190:191], s[28:29], 0, v[168:169]
	s_add_i32 m0, s1, 0xe000
	s_nop 0
	global_load_lds_dwordx4 v[190:191], off
	s_waitcnt vmcnt(8)
	s_waitcnt lgkmcnt(0)
	s_barrier
	s_setprio 1
	s_waitcnt lgkmcnt(0)
	v_mfma_f32_16x16x32_bf16 v[134:137], v[122:125], v[174:177], v[134:137]
	v_mfma_f32_16x16x32_bf16 v[130:133], v[138:141], v[174:177], v[130:133]
	v_mfma_f32_16x16x32_bf16 v[110:113], v[122:125], v[182:185], v[110:113]
	v_mfma_f32_16x16x32_bf16 v[106:109], v[138:141], v[182:185], v[106:109]
	v_mfma_f32_16x16x32_bf16 v[94:97], v[122:125], v[204:207], v[94:97]
	v_mfma_f32_16x16x32_bf16 v[90:93], v[138:141], v[204:207], v[90:93]
	v_mfma_f32_16x16x32_bf16 v[78:81], v[122:125], v[212:215], v[78:81]
	v_mfma_f32_16x16x32_bf16 v[74:77], v[138:141], v[212:215], v[74:77]
	v_mfma_f32_16x16x32_bf16 v[134:137], v[126:129], v[178:181], v[134:137]
	v_mfma_f32_16x16x32_bf16 v[130:133], v[142:145], v[178:181], v[130:133]
	v_mfma_f32_16x16x32_bf16 v[110:113], v[126:129], v[186:189], v[110:113]
	v_mfma_f32_16x16x32_bf16 v[106:109], v[142:145], v[186:189], v[106:109]
	v_mfma_f32_16x16x32_bf16 v[94:97], v[126:129], v[208:211], v[94:97]
	v_mfma_f32_16x16x32_bf16 v[90:93], v[142:145], v[208:211], v[90:93]
	v_mfma_f32_16x16x32_bf16 v[78:81], v[126:129], v[216:219], v[78:81]
	v_mfma_f32_16x16x32_bf16 v[74:77], v[142:145], v[216:219], v[74:77]
	s_setprio 0
	s_setprio 1
	v_mfma_f32_16x16x32_bf16 v[118:121], v[146:149], v[174:177], v[118:121]
	v_mfma_f32_16x16x32_bf16 v[114:117], v[154:157], v[174:177], v[114:117]
	v_mfma_f32_16x16x32_bf16 v[102:105], v[146:149], v[182:185], v[102:105]
	v_mfma_f32_16x16x32_bf16 v[98:101], v[154:157], v[182:185], v[98:101]
	v_mfma_f32_16x16x32_bf16 v[86:89], v[146:149], v[204:207], v[86:89]
	v_mfma_f32_16x16x32_bf16 v[82:85], v[154:157], v[204:207], v[82:85]
	v_mfma_f32_16x16x32_bf16 v[70:73], v[146:149], v[212:215], v[70:73]
	v_mfma_f32_16x16x32_bf16 v[66:69], v[154:157], v[212:215], v[66:69]
	v_mfma_f32_16x16x32_bf16 v[118:121], v[150:153], v[178:181], v[118:121]
	v_mfma_f32_16x16x32_bf16 v[114:117], v[170:173], v[178:181], v[114:117]
	v_mfma_f32_16x16x32_bf16 v[102:105], v[150:153], v[186:189], v[102:105]
	v_mfma_f32_16x16x32_bf16 v[98:101], v[170:173], v[186:189], v[98:101]
	v_mfma_f32_16x16x32_bf16 v[86:89], v[150:153], v[208:211], v[86:89]
	v_mfma_f32_16x16x32_bf16 v[82:85], v[170:173], v[208:211], v[82:85]
	v_mfma_f32_16x16x32_bf16 v[70:73], v[150:153], v[216:219], v[70:73]
	v_mfma_f32_16x16x32_bf16 v[66:69], v[170:173], v[216:219], v[66:69]
	s_setprio 0
	s_barrier
	s_add_i32 s68, s68, s0
	v_lshl_add_u64 v[190:191], s[66:67], 0, v[0:1]
	s_mov_b32 m0, s68
	ds_read_b128 v[174:177], v194 offset:16384
	ds_read_b128 v[178:181], v194 offset:17408
	ds_read_b128 v[182:185], v194 offset:18432
	ds_read_b128 v[186:189], v194 offset:19456
	ds_read_b128 v[204:207], v194 offset:20480
	ds_read_b128 v[208:211], v194 offset:21504
	ds_read_b128 v[212:215], v194 offset:22528
	ds_read_b128 v[216:219], v194 offset:23552
	global_load_lds_dwordx4 v[190:191], off
	s_add_i32 m0, s68, 0x2000
	v_lshl_add_u64 v[196:197], s[66:67], 0, v[164:165]
	s_add_u32 s66, s66, s12
	s_addc_u32 s67, s67, s13
	s_add_i32 s68, s70, s0
	global_load_lds_dwordx4 v[196:197], off
	v_lshl_add_u64 v[198:199], s[66:67], 0, v[0:1]
	s_mov_b32 m0, s68
	v_lshl_add_u64 v[200:201], s[66:67], 0, v[164:165]
	global_load_lds_dwordx4 v[198:199], off
	s_add_i32 m0, s68, 0x2000
	v_lshl_add_u64 v[220:221], s[30:31], 0, v[158:159]
	global_load_lds_dwordx4 v[200:201], off
	s_mov_b32 m0, s1
	v_lshl_add_u64 v[222:223], s[30:31], 0, v[160:161]
	global_load_lds_dwordx4 v[220:221], off
	s_mov_b32 m0, s36
	s_nop 0
	global_load_lds_dwordx4 v[222:223], off
	s_waitcnt vmcnt(8)
	s_waitcnt lgkmcnt(0)
	s_barrier
; #define PG8_STAGE(bufoff, gbase, voff) do { _Pragma("unroll") for (int _i = 0; _i < 2; ++_i) \
;         __builtin_amdgcn_global_load_lds((const unsigned*)((const char*)(gbase) + (voff)[_i]), (PG8_LAS unsigned*)(lds + (bufoff) + ldsw + _i * 8192), 16, 0, 0); } while (0)
; #define PG8_WAIT_V(n) asm volatile("s_waitcnt vmcnt(" #n ")" ::: "memory")
; #define PG8_WAIT_L(n) asm volatile("s_waitcnt lgkmcnt(" #n ")" ::: "memory")
; #define PG8_BAR __builtin_amdgcn_s_barrier()
; #define PG8_SCHED __builtin_amdgcn_sched_barrier(0)
; template <class Epi, class Sched, bool ALIGN_EPI = false, bool SP2 = false, bool F8 = false>
; __device__ __forceinline__ void gemm_phase(PG8_LAS unsigned char* lds, const Gemm g, const Sched& S, const Epi& E, const int tidb  ) {
;     ...
;             PG8_WAIT_V(8); PG8_WAIT_L(0); PG8_BAR; PG8_MMA(1, 0, At, B0); PG8_MMA(1, 1, At, B1); PG8_BAR; PG8_SCHED;
;             PG8_LDB(B0, 1, 0); PG8_LDB(B1, 1, 1); PG8_SCHED; PG8_LDA(At, 1, 0); PG8_STAGE(PG8_SA(0, 1), a2 + hstep, voffA);
;             PG8_WAIT_V(8); PG8_WAIT_L(0); PG8_BAR; PG8_MMA(0, 0, At, B0); PG8_MMA(0, 1, At, B1); PG8_BAR; PG8_SCHED;
	s_setprio 1
	s_waitcnt lgkmcnt(0)
	v_mfma_f32_16x16x32_bf16 v[62:65], v[122:125], v[174:177], v[62:65]
	v_mfma_f32_16x16x32_bf16 v[58:61], v[138:141], v[174:177], v[58:61]
	v_mfma_f32_16x16x32_bf16 v[46:49], v[122:125], v[182:185], v[46:49]
	v_mfma_f32_16x16x32_bf16 v[42:45], v[138:141], v[182:185], v[42:45]
	v_mfma_f32_16x16x32_bf16 v[30:33], v[122:125], v[204:207], v[30:33]
	v_mfma_f32_16x16x32_bf16 v[26:29], v[138:141], v[204:207], v[26:29]
	v_mfma_f32_16x16x32_bf16 v[14:17], v[122:125], v[212:215], v[14:17]
	v_mfma_f32_16x16x32_bf16 v[10:13], v[138:141], v[212:215], v[10:13]
	v_mfma_f32_16x16x32_bf16 v[62:65], v[126:129], v[178:181], v[62:65]
	v_mfma_f32_16x16x32_bf16 v[58:61], v[142:145], v[178:181], v[58:61]
	v_mfma_f32_16x16x32_bf16 v[46:49], v[126:129], v[186:189], v[46:49]
	v_mfma_f32_16x16x32_bf16 v[42:45], v[142:145], v[186:189], v[42:45]
	v_mfma_f32_16x16x32_bf16 v[30:33], v[126:129], v[208:211], v[30:33]
	v_mfma_f32_16x16x32_bf16 v[26:29], v[142:145], v[208:211], v[26:29]
	v_mfma_f32_16x16x32_bf16 v[14:17], v[126:129], v[216:219], v[14:17]
	v_mfma_f32_16x16x32_bf16 v[10:13], v[142:145], v[216:219], v[10:13]
	s_setprio 0
	s_setprio 1
	v_mfma_f32_16x16x32_bf16 v[54:57], v[146:149], v[174:177], v[54:57]
	v_mfma_f32_16x16x32_bf16 v[50:53], v[154:157], v[174:177], v[50:53]
	v_mfma_f32_16x16x32_bf16 v[38:41], v[146:149], v[182:185], v[38:41]
	v_mfma_f32_16x16x32_bf16 v[34:37], v[154:157], v[182:185], v[34:37]
	v_mfma_f32_16x16x32_bf16 v[22:25], v[146:149], v[204:207], v[22:25]
	v_mfma_f32_16x16x32_bf16 v[18:21], v[154:157], v[204:207], v[18:21]
	v_mfma_f32_16x16x32_bf16 v[6:9], v[146:149], v[212:215], v[6:9]
	v_mfma_f32_16x16x32_bf16 v[2:5], v[154:157], v[212:215], v[2:5]
	v_mfma_f32_16x16x32_bf16 v[54:57], v[150:153], v[178:181], v[54:57]
	v_mfma_f32_16x16x32_bf16 v[50:53], v[170:173], v[178:181], v[50:53]
	v_mfma_f32_16x16x32_bf16 v[38:41], v[150:153], v[186:189], v[38:41]
	v_mfma_f32_16x16x32_bf16 v[34:37], v[170:173], v[186:189], v[34:37]
	v_mfma_f32_16x16x32_bf16 v[22:25], v[150:153], v[208:211], v[22:25]
	v_mfma_f32_16x16x32_bf16 v[18:21], v[170:173], v[208:211], v[18:21]
	v_mfma_f32_16x16x32_bf16 v[6:9], v[150:153], v[216:219], v[6:9]
	v_mfma_f32_16x16x32_bf16 v[2:5], v[170:173], v[216:219], v[2:5]
	s_setprio 0
	s_barrier
	s_add_i32 s66, 0, 0x18000
	s_add_i32 s67, 0, 0x1c000
	v_add_u32_e32 v142, s66, v192
	v_add_u32_e32 v170, s67, v192
	ds_read_b128 v[122:125], v142
	ds_read_b128 v[126:129], v142 offset:1024
	ds_read_b128 v[138:141], v142 offset:2048
	ds_read_b128 v[142:145], v142 offset:3072
	ds_read_b128 v[146:149], v170
	ds_read_b128 v[150:153], v170 offset:1024
	ds_read_b128 v[154:157], v170 offset:2048
	ds_read_b128 v[170:173], v170 offset:3072
	s_add_u32 s30, s30, s12
	s_addc_u32 s31, s31, s13
	s_mov_b32 m0, s37
	v_lshl_add_u64 v[224:225], s[30:31], 0, v[158:159]
	ds_read_b128 v[174:177], v194 offset:32768
	ds_read_b128 v[178:181], v194 offset:33792
	ds_read_b128 v[182:185], v194 offset:34816
	ds_read_b128 v[186:189], v194 offset:35840
	ds_read_b128 v[204:207], v194 offset:36864
	ds_read_b128 v[208:211], v194 offset:37888
	ds_read_b128 v[212:215], v194 offset:38912
	ds_read_b128 v[216:219], v194 offset:39936
	global_load_lds_dwordx4 v[224:225], off
	v_lshl_add_u64 v[224:225], s[30:31], 0, v[160:161]
	s_mov_b32 m0, s41
	s_nop 0
	global_load_lds_dwordx4 v[224:225], off
	s_waitcnt vmcnt(8)
	s_waitcnt lgkmcnt(0)
	s_barrier
	s_setprio 1
	s_waitcnt lgkmcnt(0)
	v_mfma_f32_16x16x32_bf16 v[134:137], v[122:125], v[174:177], v[134:137]
	v_mfma_f32_16x16x32_bf16 v[130:133], v[138:141], v[174:177], v[130:133]
	v_mfma_f32_16x16x32_bf16 v[110:113], v[122:125], v[182:185], v[110:113]
	v_mfma_f32_16x16x32_bf16 v[106:109], v[138:141], v[182:185], v[106:109]
	v_mfma_f32_16x16x32_bf16 v[94:97], v[122:125], v[204:207], v[94:97]
	v_mfma_f32_16x16x32_bf16 v[90:93], v[138:141], v[204:207], v[90:93]
	v_mfma_f32_16x16x32_bf16 v[78:81], v[122:125], v[212:215], v[78:81]
	v_mfma_f32_16x16x32_bf16 v[74:77], v[138:141], v[212:215], v[74:77]
	v_mfma_f32_16x16x32_bf16 v[134:137], v[126:129], v[178:181], v[134:137]
	v_mfma_f32_16x16x32_bf16 v[130:133], v[142:145], v[178:181], v[130:133]
	v_mfma_f32_16x16x32_bf16 v[110:113], v[126:129], v[186:189], v[110:113]
	v_mfma_f32_16x16x32_bf16 v[106:109], v[142:145], v[186:189], v[106:109]
	v_mfma_f32_16x16x32_bf16 v[94:97], v[126:129], v[208:211], v[94:97]
	v_mfma_f32_16x16x32_bf16 v[90:93], v[142:145], v[208:211], v[90:93]
	v_mfma_f32_16x16x32_bf16 v[78:81], v[126:129], v[216:219], v[78:81]
	v_mfma_f32_16x16x32_bf16 v[74:77], v[142:145], v[216:219], v[74:77]
	s_setprio 0
	s_setprio 1
	v_mfma_f32_16x16x32_bf16 v[118:121], v[146:149], v[174:177], v[118:121]
	v_mfma_f32_16x16x32_bf16 v[114:117], v[154:157], v[174:177], v[114:117]
	v_mfma_f32_16x16x32_bf16 v[102:105], v[146:149], v[182:185], v[102:105]
	v_mfma_f32_16x16x32_bf16 v[98:101], v[154:157], v[182:185], v[98:101]
	v_mfma_f32_16x16x32_bf16 v[86:89], v[146:149], v[204:207], v[86:89]
	v_mfma_f32_16x16x32_bf16 v[82:85], v[154:157], v[204:207], v[82:85]
	v_mfma_f32_16x16x32_bf16 v[70:73], v[146:149], v[212:215], v[70:73]
	v_mfma_f32_16x16x32_bf16 v[66:69], v[154:157], v[212:215], v[66:69]
	v_mfma_f32_16x16x32_bf16 v[118:121], v[150:153], v[178:181], v[118:121]
	v_mfma_f32_16x16x32_bf16 v[114:117], v[170:173], v[178:181], v[114:117]
	v_mfma_f32_16x16x32_bf16 v[102:105], v[150:153], v[186:189], v[102:105]
	v_mfma_f32_16x16x32_bf16 v[98:101], v[170:173], v[186:189], v[98:101]
	v_mfma_f32_16x16x32_bf16 v[86:89], v[150:153], v[208:211], v[86:89]
	v_mfma_f32_16x16x32_bf16 v[82:85], v[170:173], v[208:211], v[82:85]
	v_mfma_f32_16x16x32_bf16 v[70:73], v[150:153], v[216:219], v[70:73]
	v_mfma_f32_16x16x32_bf16 v[66:69], v[170:173], v[216:219], v[66:69]
	s_setprio 0
	s_barrier
; #define PG8_STAGE(bufoff, gbase, voff) do { _Pragma("unroll") for (int _i = 0; _i < 2; ++_i) \
;         __builtin_amdgcn_global_load_lds((const unsigned*)((const char*)(gbase) + (voff)[_i]), (PG8_LAS unsigned*)(lds + (bufoff) + ldsw + _i * 8192), 16, 0, 0); } while (0)
; #define PG8_WAIT_V(n) asm volatile("s_waitcnt vmcnt(" #n ")" ::: "memory")
; #define PG8_WAIT_L(n) asm volatile("s_waitcnt lgkmcnt(" #n ")" ::: "memory")
; #define PG8_BAR __builtin_amdgcn_s_barrier()
; #define PG8_SCHED __builtin_amdgcn_sched_barrier(0)
; template <class Epi, class Sched, bool ALIGN_EPI = false, bool SP2 = false, bool F8 = false>
; __device__ __forceinline__ void gemm_phase(PG8_LAS unsigned char* lds, const Gemm g, const Sched& S, const Epi& E, const int tidb  ) {
;     ...
;         for (int t = 0; t < nt; t += 2) {
;             const bool last = (t == nt - 2);
;             if constexpr (Epi::PREFETCH) { if (t == 0) E.prefetch(cur, wid, lane); }
;             const char* a1 = cA + (size_t)(t + 1) * kstep;
;             const char* a2 = last ? nA : cA + (size_t)(t + 2) * kstep; const char* b2 = last ? nB : cB + (size_t)(t + 2) * kstep;
;             const char* a3 = a2 + kstep; const char* b3 = b2 + kstep;
;     ...
;             PG8_LDA(At, 1, 1); PG8_STAGE(PG8_SB(1, 0), b3, voffB); PG8_STAGE(PG8_SB(1, 1), b3 + hstep, voffB); PG8_STAGE(PG8_SA(1, 0), a3, voffA);
;             PG8_WAIT_V(8); PG8_WAIT_L(0); PG8_BAR; PG8_MMA(1, 0, At, B0); PG8_MMA(1, 1, At, B1); PG8_BAR; PG8_SCHED;
	s_add_i32 s30, s66, s0
	v_lshl_add_u64 v[190:191], v[190:191], 0, s[92:93]
	s_mov_b32 m0, s30
	ds_read_b128 v[174:177], v194 offset:49152
	ds_read_b128 v[178:181], v194 offset:50176
	ds_read_b128 v[182:185], v194 offset:51200
	ds_read_b128 v[186:189], v194 offset:52224
	ds_read_b128 v[204:207], v194 offset:53248
	ds_read_b128 v[208:211], v194 offset:54272
	ds_read_b128 v[212:215], v194 offset:55296
	ds_read_b128 v[216:219], v194 offset:56320
	global_load_lds_dwordx4 v[190:191], off
	v_lshl_add_u64 v[190:191], v[196:197], 0, s[92:93]
	s_add_i32 m0, s30, 0x2000
	s_add_i32 s30, s67, s0
	global_load_lds_dwordx4 v[190:191], off
	v_lshl_add_u64 v[190:191], v[198:199], 0, s[92:93]
	s_mov_b32 m0, s30
	s_nop 0
	global_load_lds_dwordx4 v[190:191], off
	v_lshl_add_u64 v[190:191], v[200:201], 0, s[92:93]
	s_add_i32 m0, s30, 0x2000
	s_nop 0
	global_load_lds_dwordx4 v[190:191], off
	v_lshl_add_u64 v[190:191], v[220:221], 0, s[92:93]
	s_mov_b32 m0, s43
	s_nop 0
	global_load_lds_dwordx4 v[190:191], off
	v_lshl_add_u64 v[190:191], v[222:223], 0, s[92:93]
	s_mov_b32 m0, s45
	s_nop 0
	global_load_lds_dwordx4 v[190:191], off
	s_waitcnt vmcnt(8)
	s_waitcnt lgkmcnt(0)
	s_barrier
	s_setprio 1
	s_waitcnt lgkmcnt(0)
	v_mfma_f32_16x16x32_bf16 v[62:65], v[122:125], v[174:177], v[62:65]
	v_mfma_f32_16x16x32_bf16 v[58:61], v[138:141], v[174:177], v[58:61]
	v_mfma_f32_16x16x32_bf16 v[46:49], v[122:125], v[182:185], v[46:49]
	v_mfma_f32_16x16x32_bf16 v[42:45], v[138:141], v[182:185], v[42:45]
	v_mfma_f32_16x16x32_bf16 v[30:33], v[122:125], v[204:207], v[30:33]
	v_mfma_f32_16x16x32_bf16 v[26:29], v[138:141], v[204:207], v[26:29]
	v_mfma_f32_16x16x32_bf16 v[14:17], v[122:125], v[212:215], v[14:17]
	v_mfma_f32_16x16x32_bf16 v[10:13], v[138:141], v[212:215], v[10:13]
	v_mfma_f32_16x16x32_bf16 v[62:65], v[126:129], v[178:181], v[62:65]
	v_mfma_f32_16x16x32_bf16 v[58:61], v[142:145], v[178:181], v[58:61]
	v_mfma_f32_16x16x32_bf16 v[46:49], v[126:129], v[186:189], v[46:49]
	v_mfma_f32_16x16x32_bf16 v[42:45], v[142:145], v[186:189], v[42:45]
	v_mfma_f32_16x16x32_bf16 v[30:33], v[126:129], v[208:211], v[30:33]
	v_mfma_f32_16x16x32_bf16 v[26:29], v[142:145], v[208:211], v[26:29]
	v_mfma_f32_16x16x32_bf16 v[14:17], v[126:129], v[216:219], v[14:17]
	v_mfma_f32_16x16x32_bf16 v[10:13], v[142:145], v[216:219], v[10:13]
	s_setprio 0
	s_setprio 1
	v_mfma_f32_16x16x32_bf16 v[54:57], v[146:149], v[174:177], v[54:57]
	v_mfma_f32_16x16x32_bf16 v[50:53], v[154:157], v[174:177], v[50:53]
	v_mfma_f32_16x16x32_bf16 v[38:41], v[146:149], v[182:185], v[38:41]
	v_mfma_f32_16x16x32_bf16 v[34:37], v[154:157], v[182:185], v[34:37]
	v_mfma_f32_16x16x32_bf16 v[22:25], v[146:149], v[204:207], v[22:25]
	v_mfma_f32_16x16x32_bf16 v[18:21], v[154:157], v[204:207], v[18:21]
	v_mfma_f32_16x16x32_bf16 v[6:9], v[146:149], v[212:215], v[6:9]
	v_mfma_f32_16x16x32_bf16 v[2:5], v[154:157], v[212:215], v[2:5]
	v_mfma_f32_16x16x32_bf16 v[54:57], v[150:153], v[178:181], v[54:57]
	v_mfma_f32_16x16x32_bf16 v[50:53], v[170:173], v[178:181], v[50:53]
	v_mfma_f32_16x16x32_bf16 v[38:41], v[150:153], v[186:189], v[38:41]
	v_mfma_f32_16x16x32_bf16 v[34:37], v[170:173], v[186:189], v[34:37]
	v_mfma_f32_16x16x32_bf16 v[22:25], v[150:153], v[208:211], v[22:25]
	v_mfma_f32_16x16x32_bf16 v[18:21], v[170:173], v[208:211], v[18:21]
	v_mfma_f32_16x16x32_bf16 v[6:9], v[150:153], v[216:219], v[6:9]
	v_mfma_f32_16x16x32_bf16 v[2:5], v[170:173], v[216:219], v[2:5]
	s_setprio 0
	s_add_u32 s28, s28, 0x100
	s_addc_u32 s29, s29, 0
	s_add_u32 s62, s62, 0x100
	s_addc_u32 s63, s63, 0
	s_cmp_ge_i32 s65, s46
	s_mov_b32 s30, s65
	s_barrier
	s_cbranch_scc0 .LBB0_1807
	s_movk_i32 s67, 0x300

;     __device__ __forceinline__ bool next(int i, Unit& u) const { return so.next(i, u); }
; #define PG8_STAGE(bufoff, gbase, voff) do { _Pragma("unroll") for (int _i = 0; _i < 2; ++_i) \
;         __builtin_amdgcn_global_load_lds((const unsigned*)((const char*)(gbase) + (voff)[_i]), (PG8_LAS unsigned*)(lds + (bufoff) + ldsw + _i * 8192), 16, 0, 0); } while (0)
; #define PG8_WAIT_V(n) asm volatile("s_waitcnt vmcnt(" #n ")" ::: "memory")
; #define PG8_WAIT_L(n) asm volatile("s_waitcnt lgkmcnt(" #n ")" ::: "memory")
; #define PG8_BAR __builtin_amdgcn_s_barrier()
; #define PG8_SCHED __builtin_amdgcn_sched_barrier(0)
; template <class Epi, class Sched, bool ALIGN_EPI = false, bool SP2 = false, bool F8 = false>
; __device__ __forceinline__ void gemm_phase(PG8_LAS unsigned char* lds, const Gemm g, const Sched& S, const Epi& E, const int tidb  ) {
;     ...
;         const bool has_next = S.next(ui + 1, nxt);
;         const char* nA = has_next ? (const char*)g.A + (size_t)nxt.pm * tstep : cA; const char* nB = has_next ? (const char*)g.Bt + S.boff(nxt) + (size_t)nxt.pn * tstep : cB;
;         for (int t = 0; t < nt; t += 2) {
;             const bool last = (t == nt - 2);
;             if constexpr (Epi::PREFETCH) { if (t == 0) E.prefetch(cur, wid, lane); }
;             const char* a1 = cA + (size_t)(t + 1) * kstep;
;             const char* a2 = last ? nA : cA + (size_t)(t + 2) * kstep; const char* b2 = last ? nB : cB + (size_t)(t + 2) * kstep;
;             const char* a3 = a2 + kstep; const char* b3 = b2 + kstep;
;             if (last && has_next) S.a_ready(nxt);
;             if constexpr (SP2) {
;             PG8_LDB(B0, 0, 0); PG8_LDB(B1, 0, 1); PG8_SCHED; PG8_LDA(At, 0, 0); PG8_STAGE(PG8_SA(1, 1), a1 + hstep, voffA);
;             PG8_WAIT_V(8); PG8_WAIT_L(0); PG8_BAR; PG8_MMA(0, 0, At, B0); PG8_MMA(0, 1, At, B1); PG8_BAR; PG8_SCHED;
;             PG8_LDA(At, 0, 1); PG8_STAGE(PG8_SB(0, 0), b2, voffB); PG8_STAGE(PG8_SB(0, 1), b2 + hstep, voffB); PG8_STAGE(PG8_SA(0, 0), a2, voffA);
;             PG8_WAIT_V(8); PG8_WAIT_L(0); PG8_BAR; PG8_MMA(1, 0, At, B0); PG8_MMA(1, 1, At, B1); PG8_BAR; PG8_SCHED;
.LBB0_1857:
	s_add_i32 s65, s28, 2
	s_add_u32 s30, s26, 0x80
	s_addc_u32 s29, s27, 0
	s_add_i32 s66, 0, 0x10000
	s_cmp_eq_u32 s47, s28
	s_cselect_b32 s29, s7, s29
	s_cselect_b32 s28, s6, s30
	s_cselect_b32 s31, s11, s63
	s_cselect_b32 s30, s10, s62
	s_add_i32 s67, 0, 0x14000
	v_add_u32_e32 v2, s66, v192
	v_add_u32_e32 v14, s67, v192
	ds_read_b128 v[18:21], v2
	ds_read_b128 v[22:25], v2 offset:1024
	ds_read_b128 v[26:29], v2 offset:2048
	ds_read_b128 v[30:33], v2 offset:3072
	ds_read_b128 v[2:5], v14
	ds_read_b128 v[6:9], v14 offset:1024
	ds_read_b128 v[10:13], v14 offset:2048
	ds_read_b128 v[14:17], v14 offset:3072
	v_lshl_add_u64 v[190:191], s[26:27], 0, v[170:171]
	s_add_i32 m0, s1, 0xc000
	ds_read_b128 v[174:177], v194
	ds_read_b128 v[178:181], v194 offset:1024
	ds_read_b128 v[182:185], v194 offset:2048
	ds_read_b128 v[186:189], v194 offset:3072
	ds_read_b128 v[204:207], v194 offset:4096
	ds_read_b128 v[208:211], v194 offset:5120
	ds_read_b128 v[212:215], v194 offset:6144
	ds_read_b128 v[216:219], v194 offset:7168
	global_load_lds_dwordx4 v[190:191], off
	v_lshl_add_u64 v[190:191], s[26:27], 0, v[172:173]
	s_add_i32 m0, s1, 0xe000
	s_nop 0
	global_load_lds_dwordx4 v[190:191], off
	s_waitcnt vmcnt(8)
	s_waitcnt lgkmcnt(0)
	s_barrier
	s_setprio 1
	s_waitcnt lgkmcnt(0)
	v_mfma_scale_f32_16x16x128_f8f6f4 v[158:161], v[18:25], v[174:181], v[158:161], v246, v247 op_sel_hi:[0,0,0]
	v_mfma_scale_f32_16x16x128_f8f6f4 v[154:157], v[26:33], v[174:181], v[154:157], v246, v247 op_sel_hi:[0,0,0]
	v_mfma_scale_f32_16x16x128_f8f6f4 v[142:145], v[18:25], v[182:189], v[142:145], v246, v247 op_sel_hi:[0,0,0]
	v_mfma_scale_f32_16x16x128_f8f6f4 v[138:141], v[26:33], v[182:189], v[138:141], v246, v247 op_sel_hi:[0,0,0]
	v_mfma_scale_f32_16x16x128_f8f6f4 v[126:129], v[18:25], v[204:211], v[126:129], v246, v247 op_sel_hi:[0,0,0]
	v_mfma_scale_f32_16x16x128_f8f6f4 v[122:125], v[26:33], v[204:211], v[122:125], v246, v247 op_sel_hi:[0,0,0]
	v_mfma_scale_f32_16x16x128_f8f6f4 v[110:113], v[18:25], v[212:219], v[110:113], v246, v247 op_sel_hi:[0,0,0]
	v_mfma_scale_f32_16x16x128_f8f6f4 v[106:109], v[26:33], v[212:219], v[106:109], v246, v247 op_sel_hi:[0,0,0]
	s_setprio 0
	s_setprio 1
	v_mfma_scale_f32_16x16x128_f8f6f4 v[150:153], v[2:9], v[174:181], v[150:153], v246, v247 op_sel_hi:[0,0,0]
	v_mfma_scale_f32_16x16x128_f8f6f4 v[146:149], v[10:17], v[174:181], v[146:149], v246, v247 op_sel_hi:[0,0,0]
	v_mfma_scale_f32_16x16x128_f8f6f4 v[134:137], v[2:9], v[182:189], v[134:137], v246, v247 op_sel_hi:[0,0,0]
	v_mfma_scale_f32_16x16x128_f8f6f4 v[130:133], v[10:17], v[182:189], v[130:133], v246, v247 op_sel_hi:[0,0,0]
	v_mfma_scale_f32_16x16x128_f8f6f4 v[118:121], v[2:9], v[204:211], v[118:121], v246, v247 op_sel_hi:[0,0,0]
	v_mfma_scale_f32_16x16x128_f8f6f4 v[114:117], v[10:17], v[204:211], v[114:117], v246, v247 op_sel_hi:[0,0,0]
	v_mfma_scale_f32_16x16x128_f8f6f4 v[102:105], v[2:9], v[212:219], v[102:105], v246, v247 op_sel_hi:[0,0,0]
	v_mfma_scale_f32_16x16x128_f8f6f4 v[98:101], v[10:17], v[212:219], v[98:101], v246, v247 op_sel_hi:[0,0,0]
	s_setprio 0
	s_barrier
	s_add_i32 s66, s66, s0
	v_lshl_add_u64 v[174:175], s[30:31], 0, v[0:1]
	s_mov_b32 m0, s66
	ds_read_b128 v[204:207], v194 offset:16384
	ds_read_b128 v[208:211], v194 offset:17408
	ds_read_b128 v[212:215], v194 offset:18432
	ds_read_b128 v[216:219], v194 offset:19456
	ds_read_b128 v[220:223], v194 offset:20480
	ds_read_b128 v[224:227], v194 offset:21504
	ds_read_b128 v[228:231], v194 offset:22528
	ds_read_b128 v[232:235], v194 offset:23552
	global_load_lds_dwordx4 v[174:175], off
	s_add_i32 m0, s66, 0x2000
	v_lshl_add_u64 v[176:177], s[30:31], 0, v[168:169]
	s_add_u32 s30, s30, s12
	s_addc_u32 s31, s31, s13
	s_add_i32 s66, s67, s0
	global_load_lds_dwordx4 v[176:177], off
	v_lshl_add_u64 v[178:179], s[30:31], 0, v[0:1]
	s_mov_b32 m0, s66
	v_lshl_add_u64 v[180:181], s[30:31], 0, v[168:169]
	global_load_lds_dwordx4 v[178:179], off
	s_add_i32 m0, s66, 0x2000
	v_lshl_add_u64 v[182:183], s[28:29], 0, v[164:165]
	global_load_lds_dwordx4 v[180:181], off
	s_mov_b32 m0, s1
	v_lshl_add_u64 v[184:185], s[28:29], 0, v[166:167]
	global_load_lds_dwordx4 v[182:183], off
	s_mov_b32 m0, s36
	s_nop 0
	global_load_lds_dwordx4 v[184:185], off
	s_waitcnt vmcnt(8)
	s_waitcnt lgkmcnt(0)
	s_barrier
	s_setprio 1
	s_waitcnt lgkmcnt(0)
	v_mfma_scale_f32_16x16x128_f8f6f4 v[94:97], v[18:25], v[204:211], v[94:97], v246, v247 op_sel_hi:[0,0,0]
	v_mfma_scale_f32_16x16x128_f8f6f4 v[90:93], v[26:33], v[204:211], v[90:93], v246, v247 op_sel_hi:[0,0,0]
	v_mfma_scale_f32_16x16x128_f8f6f4 v[78:81], v[18:25], v[212:219], v[78:81], v246, v247 op_sel_hi:[0,0,0]
	v_mfma_scale_f32_16x16x128_f8f6f4 v[74:77], v[26:33], v[212:219], v[74:77], v246, v247 op_sel_hi:[0,0,0]
	v_mfma_scale_f32_16x16x128_f8f6f4 v[62:65], v[18:25], v[220:227], v[62:65], v246, v247 op_sel_hi:[0,0,0]
	v_mfma_scale_f32_16x16x128_f8f6f4 v[58:61], v[26:33], v[220:227], v[58:61], v246, v247 op_sel_hi:[0,0,0]
	v_mfma_scale_f32_16x16x128_f8f6f4 v[46:49], v[18:25], v[228:235], v[46:49], v246, v247 op_sel_hi:[0,0,0]
	v_mfma_scale_f32_16x16x128_f8f6f4 v[42:45], v[26:33], v[228:235], v[42:45], v246, v247 op_sel_hi:[0,0,0]
	s_setprio 0
	s_setprio 1
	v_mfma_scale_f32_16x16x128_f8f6f4 v[86:89], v[2:9], v[204:211], v[86:89], v246, v247 op_sel_hi:[0,0,0]
	v_mfma_scale_f32_16x16x128_f8f6f4 v[82:85], v[10:17], v[204:211], v[82:85], v246, v247 op_sel_hi:[0,0,0]
	v_mfma_scale_f32_16x16x128_f8f6f4 v[70:73], v[2:9], v[212:219], v[70:73], v246, v247 op_sel_hi:[0,0,0]
	v_mfma_scale_f32_16x16x128_f8f6f4 v[66:69], v[10:17], v[212:219], v[66:69], v246, v247 op_sel_hi:[0,0,0]
	v_mfma_scale_f32_16x16x128_f8f6f4 v[54:57], v[2:9], v[220:227], v[54:57], v246, v247 op_sel_hi:[0,0,0]
	v_mfma_scale_f32_16x16x128_f8f6f4 v[50:53], v[10:17], v[220:227], v[50:53], v246, v247 op_sel_hi:[0,0,0]
	v_mfma_scale_f32_16x16x128_f8f6f4 v[38:41], v[2:9], v[228:235], v[38:41], v246, v247 op_sel_hi:[0,0,0]
	v_mfma_scale_f32_16x16x128_f8f6f4 v[34:37], v[10:17], v[228:235], v[34:37], v246, v247 op_sel_hi:[0,0,0]
	s_setprio 0
	s_barrier
; #define PG8_STAGE(bufoff, gbase, voff) do { _Pragma("unroll") for (int _i = 0; _i < 2; ++_i) \
;         __builtin_amdgcn_global_load_lds((const unsigned*)((const char*)(gbase) + (voff)[_i]), (PG8_LAS unsigned*)(lds + (bufoff) + ldsw + _i * 8192), 16, 0, 0); } while (0)
; #define PG8_WAIT_V(n) asm volatile("s_waitcnt vmcnt(" #n ")" ::: "memory")
; #define PG8_WAIT_L(n) asm volatile("s_waitcnt lgkmcnt(" #n ")" ::: "memory")
; #define PG8_BAR __builtin_amdgcn_s_barrier()
; #define PG8_SCHED __builtin_amdgcn_sched_barrier(0)
; template <class Epi, class Sched, bool ALIGN_EPI = false, bool SP2 = false, bool F8 = false>
; __device__ __forceinline__ void gemm_phase(PG8_LAS unsigned char* lds, const Gemm g, const Sched& S, const Epi& E, const int tidb  ) {
;     ...
;             PG8_LDB(B0, 1, 0); PG8_LDB(B1, 1, 1); PG8_SCHED; PG8_LDA(At, 1, 0); PG8_STAGE(PG8_SA(0, 1), a2 + hstep, voffA);
;             PG8_WAIT_V(8); PG8_WAIT_L(0); PG8_BAR; PG8_MMA(0, 0, At, B0); PG8_MMA(0, 1, At, B1); PG8_BAR; PG8_SCHED;
;             PG8_LDA(At, 1, 1); PG8_STAGE(PG8_SB(1, 0), b3, voffB); PG8_STAGE(PG8_SB(1, 1), b3 + hstep, voffB); PG8_STAGE(PG8_SA(1, 0), a3, voffA);
;             PG8_WAIT_V(8); PG8_WAIT_L(0); PG8_BAR; PG8_MMA(1, 0, At, B0); PG8_MMA(1, 1, At, B1); PG8_BAR; PG8_SCHED;
	s_add_i32 s30, 0, 0x18000
	s_add_i32 s31, 0, 0x1c000
	v_add_u32_e32 v14, s30, v192
	v_add_u32_e32 v30, s31, v192
	ds_read_b128 v[2:5], v14
	ds_read_b128 v[6:9], v14 offset:1024
	ds_read_b128 v[10:13], v14 offset:2048
	ds_read_b128 v[14:17], v14 offset:3072
	ds_read_b128 v[18:21], v30
	ds_read_b128 v[22:25], v30 offset:1024
	ds_read_b128 v[26:29], v30 offset:2048
	ds_read_b128 v[30:33], v30 offset:3072
	s_add_u32 s28, s28, s12
	s_addc_u32 s29, s29, s13
	s_mov_b32 m0, s37
	v_lshl_add_u64 v[186:187], s[28:29], 0, v[164:165]
	ds_read_b128 v[204:207], v194 offset:32768
	ds_read_b128 v[208:211], v194 offset:33792
	ds_read_b128 v[212:215], v194 offset:34816
	ds_read_b128 v[216:219], v194 offset:35840
	ds_read_b128 v[220:223], v194 offset:36864
	ds_read_b128 v[224:227], v194 offset:37888
	ds_read_b128 v[228:231], v194 offset:38912
	ds_read_b128 v[232:235], v194 offset:39936
	global_load_lds_dwordx4 v[186:187], off
	v_lshl_add_u64 v[186:187], s[28:29], 0, v[166:167]
	s_mov_b32 m0, s41
	s_nop 0
	global_load_lds_dwordx4 v[186:187], off
	s_waitcnt vmcnt(8)
	s_waitcnt lgkmcnt(0)
	s_barrier
	s_setprio 1
	s_waitcnt lgkmcnt(0)
	v_mfma_scale_f32_16x16x128_f8f6f4 v[158:161], v[2:9], v[204:211], v[158:161], v246, v247 op_sel_hi:[0,0,0]
	v_mfma_scale_f32_16x16x128_f8f6f4 v[154:157], v[10:17], v[204:211], v[154:157], v246, v247 op_sel_hi:[0,0,0]
	v_mfma_scale_f32_16x16x128_f8f6f4 v[142:145], v[2:9], v[212:219], v[142:145], v246, v247 op_sel_hi:[0,0,0]
	v_mfma_scale_f32_16x16x128_f8f6f4 v[138:141], v[10:17], v[212:219], v[138:141], v246, v247 op_sel_hi:[0,0,0]
	v_mfma_scale_f32_16x16x128_f8f6f4 v[126:129], v[2:9], v[220:227], v[126:129], v246, v247 op_sel_hi:[0,0,0]
	v_mfma_scale_f32_16x16x128_f8f6f4 v[122:125], v[10:17], v[220:227], v[122:125], v246, v247 op_sel_hi:[0,0,0]
	v_mfma_scale_f32_16x16x128_f8f6f4 v[110:113], v[2:9], v[228:235], v[110:113], v246, v247 op_sel_hi:[0,0,0]
	v_mfma_scale_f32_16x16x128_f8f6f4 v[106:109], v[10:17], v[228:235], v[106:109], v246, v247 op_sel_hi:[0,0,0]
	s_setprio 0
	s_setprio 1
	v_mfma_scale_f32_16x16x128_f8f6f4 v[150:153], v[18:25], v[204:211], v[150:153], v246, v247 op_sel_hi:[0,0,0]
	v_mfma_scale_f32_16x16x128_f8f6f4 v[146:149], v[26:33], v[204:211], v[146:149], v246, v247 op_sel_hi:[0,0,0]
	v_mfma_scale_f32_16x16x128_f8f6f4 v[134:137], v[18:25], v[212:219], v[134:137], v246, v247 op_sel_hi:[0,0,0]
	v_mfma_scale_f32_16x16x128_f8f6f4 v[130:133], v[26:33], v[212:219], v[130:133], v246, v247 op_sel_hi:[0,0,0]
	v_mfma_scale_f32_16x16x128_f8f6f4 v[118:121], v[18:25], v[220:227], v[118:121], v246, v247 op_sel_hi:[0,0,0]
	v_mfma_scale_f32_16x16x128_f8f6f4 v[114:117], v[26:33], v[220:227], v[114:117], v246, v247 op_sel_hi:[0,0,0]
	v_mfma_scale_f32_16x16x128_f8f6f4 v[102:105], v[18:25], v[228:235], v[102:105], v246, v247 op_sel_hi:[0,0,0]
	v_mfma_scale_f32_16x16x128_f8f6f4 v[98:101], v[26:33], v[228:235], v[98:101], v246, v247 op_sel_hi:[0,0,0]
	s_setprio 0
	s_barrier
	s_add_i32 s28, s30, s0
	v_lshl_add_u64 v[174:175], v[174:175], 0, s[92:93]
	s_mov_b32 m0, s28
	ds_read_b128 v[204:207], v194 offset:49152
	ds_read_b128 v[208:211], v194 offset:50176
	ds_read_b128 v[212:215], v194 offset:51200
	ds_read_b128 v[216:219], v194 offset:52224
	ds_read_b128 v[220:223], v194 offset:53248
	ds_read_b128 v[224:227], v194 offset:54272
	ds_read_b128 v[228:231], v194 offset:55296
	ds_read_b128 v[232:235], v194 offset:56320
	global_load_lds_dwordx4 v[174:175], off
	v_lshl_add_u64 v[174:175], v[176:177], 0, s[92:93]
	s_add_i32 m0, s28, 0x2000
	s_add_i32 s28, s31, s0
	global_load_lds_dwordx4 v[174:175], off
	v_lshl_add_u64 v[174:175], v[178:179], 0, s[92:93]
	s_mov_b32 m0, s28
	s_nop 0
	global_load_lds_dwordx4 v[174:175], off
	v_lshl_add_u64 v[174:175], v[180:181], 0, s[92:93]
	s_add_i32 m0, s28, 0x2000
	s_nop 0
	global_load_lds_dwordx4 v[174:175], off
	v_lshl_add_u64 v[174:175], v[182:183], 0, s[92:93]
	s_mov_b32 m0, s43
	s_nop 0
	global_load_lds_dwordx4 v[174:175], off
	v_lshl_add_u64 v[174:175], v[184:185], 0, s[92:93]
	s_mov_b32 m0, s45
	s_nop 0
	global_load_lds_dwordx4 v[174:175], off
	s_waitcnt vmcnt(8)
	s_waitcnt lgkmcnt(0)
	s_barrier
	s_setprio 1
	s_waitcnt lgkmcnt(0)
	v_mfma_scale_f32_16x16x128_f8f6f4 v[94:97], v[2:9], v[204:211], v[94:97], v246, v247 op_sel_hi:[0,0,0]
	v_mfma_scale_f32_16x16x128_f8f6f4 v[90:93], v[10:17], v[204:211], v[90:93], v246, v247 op_sel_hi:[0,0,0]
	v_mfma_scale_f32_16x16x128_f8f6f4 v[78:81], v[2:9], v[212:219], v[78:81], v246, v247 op_sel_hi:[0,0,0]
	v_mfma_scale_f32_16x16x128_f8f6f4 v[74:77], v[10:17], v[212:219], v[74:77], v246, v247 op_sel_hi:[0,0,0]
	v_mfma_scale_f32_16x16x128_f8f6f4 v[62:65], v[2:9], v[220:227], v[62:65], v246, v247 op_sel_hi:[0,0,0]
	v_mfma_scale_f32_16x16x128_f8f6f4 v[58:61], v[10:17], v[220:227], v[58:61], v246, v247 op_sel_hi:[0,0,0]
	v_mfma_scale_f32_16x16x128_f8f6f4 v[46:49], v[2:9], v[228:235], v[46:49], v246, v247 op_sel_hi:[0,0,0]
	v_mfma_scale_f32_16x16x128_f8f6f4 v[42:45], v[10:17], v[228:235], v[42:45], v246, v247 op_sel_hi:[0,0,0]
	s_setprio 0
	s_setprio 1
	v_mfma_scale_f32_16x16x128_f8f6f4 v[86:89], v[18:25], v[204:211], v[86:89], v246, v247 op_sel_hi:[0,0,0]
	v_mfma_scale_f32_16x16x128_f8f6f4 v[82:85], v[26:33], v[204:211], v[82:85], v246, v247 op_sel_hi:[0,0,0]
	v_mfma_scale_f32_16x16x128_f8f6f4 v[70:73], v[18:25], v[212:219], v[70:73], v246, v247 op_sel_hi:[0,0,0]
	v_mfma_scale_f32_16x16x128_f8f6f4 v[66:69], v[26:33], v[212:219], v[66:69], v246, v247 op_sel_hi:[0,0,0]
	v_mfma_scale_f32_16x16x128_f8f6f4 v[54:57], v[18:25], v[220:227], v[54:57], v246, v247 op_sel_hi:[0,0,0]
	v_mfma_scale_f32_16x16x128_f8f6f4 v[50:53], v[26:33], v[220:227], v[50:53], v246, v247 op_sel_hi:[0,0,0]
	v_mfma_scale_f32_16x16x128_f8f6f4 v[38:41], v[18:25], v[228:235], v[38:41], v246, v247 op_sel_hi:[0,0,0]
	v_mfma_scale_f32_16x16x128_f8f6f4 v[34:37], v[26:33], v[228:235], v[34:37], v246, v247 op_sel_hi:[0,0,0]
	s_setprio 0
	s_add_u32 s26, s26, 0x100
	s_addc_u32 s27, s27, 0
	s_add_u32 s62, s62, 0x100
	s_addc_u32 s63, s63, 0
	s_cmp_ge_i32 s65, s46
	s_mov_b32 s28, s65
	s_barrier
	s_cbranch_scc0 .LBB0_1857
	s_movk_i32 s67, 0x300
